# no-op lgkmcnt waits inside MFMA clusters removed, s_setprio 1 issued before the interval's opening barrier, ragged-tile test moved in front of the barrier
# speedup vs baseline: 1.0006x; 1.0006x over previous
.Lz1_a:
	s_waitcnt vmcnt(8)
	s_waitcnt lgkmcnt(0)
	s_setprio 1
	s_barrier
	v_mfma_scale_f32_16x16x128_f8f6f4 v[124:127], v[146:153], v[178:185], v[124:127], v143, v143 op_sel_hi:[0,0,0]
	v_mfma_scale_f32_16x16x128_f8f6f4 v[120:123], v[154:161], v[178:185], v[120:123], v143, v143 op_sel_hi:[0,0,0]
	v_mfma_scale_f32_16x16x128_f8f6f4 v[108:111], v[146:153], v[186:193], v[108:111], v143, v143 op_sel_hi:[0,0,0]
	v_mfma_scale_f32_16x16x128_f8f6f4 v[104:107], v[154:161], v[186:193], v[104:107], v143, v143 op_sel_hi:[0,0,0]
	v_mfma_scale_f32_16x16x128_f8f6f4 v[130:133], v[146:153], v[194:201], v[92:95], v143, v143 op_sel_hi:[0,0,0]
	v_mfma_scale_f32_16x16x128_f8f6f4 v[210:213], v[154:161], v[194:201], v[88:91], v143, v143 op_sel_hi:[0,0,0]
	v_mfma_scale_f32_16x16x128_f8f6f4 v[214:217], v[146:153], v[202:209], v[76:79], v143, v143 op_sel_hi:[0,0,0]
	v_mfma_scale_f32_16x16x128_f8f6f4 v[218:221], v[154:161], v[202:209], v[72:75], v143, v143 op_sel_hi:[0,0,0]
	s_setprio 0
	s_setprio 1
	v_mfma_scale_f32_16x16x128_f8f6f4 v[116:119], v[162:169], v[178:185], v[116:119], v143, v143 op_sel_hi:[0,0,0]
	v_mfma_scale_f32_16x16x128_f8f6f4 v[112:115], v[170:177], v[178:185], v[112:115], v143, v143 op_sel_hi:[0,0,0]
	v_mfma_scale_f32_16x16x128_f8f6f4 v[100:103], v[162:169], v[186:193], v[100:103], v143, v143 op_sel_hi:[0,0,0]
	v_mfma_scale_f32_16x16x128_f8f6f4 v[96:99], v[170:177], v[186:193], v[96:99], v143, v143 op_sel_hi:[0,0,0]
	v_mfma_scale_f32_16x16x128_f8f6f4 v[178:181], v[162:169], v[194:201], v[84:87], v143, v143 op_sel_hi:[0,0,0]
	v_mfma_scale_f32_16x16x128_f8f6f4 v[182:185], v[170:177], v[194:201], v[80:83], v143, v143 op_sel_hi:[0,0,0]
	v_mfma_scale_f32_16x16x128_f8f6f4 v[186:189], v[162:169], v[202:209], v[68:71], v143, v143 op_sel_hi:[0,0,0]
	v_mfma_scale_f32_16x16x128_f8f6f4 v[190:193], v[170:177], v[202:209], v[64:67], v143, v143 op_sel_hi:[0,0,0]
	s_setprio 0
	s_barrier
	s_nop 4
	ds_read_b128 v[64:67], v142 offset:16384
	ds_read_b128 v[68:71], v142 offset:17408
	ds_read_b128 v[72:75], v142 offset:18432
	ds_read_b128 v[76:79], v142 offset:19456
	ds_read_b128 v[80:83], v142 offset:20480
	ds_read_b128 v[84:87], v142 offset:21504
	ds_read_b128 v[88:91], v142 offset:22528
	ds_read_b128 v[92:95], v142 offset:23552
	s_mov_b32 s0, m0
	s_mov_b32 m0, s19
	s_nop 2
	global_load_lds_dwordx4 v136, s[84:85]
	s_mov_b32 m0, s0
	s_nop 0
	s_mov_b32 s0, m0
	s_mov_b32 m0, s40
	s_nop 2
	global_load_lds_dwordx4 v137, s[84:85]
	s_mov_b32 m0, s0
	s_nop 0
	s_mov_b32 s0, m0
	s_mov_b32 m0, s41
	s_nop 2
	global_load_lds_dwordx4 v136, s[62:63]
	s_mov_b32 m0, s0
	s_nop 0
	s_mov_b32 s0, m0
	s_mov_b32 m0, s42
	s_nop 2
	global_load_lds_dwordx4 v137, s[62:63]
	s_mov_b32 m0, s0
	s_nop 0
	s_mov_b32 s0, m0
	s_mov_b32 m0, s97
	s_nop 2
	global_load_lds_dwordx4 v138, s[80:81]
	s_mov_b32 m0, s0
	s_nop 0
	s_mov_b32 s0, m0
	s_mov_b32 m0, s43
	s_nop 2
	global_load_lds_dwordx4 v139, s[80:81]
	s_mov_b32 m0, s0
	s_cmp_lg_u32 s9, -2
	s_cbranch_scc1 .Lz1_b
	v_mov_b32_e32 v60, 0
	v_mov_b32_e32 v61, 0
	v_pk_mov_b32 v[62:63], v[60:61], v[60:61]
	v_pk_mov_b32 v[56:57], v[60:61], v[60:61]
	v_pk_mov_b32 v[58:59], v[60:61], v[60:61]
	v_pk_mov_b32 v[44:45], v[60:61], v[60:61]
	v_pk_mov_b32 v[46:47], v[60:61], v[60:61]
	v_pk_mov_b32 v[40:41], v[60:61], v[60:61]
	v_pk_mov_b32 v[42:43], v[60:61], v[60:61]
	v_pk_mov_b32 v[28:29], v[60:61], v[60:61]
	v_pk_mov_b32 v[30:31], v[60:61], v[60:61]
	v_pk_mov_b32 v[24:25], v[60:61], v[60:61]
	v_pk_mov_b32 v[26:27], v[60:61], v[60:61]
	v_pk_mov_b32 v[12:13], v[60:61], v[60:61]
	v_pk_mov_b32 v[14:15], v[60:61], v[60:61]
	v_pk_mov_b32 v[0:1], v[60:61], v[60:61]
	v_pk_mov_b32 v[2:3], v[60:61], v[60:61]
	v_pk_mov_b32 v[52:53], v[60:61], v[60:61]
	v_pk_mov_b32 v[54:55], v[60:61], v[60:61]
	v_pk_mov_b32 v[48:49], v[60:61], v[60:61]
	v_pk_mov_b32 v[50:51], v[60:61], v[60:61]
	v_pk_mov_b32 v[36:37], v[60:61], v[60:61]
	v_pk_mov_b32 v[38:39], v[60:61], v[60:61]
	v_pk_mov_b32 v[32:33], v[60:61], v[60:61]
	v_pk_mov_b32 v[34:35], v[60:61], v[60:61]
	v_pk_mov_b32 v[20:21], v[60:61], v[60:61]
	v_pk_mov_b32 v[22:23], v[60:61], v[60:61]
	v_pk_mov_b32 v[16:17], v[60:61], v[60:61]
	v_pk_mov_b32 v[18:19], v[60:61], v[60:61]
	v_pk_mov_b32 v[8:9], v[60:61], v[60:61]
	v_pk_mov_b32 v[10:11], v[60:61], v[60:61]
	v_pk_mov_b32 v[4:5], v[60:61], v[60:61]
	v_pk_mov_b32 v[6:7], v[60:61], v[60:61]
.Lz1_b:
	s_waitcnt vmcnt(8)
	s_waitcnt lgkmcnt(0)
	s_setprio 1
	s_barrier
	v_mfma_scale_f32_16x16x128_f8f6f4 v[60:63], v[146:153], v[64:71], v[60:63], v143, v143 op_sel_hi:[0,0,0]
	v_mfma_scale_f32_16x16x128_f8f6f4 v[56:59], v[154:161], v[64:71], v[56:59], v143, v143 op_sel_hi:[0,0,0]
	v_mfma_scale_f32_16x16x128_f8f6f4 v[194:197], v[146:153], v[72:79], v[44:47], v143, v143 op_sel_hi:[0,0,0]
	v_mfma_scale_f32_16x16x128_f8f6f4 v[198:201], v[154:161], v[72:79], v[40:43], v143, v143 op_sel_hi:[0,0,0]
	v_mfma_scale_f32_16x16x128_f8f6f4 v[202:205], v[146:153], v[80:87], v[28:31], v143, v143 op_sel_hi:[0,0,0]
	v_mfma_scale_f32_16x16x128_f8f6f4 v[206:209], v[154:161], v[80:87], v[24:27], v143, v143 op_sel_hi:[0,0,0]
	v_mfma_scale_f32_16x16x128_f8f6f4 v[222:225], v[146:153], v[88:95], v[12:15], v143, v143 op_sel_hi:[0,0,0]
	v_mfma_scale_f32_16x16x128_f8f6f4 v[226:229], v[154:161], v[88:95], v[0:3], v143, v143 op_sel_hi:[0,0,0]
	s_setprio 0
	s_setprio 1
	v_mfma_scale_f32_16x16x128_f8f6f4 v[52:55], v[162:169], v[64:71], v[52:55], v143, v143 op_sel_hi:[0,0,0]
	v_mfma_scale_f32_16x16x128_f8f6f4 v[48:51], v[170:177], v[64:71], v[48:51], v143, v143 op_sel_hi:[0,0,0]
	v_mfma_scale_f32_16x16x128_f8f6f4 v[230:233], v[162:169], v[72:79], v[36:39], v143, v143 op_sel_hi:[0,0,0]
	v_mfma_scale_f32_16x16x128_f8f6f4 v[234:237], v[170:177], v[72:79], v[32:35], v143, v143 op_sel_hi:[0,0,0]
	v_mfma_scale_f32_16x16x128_f8f6f4 v[238:241], v[162:169], v[80:87], v[20:23], v143, v143 op_sel_hi:[0,0,0]
	v_mfma_scale_f32_16x16x128_f8f6f4 v[242:245], v[170:177], v[80:87], v[16:19], v143, v143 op_sel_hi:[0,0,0]
	v_mfma_scale_f32_16x16x128_f8f6f4 v[246:249], v[162:169], v[88:95], v[8:11], v143, v143 op_sel_hi:[0,0,0]
	v_mfma_scale_f32_16x16x128_f8f6f4 v[250:253], v[170:177], v[88:95], v[4:7], v143, v143 op_sel_hi:[0,0,0]
	s_setprio 0
	s_barrier
	ds_read_b128 v[0:3], v144
	s_nop 3
	ds_read_b128 v[4:7], v144 offset:1024
	ds_read_b128 v[16:19], v144 offset:2048
	ds_read_b128 v[20:23], v144 offset:3072
	ds_read_b128 v[146:149], v145
	ds_read_b128 v[150:153], v145 offset:1024
	ds_read_b128 v[154:157], v145 offset:2048
	ds_read_b128 v[158:161], v145 offset:3072
	ds_read_b128 v[8:11], v142 offset:32768
	ds_read_b128 v[12:15], v142 offset:33792
	ds_read_b128 v[24:27], v142 offset:34816
	ds_read_b128 v[28:31], v142 offset:35840
	ds_read_b128 v[32:35], v142 offset:36864
	ds_read_b128 v[36:39], v142 offset:37888
	ds_read_b128 v[40:43], v142 offset:38912
	ds_read_b128 v[44:47], v142 offset:39936
	s_add_u32 s34, s80, 0x40000
	s_addc_u32 s35, s81, 0
	s_mov_b32 s0, m0
	s_mov_b32 m0, s44
	s_nop 2
	global_load_lds_dwordx4 v138, s[34:35]
	s_mov_b32 m0, s0
	s_nop 0
	s_mov_b32 s0, m0
	s_mov_b32 m0, s45
	s_nop 2
	global_load_lds_dwordx4 v139, s[34:35]
	s_mov_b32 m0, s0
	s_waitcnt vmcnt(8)
	s_waitcnt lgkmcnt(0)
	s_setprio 1
	s_barrier
	v_mfma_scale_f32_16x16x128_f8f6f4 v[124:127], v[0:7], v[8:15], v[124:127], v143, v143 op_sel_hi:[0,0,0]
	v_mfma_scale_f32_16x16x128_f8f6f4 v[120:123], v[16:23], v[8:15], v[120:123], v143, v143 op_sel_hi:[0,0,0]
	v_mfma_scale_f32_16x16x128_f8f6f4 v[108:111], v[0:7], v[24:31], v[108:111], v143, v143 op_sel_hi:[0,0,0]
	v_mfma_scale_f32_16x16x128_f8f6f4 v[104:107], v[16:23], v[24:31], v[104:107], v143, v143 op_sel_hi:[0,0,0]
	v_mfma_scale_f32_16x16x128_f8f6f4 v[92:95], v[0:7], v[32:39], v[130:133], v143, v143 op_sel_hi:[0,0,0]
	v_mfma_scale_f32_16x16x128_f8f6f4 v[88:91], v[16:23], v[32:39], v[210:213], v143, v143 op_sel_hi:[0,0,0]
	v_mfma_scale_f32_16x16x128_f8f6f4 v[76:79], v[0:7], v[40:47], v[214:217], v143, v143 op_sel_hi:[0,0,0]
	v_mfma_scale_f32_16x16x128_f8f6f4 v[72:75], v[16:23], v[40:47], v[218:221], v143, v143 op_sel_hi:[0,0,0]
	s_setprio 0
	s_setprio 1
	v_mfma_scale_f32_16x16x128_f8f6f4 v[116:119], v[146:153], v[8:15], v[116:119], v143, v143 op_sel_hi:[0,0,0]
	v_mfma_scale_f32_16x16x128_f8f6f4 v[112:115], v[154:161], v[8:15], v[112:115], v143, v143 op_sel_hi:[0,0,0]
	v_mfma_scale_f32_16x16x128_f8f6f4 v[100:103], v[146:153], v[24:31], v[100:103], v143, v143 op_sel_hi:[0,0,0]
	v_mfma_scale_f32_16x16x128_f8f6f4 v[96:99], v[154:161], v[24:31], v[96:99], v143, v143 op_sel_hi:[0,0,0]
	v_mfma_scale_f32_16x16x128_f8f6f4 v[84:87], v[146:153], v[32:39], v[178:181], v143, v143 op_sel_hi:[0,0,0]
	v_mfma_scale_f32_16x16x128_f8f6f4 v[80:83], v[154:161], v[32:39], v[182:185], v143, v143 op_sel_hi:[0,0,0]
	v_mfma_scale_f32_16x16x128_f8f6f4 v[68:71], v[146:153], v[40:47], v[186:189], v143, v143 op_sel_hi:[0,0,0]
	v_mfma_scale_f32_16x16x128_f8f6f4 v[64:67], v[154:161], v[40:47], v[190:193], v143, v143 op_sel_hi:[0,0,0]
	s_setprio 0
	s_barrier
	ds_read_b128 v[32:35], v142 offset:49152
	ds_read_b128 v[36:39], v142 offset:50176
	ds_read_b128 v[162:165], v142 offset:51200
	ds_read_b128 v[166:169], v142 offset:52224
	ds_read_b128 v[170:173], v142 offset:53248
	ds_read_b128 v[174:177], v142 offset:54272
	ds_read_b128 v[178:181], v142 offset:55296
	ds_read_b128 v[182:185], v142 offset:56320
	s_mov_b32 s0, m0
	s_mov_b32 m0, s46
	s_nop 2
	global_load_lds_dwordx4 v136, s[78:79]
	s_mov_b32 m0, s0
	s_add_u32 s34, s62, 0x80
	s_mov_b32 s0, m0
	s_mov_b32 m0, s48
	s_nop 2
	global_load_lds_dwordx4 v137, s[78:79]
	s_mov_b32 m0, s0
	s_addc_u32 s35, s63, 0
	s_mov_b32 s0, m0
	s_mov_b32 m0, s51
	s_nop 2
	global_load_lds_dwordx4 v136, s[34:35]
	s_mov_b32 m0, s0
	s_nop 0
	s_mov_b32 s0, m0
	s_mov_b32 m0, s52
	s_nop 2
	global_load_lds_dwordx4 v137, s[34:35]
	s_mov_b32 m0, s0
	s_nop 0
	s_mov_b32 s0, m0
	s_mov_b32 m0, s49
	s_nop 2
	global_load_lds_dwordx4 v138, s[76:77]
	s_mov_b32 m0, s0
	s_nop 0
	s_mov_b32 s0, m0
	s_mov_b32 m0, s50
	s_nop 2
	global_load_lds_dwordx4 v139, s[76:77]
	s_mov_b32 m0, s0
	s_waitcnt vmcnt(8)
	s_waitcnt lgkmcnt(0)
	s_setprio 1
	s_barrier
	v_mfma_scale_f32_16x16x128_f8f6f4 v[60:63], v[0:7], v[32:39], v[60:63], v143, v143 op_sel_hi:[0,0,0]
	v_mfma_scale_f32_16x16x128_f8f6f4 v[56:59], v[16:23], v[32:39], v[56:59], v143, v143 op_sel_hi:[0,0,0]
	v_mfma_scale_f32_16x16x128_f8f6f4 v[44:47], v[0:7], v[162:169], v[194:197], v143, v143 op_sel_hi:[0,0,0]
	v_mfma_scale_f32_16x16x128_f8f6f4 v[40:43], v[16:23], v[162:169], v[198:201], v143, v143 op_sel_hi:[0,0,0]
	v_mfma_scale_f32_16x16x128_f8f6f4 v[28:31], v[0:7], v[170:177], v[202:205], v143, v143 op_sel_hi:[0,0,0]
	v_mfma_scale_f32_16x16x128_f8f6f4 v[24:27], v[16:23], v[170:177], v[206:209], v143, v143 op_sel_hi:[0,0,0]
	v_mfma_scale_f32_16x16x128_f8f6f4 v[12:15], v[0:7], v[178:185], v[222:225], v143, v143 op_sel_hi:[0,0,0]
	v_mfma_scale_f32_16x16x128_f8f6f4 v[0:3], v[16:23], v[178:185], v[226:229], v143, v143 op_sel_hi:[0,0,0]
	s_setprio 0
	s_setprio 1
	v_mfma_scale_f32_16x16x128_f8f6f4 v[52:55], v[146:153], v[32:39], v[52:55], v143, v143 op_sel_hi:[0,0,0]
	v_mfma_scale_f32_16x16x128_f8f6f4 v[48:51], v[154:161], v[32:39], v[48:51], v143, v143 op_sel_hi:[0,0,0]
	v_mfma_scale_f32_16x16x128_f8f6f4 v[36:39], v[146:153], v[162:169], v[230:233], v143, v143 op_sel_hi:[0,0,0]
	v_mfma_scale_f32_16x16x128_f8f6f4 v[32:35], v[154:161], v[162:169], v[234:237], v143, v143 op_sel_hi:[0,0,0]
	v_mfma_scale_f32_16x16x128_f8f6f4 v[20:23], v[146:153], v[170:177], v[238:241], v143, v143 op_sel_hi:[0,0,0]
	v_mfma_scale_f32_16x16x128_f8f6f4 v[16:19], v[154:161], v[170:177], v[242:245], v143, v143 op_sel_hi:[0,0,0]
	v_mfma_scale_f32_16x16x128_f8f6f4 v[8:11], v[146:153], v[178:185], v[246:249], v143, v143 op_sel_hi:[0,0,0]
	v_mfma_scale_f32_16x16x128_f8f6f4 v[4:7], v[154:161], v[178:185], v[250:253], v143, v143 op_sel_hi:[0,0,0]
	s_setprio 0
	s_barrier
	s_add_i32 s9, s9, 2
	s_add_u32 s8, s8, 0x100
	s_addc_u32 s6, s6, 0
	s_add_u32 s7, s7, 0x100
	s_addc_u32 s33, s33, 0
	s_cmp_gt_u32 s9, 13
	s_mov_b64 s[34:35], s[36:37]
	s_cbranch_scc0 .LBB0_198
	s_and_b64 vcc, exec, s[16:17]
	s_cbranch_vccz .LBB0_201
	s_barrier

.LBB0_290:
	ds_read_b128 v[0:3], v134
	ds_read_b128 v[4:7], v134 offset:1024
	ds_read_b128 v[8:11], v134 offset:2048
	ds_read_b128 v[12:15], v134 offset:3072
	ds_read_b128 v[16:19], v135
	ds_read_b128 v[20:23], v135 offset:1024
	ds_read_b128 v[24:27], v135 offset:2048
	ds_read_b128 v[28:31], v135 offset:3072
	s_and_b64 s[34:35], s[26:27], exec
	s_cselect_b32 s37, s19, s29
	s_cselect_b32 s36, s18, s28
	s_cselect_b32 s63, s21, s57
	s_cselect_b32 s62, s20, s56
	s_cselect_b32 s35, s23, s31
	s_cselect_b32 s34, s22, s30
	s_add_u32 s78, s28, 0x100
	s_addc_u32 s79, s29, 0
	s_add_u32 s84, s56, 0x100
	s_addc_u32 s85, s57, 0
	s_add_u32 s80, s30, 0x100
	s_addc_u32 s81, s31, 0
	s_add_u32 s76, s56, 0x180
	s_addc_u32 s77, s57, 0
	s_add_u32 s56, s28, 0x180
	s_addc_u32 s57, s29, 0
	ds_read_b128 v[32:35], v136
	ds_read_b128 v[36:39], v136 offset:1024
	ds_read_b128 v[40:43], v136 offset:2048
	ds_read_b128 v[44:47], v136 offset:3072
	ds_read_b128 v[48:51], v136 offset:4096
	ds_read_b128 v[52:55], v136 offset:5120
	ds_read_b128 v[56:59], v136 offset:6144
	ds_read_b128 v[60:63], v136 offset:7168
	s_add_u32 s86, s28, 0x40080
	s_addc_u32 s87, s29, 0
	s_mov_b32 s7, m0
	s_mov_b32 m0, s54
	s_nop 2
	global_load_lds_dwordx4 v132, s[86:87]
	s_mov_b32 m0, s7
	s_nop 0
	s_mov_b32 s7, m0
	s_mov_b32 m0, s55
	s_nop 2
	global_load_lds_dwordx4 v133, s[86:87]
	s_mov_b32 m0, s7
	s_waitcnt vmcnt(8)
	s_waitcnt lgkmcnt(0)
	s_setprio 1
	s_barrier
	v_mfma_f32_16x16x32_bf16 v[64:67], v[0:3], v[32:35], 0
	v_mfma_f32_16x16x32_bf16 v[68:71], v[8:11], v[32:35], 0
	v_mfma_f32_16x16x32_bf16 v[72:75], v[0:3], v[40:43], 0
	v_mfma_f32_16x16x32_bf16 v[76:79], v[8:11], v[40:43], 0
	v_mfma_f32_16x16x32_bf16 v[80:83], v[0:3], v[48:51], 0
	v_mfma_f32_16x16x32_bf16 v[84:87], v[8:11], v[48:51], 0
	v_mfma_f32_16x16x32_bf16 v[88:91], v[0:3], v[56:59], 0
	v_mfma_f32_16x16x32_bf16 v[92:95], v[8:11], v[56:59], 0
	v_mfma_f32_16x16x32_bf16 v[64:67], v[4:7], v[36:39], v[64:67]
	v_mfma_f32_16x16x32_bf16 v[68:71], v[12:15], v[36:39], v[68:71]
	v_mfma_f32_16x16x32_bf16 v[72:75], v[4:7], v[44:47], v[72:75]
	v_mfma_f32_16x16x32_bf16 v[76:79], v[12:15], v[44:47], v[76:79]
	v_mfma_f32_16x16x32_bf16 v[80:83], v[4:7], v[52:55], v[80:83]
	v_mfma_f32_16x16x32_bf16 v[84:87], v[12:15], v[52:55], v[84:87]
	v_mfma_f32_16x16x32_bf16 v[88:91], v[4:7], v[60:63], v[88:91]
	v_mfma_f32_16x16x32_bf16 v[92:95], v[12:15], v[60:63], v[92:95]
	s_setprio 0
	s_setprio 1
	v_mfma_f32_16x16x32_bf16 v[96:99], v[16:19], v[32:35], 0
	v_mfma_f32_16x16x32_bf16 v[32:35], v[24:27], v[32:35], 0
	v_mfma_f32_16x16x32_bf16 v[96:99], v[20:23], v[36:39], v[96:99]
	v_mfma_f32_16x16x32_bf16 v[32:35], v[28:31], v[36:39], v[32:35]
	v_mfma_f32_16x16x32_bf16 v[36:39], v[16:19], v[40:43], 0
	v_mfma_f32_16x16x32_bf16 v[40:43], v[24:27], v[40:43], 0
	v_mfma_f32_16x16x32_bf16 v[36:39], v[20:23], v[44:47], v[36:39]
	v_mfma_f32_16x16x32_bf16 v[40:43], v[28:31], v[44:47], v[40:43]
	v_mfma_f32_16x16x32_bf16 v[44:47], v[16:19], v[48:51], 0
	v_mfma_f32_16x16x32_bf16 v[48:51], v[24:27], v[48:51], 0
	v_mfma_f32_16x16x32_bf16 v[44:47], v[20:23], v[52:55], v[44:47]
	v_mfma_f32_16x16x32_bf16 v[48:51], v[28:31], v[52:55], v[48:51]
	v_mfma_f32_16x16x32_bf16 v[52:55], v[16:19], v[56:59], 0
	v_mfma_f32_16x16x32_bf16 v[56:59], v[24:27], v[56:59], 0
	v_mfma_f32_16x16x32_bf16 v[52:55], v[20:23], v[60:63], v[52:55]
	v_mfma_f32_16x16x32_bf16 v[56:59], v[28:31], v[60:63], v[56:59]
	s_setprio 0
	s_barrier
	ds_read_b128 v[60:63], v136 offset:16384
	ds_read_b128 v[100:103], v136 offset:17408
	ds_read_b128 v[104:107], v136 offset:18432
	ds_read_b128 v[108:111], v136 offset:19456
	ds_read_b128 v[112:115], v136 offset:20480
	ds_read_b128 v[116:119], v136 offset:21504
	ds_read_b128 v[120:123], v136 offset:22528
	ds_read_b128 v[124:127], v136 offset:23552
	s_mov_b32 s7, m0
	s_mov_b32 m0, s40
	s_nop 2
	global_load_lds_dwordx4 v130, s[84:85]
	s_mov_b32 m0, s7
	s_nop 0
	s_mov_b32 s7, m0
	s_mov_b32 m0, s41
	s_nop 2
	global_load_lds_dwordx4 v131, s[84:85]
	s_mov_b32 m0, s7
	s_nop 0
	s_mov_b32 s7, m0
	s_mov_b32 m0, s42
	s_nop 2
	global_load_lds_dwordx4 v130, s[80:81]
	s_mov_b32 m0, s7
	s_nop 0
	s_mov_b32 s7, m0
	s_mov_b32 m0, s43
	s_nop 2
	global_load_lds_dwordx4 v131, s[80:81]
	s_mov_b32 m0, s7
	s_nop 0
	s_mov_b32 s7, m0
	s_mov_b32 m0, s97
	s_nop 2
	global_load_lds_dwordx4 v132, s[78:79]
	s_mov_b32 m0, s7
	s_nop 0
	s_mov_b32 s7, m0
	s_mov_b32 m0, s44
	s_nop 2
	global_load_lds_dwordx4 v133, s[78:79]
	s_mov_b32 m0, s7
	s_waitcnt vmcnt(8)
	s_waitcnt lgkmcnt(0)
	s_setprio 1
	s_barrier
	v_mfma_f32_16x16x32_bf16 v[140:143], v[0:3], v[60:63], 0
	v_mfma_f32_16x16x32_bf16 v[148:151], v[0:3], v[104:107], 0
	v_mfma_f32_16x16x32_bf16 v[156:159], v[0:3], v[112:115], 0
	v_mfma_f32_16x16x32_bf16 v[0:3], v[0:3], v[120:123], 0
	v_mfma_f32_16x16x32_bf16 v[140:143], v[4:7], v[100:103], v[140:143]
	v_mfma_f32_16x16x32_bf16 v[148:151], v[4:7], v[108:111], v[148:151]
	v_mfma_f32_16x16x32_bf16 v[156:159], v[4:7], v[116:119], v[156:159]
	v_mfma_f32_16x16x32_bf16 v[0:3], v[4:7], v[124:127], v[0:3]
	v_mfma_f32_16x16x32_bf16 v[4:7], v[8:11], v[120:123], 0
	v_mfma_f32_16x16x32_bf16 v[144:147], v[8:11], v[60:63], 0
	v_mfma_f32_16x16x32_bf16 v[152:155], v[8:11], v[104:107], 0
	v_mfma_f32_16x16x32_bf16 v[160:163], v[8:11], v[112:115], 0
	v_mfma_f32_16x16x32_bf16 v[4:7], v[12:15], v[124:127], v[4:7]
	v_mfma_f32_16x16x32_bf16 v[144:147], v[12:15], v[100:103], v[144:147]
	v_mfma_f32_16x16x32_bf16 v[152:155], v[12:15], v[108:111], v[152:155]
	v_mfma_f32_16x16x32_bf16 v[160:163], v[12:15], v[116:119], v[160:163]
	s_setprio 0
	s_setprio 1
	v_mfma_f32_16x16x32_bf16 v[8:11], v[16:19], v[60:63], 0
	v_mfma_f32_16x16x32_bf16 v[12:15], v[24:27], v[60:63], 0
	v_mfma_f32_16x16x32_bf16 v[8:11], v[20:23], v[100:103], v[8:11]
	v_mfma_f32_16x16x32_bf16 v[12:15], v[28:31], v[100:103], v[12:15]
	v_mfma_f32_16x16x32_bf16 v[60:63], v[16:19], v[104:107], 0
	v_mfma_f32_16x16x32_bf16 v[100:103], v[24:27], v[104:107], 0
	v_mfma_f32_16x16x32_bf16 v[104:107], v[16:19], v[112:115], 0
	v_mfma_f32_16x16x32_bf16 v[16:19], v[16:19], v[120:123], 0
	v_mfma_f32_16x16x32_bf16 v[60:63], v[20:23], v[108:111], v[60:63]
	v_mfma_f32_16x16x32_bf16 v[100:103], v[28:31], v[108:111], v[100:103]
	v_mfma_f32_16x16x32_bf16 v[104:107], v[20:23], v[116:119], v[104:107]
	v_mfma_f32_16x16x32_bf16 v[108:111], v[24:27], v[112:115], 0
	v_mfma_f32_16x16x32_bf16 v[16:19], v[20:23], v[124:127], v[16:19]
	v_mfma_f32_16x16x32_bf16 v[20:23], v[24:27], v[120:123], 0
	v_mfma_f32_16x16x32_bf16 v[108:111], v[28:31], v[116:119], v[108:111]
	v_mfma_f32_16x16x32_bf16 v[20:23], v[28:31], v[124:127], v[20:23]
	s_setprio 0
	s_barrier
	ds_read_b128 v[24:27], v137
	ds_read_b128 v[28:31], v137 offset:1024
	ds_read_b128 v[112:115], v137 offset:2048
	ds_read_b128 v[116:119], v137 offset:3072
	ds_read_b128 v[120:123], v138
	ds_read_b128 v[124:127], v138 offset:1024
	ds_read_b128 v[164:167], v138 offset:2048
	ds_read_b128 v[168:171], v138 offset:3072
	ds_read_b128 v[172:175], v136 offset:32768
	ds_read_b128 v[176:179], v136 offset:33792
	ds_read_b128 v[180:183], v136 offset:34816
	ds_read_b128 v[184:187], v136 offset:35840
	ds_read_b128 v[188:191], v136 offset:36864
	ds_read_b128 v[192:195], v136 offset:37888
	ds_read_b128 v[196:199], v136 offset:38912
	ds_read_b128 v[200:203], v136 offset:39936
	s_add_u32 s78, s28, 0x40100
	s_addc_u32 s79, s29, 0
	s_mov_b32 s7, m0
	s_mov_b32 m0, s45
	s_nop 2
	global_load_lds_dwordx4 v132, s[78:79]
	s_mov_b32 m0, s7
	s_nop 0
	s_mov_b32 s7, m0
	s_mov_b32 m0, s46
	s_nop 2
	global_load_lds_dwordx4 v133, s[78:79]
	s_mov_b32 m0, s7
	s_waitcnt vmcnt(8)
	s_waitcnt lgkmcnt(0)
	s_setprio 1
	s_barrier
	v_mfma_f32_16x16x32_bf16 v[64:67], v[24:27], v[172:175], v[64:67]
	v_mfma_f32_16x16x32_bf16 v[68:71], v[112:115], v[172:175], v[68:71]
	v_mfma_f32_16x16x32_bf16 v[72:75], v[24:27], v[180:183], v[72:75]
	v_mfma_f32_16x16x32_bf16 v[76:79], v[112:115], v[180:183], v[76:79]
	v_mfma_f32_16x16x32_bf16 v[80:83], v[24:27], v[188:191], v[80:83]
	v_mfma_f32_16x16x32_bf16 v[84:87], v[112:115], v[188:191], v[84:87]
	v_mfma_f32_16x16x32_bf16 v[88:91], v[24:27], v[196:199], v[88:91]
	v_mfma_f32_16x16x32_bf16 v[92:95], v[112:115], v[196:199], v[92:95]
	v_mfma_f32_16x16x32_bf16 v[64:67], v[28:31], v[176:179], v[64:67]
	v_mfma_f32_16x16x32_bf16 v[68:71], v[116:119], v[176:179], v[68:71]
	v_mfma_f32_16x16x32_bf16 v[72:75], v[28:31], v[184:187], v[72:75]
	v_mfma_f32_16x16x32_bf16 v[76:79], v[116:119], v[184:187], v[76:79]
	v_mfma_f32_16x16x32_bf16 v[80:83], v[28:31], v[192:195], v[80:83]
	v_mfma_f32_16x16x32_bf16 v[84:87], v[116:119], v[192:195], v[84:87]
	v_mfma_f32_16x16x32_bf16 v[88:91], v[28:31], v[200:203], v[88:91]
	v_mfma_f32_16x16x32_bf16 v[92:95], v[116:119], v[200:203], v[92:95]
	s_setprio 0
	s_setprio 1
	v_mfma_f32_16x16x32_bf16 v[96:99], v[120:123], v[172:175], v[96:99]
	v_mfma_f32_16x16x32_bf16 v[32:35], v[164:167], v[172:175], v[32:35]
	v_mfma_f32_16x16x32_bf16 v[36:39], v[120:123], v[180:183], v[36:39]
	v_mfma_f32_16x16x32_bf16 v[40:43], v[164:167], v[180:183], v[40:43]
	v_mfma_f32_16x16x32_bf16 v[44:47], v[120:123], v[188:191], v[44:47]
	v_mfma_f32_16x16x32_bf16 v[48:51], v[164:167], v[188:191], v[48:51]
	v_mfma_f32_16x16x32_bf16 v[52:55], v[120:123], v[196:199], v[52:55]
	v_mfma_f32_16x16x32_bf16 v[56:59], v[164:167], v[196:199], v[56:59]
	v_mfma_f32_16x16x32_bf16 v[96:99], v[124:127], v[176:179], v[96:99]
	v_mfma_f32_16x16x32_bf16 v[32:35], v[168:171], v[176:179], v[32:35]
	v_mfma_f32_16x16x32_bf16 v[36:39], v[124:127], v[184:187], v[36:39]
	v_mfma_f32_16x16x32_bf16 v[40:43], v[168:171], v[184:187], v[40:43]
	v_mfma_f32_16x16x32_bf16 v[44:47], v[124:127], v[192:195], v[44:47]
	v_mfma_f32_16x16x32_bf16 v[48:51], v[168:171], v[192:195], v[48:51]
	v_mfma_f32_16x16x32_bf16 v[52:55], v[124:127], v[200:203], v[52:55]
	v_mfma_f32_16x16x32_bf16 v[56:59], v[168:171], v[200:203], v[56:59]
	s_setprio 0
	s_barrier
	ds_read_b128 v[172:175], v136 offset:49152
	ds_read_b128 v[176:179], v136 offset:50176
	ds_read_b128 v[180:183], v136 offset:51200
	ds_read_b128 v[184:187], v136 offset:52224
	ds_read_b128 v[188:191], v136 offset:53248
	ds_read_b128 v[192:195], v136 offset:54272
	ds_read_b128 v[196:199], v136 offset:55296
	ds_read_b128 v[200:203], v136 offset:56320
	s_mov_b32 s7, m0
	s_mov_b32 m0, s48
	s_nop 2
	global_load_lds_dwordx4 v130, s[76:77]
	s_mov_b32 m0, s7
	s_add_u32 s30, s30, 0x180
	s_mov_b32 s7, m0
	s_mov_b32 m0, s49
	s_nop 2
	global_load_lds_dwordx4 v131, s[76:77]
	s_mov_b32 m0, s7
	s_addc_u32 s31, s31, 0
	s_mov_b32 s7, m0
	s_mov_b32 m0, s52
	s_nop 2
	global_load_lds_dwordx4 v130, s[30:31]
	s_mov_b32 m0, s7
	s_nop 0
	s_mov_b32 s7, m0
	s_mov_b32 m0, s53
	s_nop 2
	global_load_lds_dwordx4 v131, s[30:31]
	s_mov_b32 m0, s7
	s_nop 0
	s_mov_b32 s7, m0
	s_mov_b32 m0, s50
	s_nop 2
	global_load_lds_dwordx4 v132, s[56:57]
	s_mov_b32 m0, s7
	s_nop 0
	s_mov_b32 s7, m0
	s_mov_b32 m0, s51
	s_nop 2
	global_load_lds_dwordx4 v133, s[56:57]
	s_mov_b32 m0, s7
	s_waitcnt vmcnt(8)
	s_waitcnt lgkmcnt(0)
	s_setprio 1
	s_barrier
	v_mfma_f32_16x16x32_bf16 v[0:3], v[24:27], v[196:199], v[0:3]
	v_mfma_f32_16x16x32_bf16 v[4:7], v[112:115], v[196:199], v[4:7]
	v_mfma_f32_16x16x32_bf16 v[140:143], v[24:27], v[172:175], v[140:143]
	v_mfma_f32_16x16x32_bf16 v[144:147], v[112:115], v[172:175], v[144:147]
	v_mfma_f32_16x16x32_bf16 v[148:151], v[24:27], v[180:183], v[148:151]
	v_mfma_f32_16x16x32_bf16 v[152:155], v[112:115], v[180:183], v[152:155]
	v_mfma_f32_16x16x32_bf16 v[156:159], v[24:27], v[188:191], v[156:159]
	v_mfma_f32_16x16x32_bf16 v[160:163], v[112:115], v[188:191], v[160:163]
	v_mfma_f32_16x16x32_bf16 v[0:3], v[28:31], v[200:203], v[0:3]
	v_mfma_f32_16x16x32_bf16 v[4:7], v[116:119], v[200:203], v[4:7]
	v_mfma_f32_16x16x32_bf16 v[140:143], v[28:31], v[176:179], v[140:143]
	v_mfma_f32_16x16x32_bf16 v[144:147], v[116:119], v[176:179], v[144:147]
	v_mfma_f32_16x16x32_bf16 v[148:151], v[28:31], v[184:187], v[148:151]
	v_mfma_f32_16x16x32_bf16 v[152:155], v[116:119], v[184:187], v[152:155]
	v_mfma_f32_16x16x32_bf16 v[156:159], v[28:31], v[192:195], v[156:159]
	v_mfma_f32_16x16x32_bf16 v[160:163], v[116:119], v[192:195], v[160:163]
	s_setprio 0
	s_setprio 1
	v_mfma_f32_16x16x32_bf16 v[8:11], v[120:123], v[172:175], v[8:11]
	v_mfma_f32_16x16x32_bf16 v[12:15], v[164:167], v[172:175], v[12:15]
	v_mfma_f32_16x16x32_bf16 v[24:27], v[120:123], v[180:183], v[60:63]
	v_mfma_f32_16x16x32_bf16 v[28:31], v[164:167], v[180:183], v[100:103]
	v_mfma_f32_16x16x32_bf16 v[60:63], v[120:123], v[188:191], v[104:107]
	v_mfma_f32_16x16x32_bf16 v[100:103], v[164:167], v[188:191], v[108:111]
	v_mfma_f32_16x16x32_bf16 v[16:19], v[120:123], v[196:199], v[16:19]
	v_mfma_f32_16x16x32_bf16 v[20:23], v[164:167], v[196:199], v[20:23]
	v_mfma_f32_16x16x32_bf16 v[8:11], v[124:127], v[176:179], v[8:11]
	v_mfma_f32_16x16x32_bf16 v[12:15], v[168:171], v[176:179], v[12:15]
	v_mfma_f32_16x16x32_bf16 v[24:27], v[124:127], v[184:187], v[24:27]
	v_mfma_f32_16x16x32_bf16 v[28:31], v[168:171], v[184:187], v[28:31]
	v_mfma_f32_16x16x32_bf16 v[60:63], v[124:127], v[192:195], v[60:63]
	v_mfma_f32_16x16x32_bf16 v[100:103], v[168:171], v[192:195], v[100:103]
	v_mfma_f32_16x16x32_bf16 v[16:19], v[124:127], v[200:203], v[16:19]
	v_mfma_f32_16x16x32_bf16 v[20:23], v[168:171], v[200:203], v[20:23]
	s_setprio 0
	s_barrier
	ds_read_b128 v[104:107], v134
	ds_read_b128 v[108:111], v134 offset:1024
	ds_read_b128 v[112:115], v134 offset:2048
	ds_read_b128 v[116:119], v134 offset:3072
	ds_read_b128 v[120:123], v135
	ds_read_b128 v[124:127], v135 offset:1024
	ds_read_b128 v[164:167], v135 offset:2048
	ds_read_b128 v[168:171], v135 offset:3072
	s_add_u32 s56, s62, 0x80
	s_addc_u32 s57, s63, 0
	s_add_u32 s30, s36, 0x80
	s_addc_u32 s31, s37, 0
	ds_read_b128 v[172:175], v136
	ds_read_b128 v[176:179], v136 offset:1024
	ds_read_b128 v[180:183], v136 offset:2048
	ds_read_b128 v[184:187], v136 offset:3072
	ds_read_b128 v[188:191], v136 offset:4096
	ds_read_b128 v[192:195], v136 offset:5120
	ds_read_b128 v[196:199], v136 offset:6144
	ds_read_b128 v[200:203], v136 offset:7168
	s_add_u32 s28, s28, 0x40180
	s_addc_u32 s29, s29, 0
	s_mov_b32 s7, m0
	s_mov_b32 m0, s54
	s_nop 2
	global_load_lds_dwordx4 v132, s[28:29]
	s_mov_b32 m0, s7
	s_nop 0
	s_mov_b32 s7, m0
	s_mov_b32 m0, s55
	s_nop 2
	global_load_lds_dwordx4 v133, s[28:29]
	s_mov_b32 m0, s7
	s_waitcnt vmcnt(8)
	s_waitcnt lgkmcnt(0)
	s_setprio 1
	s_barrier
	v_mfma_f32_16x16x32_bf16 v[88:91], v[104:107], v[196:199], v[88:91]
	v_mfma_f32_16x16x32_bf16 v[64:67], v[104:107], v[172:175], v[64:67]
	v_mfma_f32_16x16x32_bf16 v[68:71], v[112:115], v[172:175], v[68:71]
	v_mfma_f32_16x16x32_bf16 v[72:75], v[104:107], v[180:183], v[72:75]
	v_mfma_f32_16x16x32_bf16 v[76:79], v[112:115], v[180:183], v[76:79]
	v_mfma_f32_16x16x32_bf16 v[80:83], v[104:107], v[188:191], v[80:83]
	v_mfma_f32_16x16x32_bf16 v[84:87], v[112:115], v[188:191], v[84:87]
	v_mfma_f32_16x16x32_bf16 v[204:207], v[108:111], v[200:203], v[88:91]
	v_mfma_f32_16x16x32_bf16 v[88:91], v[112:115], v[196:199], v[92:95]
	v_mfma_f32_16x16x32_bf16 v[64:67], v[108:111], v[176:179], v[64:67]
	v_mfma_f32_16x16x32_bf16 v[68:71], v[116:119], v[176:179], v[68:71]
	v_mfma_f32_16x16x32_bf16 v[72:75], v[108:111], v[184:187], v[72:75]
	v_mfma_f32_16x16x32_bf16 v[76:79], v[116:119], v[184:187], v[76:79]
	v_mfma_f32_16x16x32_bf16 v[80:83], v[108:111], v[192:195], v[80:83]
	v_mfma_f32_16x16x32_bf16 v[84:87], v[116:119], v[192:195], v[84:87]
	v_mfma_f32_16x16x32_bf16 v[92:95], v[116:119], v[200:203], v[88:91]
	s_setprio 0
	s_setprio 1
	v_mfma_f32_16x16x32_bf16 v[48:51], v[164:167], v[188:191], v[48:51]
	v_mfma_f32_16x16x32_bf16 v[88:91], v[120:123], v[172:175], v[96:99]
	v_mfma_f32_16x16x32_bf16 v[32:35], v[164:167], v[172:175], v[32:35]
	v_mfma_f32_16x16x32_bf16 v[36:39], v[120:123], v[180:183], v[36:39]
	v_mfma_f32_16x16x32_bf16 v[40:43], v[164:167], v[180:183], v[40:43]
	v_mfma_f32_16x16x32_bf16 v[44:47], v[120:123], v[188:191], v[44:47]
	v_mfma_f32_16x16x32_bf16 v[172:175], v[168:171], v[192:195], v[48:51]
	v_mfma_f32_16x16x32_bf16 v[48:51], v[120:123], v[196:199], v[52:55]
	v_mfma_f32_16x16x32_bf16 v[32:35], v[168:171], v[176:179], v[32:35]
	v_mfma_f32_16x16x32_bf16 v[36:39], v[124:127], v[184:187], v[36:39]
	v_mfma_f32_16x16x32_bf16 v[40:43], v[168:171], v[184:187], v[40:43]
	v_mfma_f32_16x16x32_bf16 v[44:47], v[124:127], v[192:195], v[44:47]
	v_mfma_f32_16x16x32_bf16 v[52:55], v[124:127], v[200:203], v[48:51]
	v_mfma_f32_16x16x32_bf16 v[48:51], v[164:167], v[196:199], v[56:59]
	v_mfma_f32_16x16x32_bf16 v[208:211], v[124:127], v[176:179], v[88:91]
	v_mfma_f32_16x16x32_bf16 v[176:179], v[168:171], v[200:203], v[48:51]
	s_setprio 0
	s_barrier
	s_nop 3
	ds_read_b128 v[48:51], v136 offset:16384
	ds_read_b128 v[56:59], v136 offset:17408
	ds_read_b128 v[88:91], v136 offset:18432
	ds_read_b128 v[96:99], v136 offset:19456
	ds_read_b128 v[180:183], v136 offset:20480
	ds_read_b128 v[184:187], v136 offset:21504
	ds_read_b128 v[188:191], v136 offset:22528
	ds_read_b128 v[192:195], v136 offset:23552
	s_mov_b32 s7, m0
	s_mov_b32 m0, s40
	s_nop 2
	global_load_lds_dwordx4 v130, s[62:63]
	s_mov_b32 m0, s7
	s_nop 0
	s_mov_b32 s7, m0
	s_mov_b32 m0, s41
	s_nop 2
	global_load_lds_dwordx4 v131, s[62:63]
	s_mov_b32 m0, s7
	s_nop 0
	s_mov_b32 s7, m0
	s_mov_b32 m0, s42
	s_nop 2
	global_load_lds_dwordx4 v130, s[34:35]
	s_mov_b32 m0, s7
	s_nop 0
	s_mov_b32 s7, m0
	s_mov_b32 m0, s43
	s_nop 2
	global_load_lds_dwordx4 v131, s[34:35]
	s_mov_b32 m0, s7
	s_nop 0
	s_mov_b32 s7, m0
	s_mov_b32 m0, s97
	s_nop 2
	global_load_lds_dwordx4 v132, s[36:37]
	s_mov_b32 m0, s7
	s_nop 0
	s_mov_b32 s7, m0
	s_mov_b32 m0, s44
	s_nop 2
	global_load_lds_dwordx4 v133, s[36:37]
	s_mov_b32 m0, s7
	s_waitcnt vmcnt(8)
	s_waitcnt lgkmcnt(0)
	s_setprio 1
	s_barrier
	v_mfma_f32_16x16x32_bf16 v[0:3], v[104:107], v[188:191], v[0:3]
	v_mfma_f32_16x16x32_bf16 v[4:7], v[112:115], v[188:191], v[4:7]
	v_mfma_f32_16x16x32_bf16 v[140:143], v[104:107], v[48:51], v[140:143]
	v_mfma_f32_16x16x32_bf16 v[144:147], v[112:115], v[48:51], v[144:147]
	v_mfma_f32_16x16x32_bf16 v[148:151], v[104:107], v[88:91], v[148:151]
	v_mfma_f32_16x16x32_bf16 v[152:155], v[112:115], v[88:91], v[152:155]
	v_mfma_f32_16x16x32_bf16 v[156:159], v[104:107], v[180:183], v[156:159]
	v_mfma_f32_16x16x32_bf16 v[160:163], v[112:115], v[180:183], v[160:163]
	v_mfma_f32_16x16x32_bf16 v[0:3], v[108:111], v[192:195], v[0:3]
	v_mfma_f32_16x16x32_bf16 v[4:7], v[116:119], v[192:195], v[4:7]
	v_mfma_f32_16x16x32_bf16 v[140:143], v[108:111], v[56:59], v[140:143]
	v_mfma_f32_16x16x32_bf16 v[144:147], v[116:119], v[56:59], v[144:147]
	v_mfma_f32_16x16x32_bf16 v[148:151], v[108:111], v[96:99], v[148:151]
	v_mfma_f32_16x16x32_bf16 v[152:155], v[116:119], v[96:99], v[152:155]
	v_mfma_f32_16x16x32_bf16 v[156:159], v[108:111], v[184:187], v[156:159]
	v_mfma_f32_16x16x32_bf16 v[160:163], v[116:119], v[184:187], v[160:163]
	s_setprio 0
	s_setprio 1
	v_mfma_f32_16x16x32_bf16 v[12:15], v[164:167], v[48:51], v[12:15]
	v_mfma_f32_16x16x32_bf16 v[196:199], v[168:171], v[56:59], v[12:15]
	v_mfma_f32_16x16x32_bf16 v[12:15], v[120:123], v[88:91], v[24:27]
	v_mfma_f32_16x16x32_bf16 v[24:27], v[124:127], v[96:99], v[12:15]
	v_mfma_f32_16x16x32_bf16 v[12:15], v[164:167], v[88:91], v[28:31]
	v_mfma_f32_16x16x32_bf16 v[200:203], v[168:171], v[96:99], v[12:15]
	v_mfma_f32_16x16x32_bf16 v[12:15], v[120:123], v[180:183], v[60:63]
	v_mfma_f32_16x16x32_bf16 v[212:215], v[124:127], v[184:187], v[12:15]
	v_mfma_f32_16x16x32_bf16 v[12:15], v[164:167], v[180:183], v[100:103]
	v_mfma_f32_16x16x32_bf16 v[8:11], v[120:123], v[48:51], v[8:11]
	v_mfma_f32_16x16x32_bf16 v[180:183], v[168:171], v[184:187], v[12:15]
	v_mfma_f32_16x16x32_bf16 v[12:15], v[120:123], v[188:191], v[16:19]
	v_mfma_f32_16x16x32_bf16 v[8:11], v[124:127], v[56:59], v[8:11]
	v_mfma_f32_16x16x32_bf16 v[184:187], v[124:127], v[192:195], v[12:15]
	v_mfma_f32_16x16x32_bf16 v[12:15], v[164:167], v[188:191], v[20:23]
	v_mfma_f32_16x16x32_bf16 v[164:167], v[168:171], v[192:195], v[12:15]
	s_setprio 0
	s_barrier
	s_nop 4
	ds_read_b128 v[12:15], v137
	ds_read_b128 v[16:19], v137 offset:1024
	ds_read_b128 v[168:171], v137 offset:2048
	ds_read_b128 v[188:191], v137 offset:3072
	ds_read_b128 v[192:195], v138
	ds_read_b128 v[216:219], v138 offset:1024
	ds_read_b128 v[220:223], v138 offset:2048
	ds_read_b128 v[224:227], v138 offset:3072
	ds_read_b128 v[20:23], v136 offset:32768
	ds_read_b128 v[28:31], v136 offset:33792
	ds_read_b128 v[60:63], v136 offset:34816
	ds_read_b128 v[100:103], v136 offset:35840
	ds_read_b128 v[228:231], v136 offset:36864
	ds_read_b128 v[232:235], v136 offset:37888
	ds_read_b128 v[236:239], v136 offset:38912
	ds_read_b128 v[240:243], v136 offset:39936
	s_add_u32 s28, s36, 0x40000
	s_addc_u32 s29, s37, 0
	s_mov_b32 s7, m0
	s_mov_b32 m0, s45
	s_nop 2
	global_load_lds_dwordx4 v132, s[28:29]
	s_mov_b32 m0, s7
	s_nop 0
	s_mov_b32 s7, m0
	s_mov_b32 m0, s46
	s_nop 2
	global_load_lds_dwordx4 v133, s[28:29]
	s_mov_b32 m0, s7
	s_waitcnt vmcnt(8)
	s_waitcnt lgkmcnt(0)
	s_setprio 1
	s_barrier
	v_mfma_f32_16x16x32_bf16 v[48:51], v[12:15], v[20:23], v[64:67]
	v_mfma_f32_16x16x32_bf16 v[120:123], v[16:19], v[28:31], v[48:51]
	v_mfma_f32_16x16x32_bf16 v[48:51], v[168:171], v[20:23], v[68:71]
	v_mfma_f32_16x16x32_bf16 v[112:115], v[188:191], v[28:31], v[48:51]
	v_mfma_f32_16x16x32_bf16 v[48:51], v[12:15], v[60:63], v[72:75]
	v_mfma_f32_16x16x32_bf16 v[104:107], v[16:19], v[100:103], v[48:51]
	v_mfma_f32_16x16x32_bf16 v[48:51], v[168:171], v[60:63], v[76:79]
	v_mfma_f32_16x16x32_bf16 v[96:99], v[188:191], v[100:103], v[48:51]
	v_mfma_f32_16x16x32_bf16 v[48:51], v[12:15], v[228:231], v[80:83]
	v_mfma_f32_16x16x32_bf16 v[88:91], v[16:19], v[232:235], v[48:51]
	v_mfma_f32_16x16x32_bf16 v[48:51], v[168:171], v[228:231], v[84:87]
	v_mfma_f32_16x16x32_bf16 v[80:83], v[188:191], v[232:235], v[48:51]
	v_mfma_f32_16x16x32_bf16 v[48:51], v[12:15], v[236:239], v[204:207]
	v_mfma_f32_16x16x32_bf16 v[56:59], v[16:19], v[240:243], v[48:51]
	v_mfma_f32_16x16x32_bf16 v[48:51], v[168:171], v[236:239], v[92:95]
	v_mfma_f32_16x16x32_bf16 v[48:51], v[188:191], v[240:243], v[48:51]
	s_setprio 0
	s_setprio 1
	v_mfma_f32_16x16x32_bf16 v[64:67], v[192:195], v[20:23], v[208:211]
	v_mfma_f32_16x16x32_bf16 v[20:23], v[220:223], v[20:23], v[32:35]
	v_mfma_f32_16x16x32_bf16 v[116:119], v[224:227], v[28:31], v[20:23]
	v_mfma_f32_16x16x32_bf16 v[20:23], v[192:195], v[60:63], v[36:39]
	v_mfma_f32_16x16x32_bf16 v[108:111], v[216:219], v[100:103], v[20:23]
	v_mfma_f32_16x16x32_bf16 v[20:23], v[220:223], v[60:63], v[40:43]
	v_mfma_f32_16x16x32_bf16 v[100:103], v[224:227], v[100:103], v[20:23]
	v_mfma_f32_16x16x32_bf16 v[20:23], v[192:195], v[228:231], v[44:47]
	v_mfma_f32_16x16x32_bf16 v[92:95], v[216:219], v[232:235], v[20:23]
	v_mfma_f32_16x16x32_bf16 v[20:23], v[220:223], v[228:231], v[172:175]
	v_mfma_f32_16x16x32_bf16 v[84:87], v[224:227], v[232:235], v[20:23]
	v_mfma_f32_16x16x32_bf16 v[20:23], v[192:195], v[236:239], v[52:55]
	v_mfma_f32_16x16x32_bf16 v[60:63], v[216:219], v[240:243], v[20:23]
	v_mfma_f32_16x16x32_bf16 v[20:23], v[220:223], v[236:239], v[176:179]
	v_mfma_f32_16x16x32_bf16 v[124:127], v[216:219], v[28:31], v[64:67]
	v_mfma_f32_16x16x32_bf16 v[52:55], v[224:227], v[240:243], v[20:23]
	s_setprio 0
	s_barrier
	ds_read_b128 v[32:35], v136 offset:49152
	ds_read_b128 v[40:43], v136 offset:50176
	ds_read_b128 v[172:175], v136 offset:51200
	ds_read_b128 v[176:179], v136 offset:52224
	ds_read_b128 v[204:207], v136 offset:53248
	ds_read_b128 v[208:211], v136 offset:54272
	ds_read_b128 v[228:231], v136 offset:55296
	ds_read_b128 v[232:235], v136 offset:56320
	s_mov_b32 s7, m0
	s_mov_b32 m0, s48
	s_nop 2
	global_load_lds_dwordx4 v130, s[56:57]
	s_mov_b32 m0, s7
	s_add_u32 s28, s34, 0x80
	s_mov_b32 s7, m0
	s_mov_b32 m0, s49
	s_nop 2
	global_load_lds_dwordx4 v131, s[56:57]
	s_mov_b32 m0, s7
	s_addc_u32 s29, s35, 0
	s_mov_b32 s7, m0
	s_mov_b32 m0, s52
	s_nop 2
	global_load_lds_dwordx4 v130, s[28:29]
	s_mov_b32 m0, s7
	s_nop 0
	s_mov_b32 s7, m0
	s_mov_b32 m0, s53
	s_nop 2
	global_load_lds_dwordx4 v131, s[28:29]
	s_mov_b32 m0, s7
	s_nop 0
	s_mov_b32 s7, m0
	s_mov_b32 m0, s50
	s_nop 2
	global_load_lds_dwordx4 v132, s[30:31]
	s_mov_b32 m0, s7
	s_nop 0
	s_mov_b32 s7, m0
	s_mov_b32 m0, s51
	s_nop 2
	global_load_lds_dwordx4 v133, s[30:31]
	s_mov_b32 m0, s7
	s_waitcnt vmcnt(8)
	s_waitcnt lgkmcnt(0)
	s_setprio 1
	s_barrier
	v_mfma_f32_16x16x32_bf16 v[20:23], v[12:15], v[32:35], v[140:143]
	v_mfma_f32_16x16x32_bf16 v[76:79], v[16:19], v[40:43], v[20:23]
	v_mfma_f32_16x16x32_bf16 v[20:23], v[168:171], v[32:35], v[144:147]
	v_mfma_f32_16x16x32_bf16 v[68:71], v[188:191], v[40:43], v[20:23]
	v_mfma_f32_16x16x32_bf16 v[20:23], v[12:15], v[172:175], v[148:151]
	v_mfma_f32_16x16x32_bf16 v[44:47], v[16:19], v[176:179], v[20:23]
	v_mfma_f32_16x16x32_bf16 v[20:23], v[168:171], v[172:175], v[152:155]
	v_mfma_f32_16x16x32_bf16 v[36:39], v[188:191], v[176:179], v[20:23]
	v_mfma_f32_16x16x32_bf16 v[20:23], v[12:15], v[204:207], v[156:159]
	v_mfma_f32_16x16x32_bf16 v[0:3], v[12:15], v[228:231], v[0:3]
	v_mfma_f32_16x16x32_bf16 v[28:31], v[16:19], v[208:211], v[20:23]
	v_mfma_f32_16x16x32_bf16 v[20:23], v[168:171], v[204:207], v[160:163]
	v_mfma_f32_16x16x32_bf16 v[12:15], v[16:19], v[232:235], v[0:3]
	v_mfma_f32_16x16x32_bf16 v[0:3], v[168:171], v[228:231], v[4:7]
	v_mfma_f32_16x16x32_bf16 v[20:23], v[188:191], v[208:211], v[20:23]
	v_mfma_f32_16x16x32_bf16 v[4:7], v[188:191], v[232:235], v[0:3]
	s_setprio 0
	s_setprio 1
	v_mfma_f32_16x16x32_bf16 v[0:3], v[192:195], v[32:35], v[8:11]
	v_mfma_f32_16x16x32_bf16 v[72:75], v[216:219], v[40:43], v[0:3]
	v_mfma_f32_16x16x32_bf16 v[0:3], v[220:223], v[32:35], v[196:199]
	v_mfma_f32_16x16x32_bf16 v[64:67], v[224:227], v[40:43], v[0:3]
	v_mfma_f32_16x16x32_bf16 v[0:3], v[192:195], v[172:175], v[24:27]
	v_mfma_f32_16x16x32_bf16 v[40:43], v[216:219], v[176:179], v[0:3]
	v_mfma_f32_16x16x32_bf16 v[0:3], v[220:223], v[172:175], v[200:203]
	v_mfma_f32_16x16x32_bf16 v[32:35], v[224:227], v[176:179], v[0:3]
	v_mfma_f32_16x16x32_bf16 v[0:3], v[192:195], v[204:207], v[212:215]
	v_mfma_f32_16x16x32_bf16 v[24:27], v[216:219], v[208:211], v[0:3]
	v_mfma_f32_16x16x32_bf16 v[0:3], v[220:223], v[204:207], v[180:183]
	v_mfma_f32_16x16x32_bf16 v[16:19], v[224:227], v[208:211], v[0:3]
	v_mfma_f32_16x16x32_bf16 v[0:3], v[192:195], v[228:231], v[184:187]
	v_mfma_f32_16x16x32_bf16 v[8:11], v[216:219], v[232:235], v[0:3]
	v_mfma_f32_16x16x32_bf16 v[0:3], v[220:223], v[228:231], v[164:167]
	v_mfma_f32_16x16x32_bf16 v[0:3], v[224:227], v[232:235], v[0:3]
	s_setprio 0
	s_barrier
	s_andn2_b64 vcc, exec, s[10:11]
	s_cbranch_vccnz .LBB0_292
	s_barrier

.LBB0_518:
	v_add_u32_e32 v140, 0x10000, v200
	v_add_u32_e32 v156, 0x14000, v200
	s_add_u32 s34, s30, 0x100
	ds_read_b128 v[128:131], v140
	ds_read_b128 v[132:135], v140 offset:1024
	ds_read_b128 v[136:139], v140 offset:2048
	ds_read_b128 v[140:143], v140 offset:3072
	ds_read_b128 v[144:147], v156
	ds_read_b128 v[148:151], v156 offset:1024
	ds_read_b128 v[152:155], v156 offset:2048
	ds_read_b128 v[156:159], v156 offset:3072
	s_addc_u32 s35, s31, 0
	s_cmp_eq_u32 s48, 28
	s_cselect_b32 s78, s41, s44
	s_cselect_b32 s79, s40, s45
	s_cselect_b32 s37, s42, s47
	s_cselect_b32 s36, s43, s46
	s_cselect_b32 s76, s21, s34
	s_cselect_b32 s77, s19, s35
	s_add_u32 s62, s78, 0x80
	s_addc_u32 s63, s79, 0
	s_add_u32 s56, s76, 0x80
	s_addc_u32 s57, s77, 0
	ds_read_b128 v[160:163], v201
	ds_read_b128 v[164:167], v201 offset:1024
	ds_read_b128 v[168:171], v201 offset:2048
	ds_read_b128 v[172:175], v201 offset:3072
	ds_read_b128 v[176:179], v201 offset:4096
	ds_read_b128 v[180:183], v201 offset:5120
	ds_read_b128 v[184:187], v201 offset:6144
	ds_read_b128 v[188:191], v201 offset:7168
	s_add_u32 s30, s30, 0x80080
	s_addc_u32 s31, s31, 0
	s_mov_b32 s49, m0
	s_mov_b32 m0, s96
	s_nop 2
	global_load_lds_dwordx4 v198, s[30:31]
	s_mov_b32 m0, s49
	s_nop 0
	s_mov_b32 s49, m0
	s_mov_b32 m0, s8
	s_nop 2
	global_load_lds_dwordx4 v199, s[30:31]
	s_mov_b32 m0, s49
	s_waitcnt vmcnt(8)
	s_waitcnt lgkmcnt(0)
	s_setprio 1
	s_barrier
	v_mfma_f32_16x16x32_bf16 v[124:127], v[128:131], v[160:163], v[124:127]
	v_mfma_f32_16x16x32_bf16 v[120:123], v[136:139], v[160:163], v[120:123]
	v_mfma_f32_16x16x32_bf16 v[108:111], v[128:131], v[168:171], v[108:111]
	v_mfma_f32_16x16x32_bf16 v[104:107], v[136:139], v[168:171], v[104:107]
	v_mfma_f32_16x16x32_bf16 v[92:95], v[128:131], v[176:179], v[92:95]
	v_mfma_f32_16x16x32_bf16 v[88:91], v[136:139], v[176:179], v[88:91]
	v_mfma_f32_16x16x32_bf16 v[76:79], v[128:131], v[184:187], v[76:79]
	v_mfma_f32_16x16x32_bf16 v[72:75], v[136:139], v[184:187], v[72:75]
	v_mfma_f32_16x16x32_bf16 v[124:127], v[132:135], v[164:167], v[124:127]
	v_mfma_f32_16x16x32_bf16 v[120:123], v[140:143], v[164:167], v[120:123]
	v_mfma_f32_16x16x32_bf16 v[108:111], v[132:135], v[172:175], v[108:111]
	v_mfma_f32_16x16x32_bf16 v[104:107], v[140:143], v[172:175], v[104:107]
	v_mfma_f32_16x16x32_bf16 v[92:95], v[132:135], v[180:183], v[92:95]
	v_mfma_f32_16x16x32_bf16 v[88:91], v[140:143], v[180:183], v[88:91]
	v_mfma_f32_16x16x32_bf16 v[76:79], v[132:135], v[188:191], v[76:79]
	v_mfma_f32_16x16x32_bf16 v[72:75], v[140:143], v[188:191], v[72:75]
	s_setprio 0
	s_setprio 1
	v_mfma_f32_16x16x32_bf16 v[116:119], v[144:147], v[160:163], v[116:119]
	v_mfma_f32_16x16x32_bf16 v[112:115], v[152:155], v[160:163], v[112:115]
	v_mfma_f32_16x16x32_bf16 v[100:103], v[144:147], v[168:171], v[100:103]
	v_mfma_f32_16x16x32_bf16 v[96:99], v[152:155], v[168:171], v[96:99]
	v_mfma_f32_16x16x32_bf16 v[84:87], v[144:147], v[176:179], v[84:87]
	v_mfma_f32_16x16x32_bf16 v[80:83], v[152:155], v[176:179], v[80:83]
	v_mfma_f32_16x16x32_bf16 v[68:71], v[144:147], v[184:187], v[68:71]
	v_mfma_f32_16x16x32_bf16 v[64:67], v[152:155], v[184:187], v[64:67]
	v_mfma_f32_16x16x32_bf16 v[116:119], v[148:151], v[164:167], v[116:119]
	v_mfma_f32_16x16x32_bf16 v[112:115], v[156:159], v[164:167], v[112:115]
	v_mfma_f32_16x16x32_bf16 v[100:103], v[148:151], v[172:175], v[100:103]
	v_mfma_f32_16x16x32_bf16 v[96:99], v[156:159], v[172:175], v[96:99]
	v_mfma_f32_16x16x32_bf16 v[84:87], v[148:151], v[180:183], v[84:87]
	v_mfma_f32_16x16x32_bf16 v[80:83], v[156:159], v[180:183], v[80:83]
	v_mfma_f32_16x16x32_bf16 v[68:71], v[148:151], v[188:191], v[68:71]
	v_mfma_f32_16x16x32_bf16 v[64:67], v[156:159], v[188:191], v[64:67]
	s_setprio 0
	s_barrier
	ds_read_b128 v[160:163], v201 offset:16384
	ds_read_b128 v[164:167], v201 offset:17408
	ds_read_b128 v[168:171], v201 offset:18432
	ds_read_b128 v[172:175], v201 offset:19456
	ds_read_b128 v[176:179], v201 offset:20480
	ds_read_b128 v[180:183], v201 offset:21504
	ds_read_b128 v[184:187], v201 offset:22528
	ds_read_b128 v[188:191], v201 offset:23552
	s_mov_b32 s30, m0
	s_mov_b32 m0, s86
	s_nop 2
	global_load_lds_dwordx4 v196, s[78:79]
	s_mov_b32 m0, s30
	s_nop 0
	s_mov_b32 s30, m0
	s_mov_b32 m0, s87
	s_nop 2
	global_load_lds_dwordx4 v197, s[78:79]
	s_mov_b32 m0, s30
	s_nop 0
	s_mov_b32 s30, m0
	s_mov_b32 m0, s97
	s_nop 2
	global_load_lds_dwordx4 v196, s[36:37]
	s_mov_b32 m0, s30
	s_nop 0
	s_mov_b32 s30, m0
	s_mov_b32 m0, s38
	s_nop 2
	global_load_lds_dwordx4 v197, s[36:37]
	s_mov_b32 m0, s30
	s_nop 0
	s_mov_b32 s30, m0
	s_mov_b32 m0, s80
	s_nop 2
	global_load_lds_dwordx4 v198, s[76:77]
	s_mov_b32 m0, s30
	s_nop 0
	s_mov_b32 s30, m0
	s_mov_b32 m0, s6
	s_nop 2
	global_load_lds_dwordx4 v199, s[76:77]
	s_mov_b32 m0, s30
	s_waitcnt vmcnt(8)
	s_waitcnt lgkmcnt(0)
	s_setprio 1
	s_barrier
	v_mfma_f32_16x16x32_bf16 v[60:63], v[128:131], v[160:163], v[60:63]
	v_mfma_f32_16x16x32_bf16 v[56:59], v[136:139], v[160:163], v[56:59]
	v_mfma_f32_16x16x32_bf16 v[44:47], v[128:131], v[168:171], v[44:47]
	v_mfma_f32_16x16x32_bf16 v[40:43], v[136:139], v[168:171], v[40:43]
	v_mfma_f32_16x16x32_bf16 v[20:23], v[128:131], v[176:179], v[20:23]
	v_mfma_f32_16x16x32_bf16 v[16:19], v[136:139], v[176:179], v[16:19]
	v_mfma_f32_16x16x32_bf16 v[4:7], v[128:131], v[184:187], v[4:7]
	v_mfma_f32_16x16x32_bf16 v[0:3], v[136:139], v[184:187], v[0:3]
	v_mfma_f32_16x16x32_bf16 v[60:63], v[132:135], v[164:167], v[60:63]
	v_mfma_f32_16x16x32_bf16 v[56:59], v[140:143], v[164:167], v[56:59]
	v_mfma_f32_16x16x32_bf16 v[44:47], v[132:135], v[172:175], v[44:47]
	v_mfma_f32_16x16x32_bf16 v[40:43], v[140:143], v[172:175], v[40:43]
	v_mfma_f32_16x16x32_bf16 v[20:23], v[132:135], v[180:183], v[20:23]
	v_mfma_f32_16x16x32_bf16 v[16:19], v[140:143], v[180:183], v[16:19]
	v_mfma_f32_16x16x32_bf16 v[4:7], v[132:135], v[188:191], v[4:7]
	v_mfma_f32_16x16x32_bf16 v[0:3], v[140:143], v[188:191], v[0:3]
	s_setprio 0
	s_setprio 1
	v_mfma_f32_16x16x32_bf16 v[52:55], v[144:147], v[160:163], v[52:55]
	v_mfma_f32_16x16x32_bf16 v[48:51], v[152:155], v[160:163], v[48:51]
	v_mfma_f32_16x16x32_bf16 v[36:39], v[144:147], v[168:171], v[36:39]
	v_mfma_f32_16x16x32_bf16 v[32:35], v[152:155], v[168:171], v[32:35]
	v_mfma_f32_16x16x32_bf16 v[28:31], v[144:147], v[176:179], v[28:31]
	v_mfma_f32_16x16x32_bf16 v[24:27], v[152:155], v[176:179], v[24:27]
	v_mfma_f32_16x16x32_bf16 v[12:15], v[144:147], v[184:187], v[12:15]
	v_mfma_f32_16x16x32_bf16 v[8:11], v[152:155], v[184:187], v[8:11]
	v_mfma_f32_16x16x32_bf16 v[52:55], v[148:151], v[164:167], v[52:55]
	v_mfma_f32_16x16x32_bf16 v[48:51], v[156:159], v[164:167], v[48:51]
	v_mfma_f32_16x16x32_bf16 v[36:39], v[148:151], v[172:175], v[36:39]
	v_mfma_f32_16x16x32_bf16 v[32:35], v[156:159], v[172:175], v[32:35]
	v_mfma_f32_16x16x32_bf16 v[28:31], v[148:151], v[180:183], v[28:31]
	v_mfma_f32_16x16x32_bf16 v[24:27], v[156:159], v[180:183], v[24:27]
	v_mfma_f32_16x16x32_bf16 v[12:15], v[148:151], v[188:191], v[12:15]
	v_mfma_f32_16x16x32_bf16 v[8:11], v[156:159], v[188:191], v[8:11]
	s_setprio 0
	s_barrier
	v_add_u32_e32 v140, 0x18000, v200
	v_add_u32_e32 v156, 0x1c000, v200
	ds_read_b128 v[128:131], v140
	ds_read_b128 v[132:135], v140 offset:1024
	ds_read_b128 v[136:139], v140 offset:2048
	ds_read_b128 v[140:143], v140 offset:3072
	ds_read_b128 v[144:147], v156
	ds_read_b128 v[148:151], v156 offset:1024
	ds_read_b128 v[152:155], v156 offset:2048
	ds_read_b128 v[156:159], v156 offset:3072
	ds_read_b128 v[160:163], v201 offset:32768
	ds_read_b128 v[164:167], v201 offset:33792
	ds_read_b128 v[168:171], v201 offset:34816
	ds_read_b128 v[172:175], v201 offset:35840
	ds_read_b128 v[176:179], v201 offset:36864
	ds_read_b128 v[180:183], v201 offset:37888
	ds_read_b128 v[184:187], v201 offset:38912
	ds_read_b128 v[188:191], v201 offset:39936
	s_add_u32 s30, s76, 0x80000
	s_addc_u32 s31, s77, 0
	s_mov_b32 s49, m0
	s_mov_b32 m0, s7
	s_nop 2
	global_load_lds_dwordx4 v198, s[30:31]
	s_mov_b32 m0, s49
	s_nop 0
	s_mov_b32 s49, m0
	s_mov_b32 m0, s3
	s_nop 2
	global_load_lds_dwordx4 v199, s[30:31]
	s_mov_b32 m0, s49
	s_waitcnt vmcnt(8)
	s_waitcnt lgkmcnt(0)
	s_setprio 1
	s_barrier
	v_mfma_f32_16x16x32_bf16 v[124:127], v[128:131], v[160:163], v[124:127]
	v_mfma_f32_16x16x32_bf16 v[120:123], v[136:139], v[160:163], v[120:123]
	v_mfma_f32_16x16x32_bf16 v[108:111], v[128:131], v[168:171], v[108:111]
	v_mfma_f32_16x16x32_bf16 v[104:107], v[136:139], v[168:171], v[104:107]
	v_mfma_f32_16x16x32_bf16 v[92:95], v[128:131], v[176:179], v[92:95]
	v_mfma_f32_16x16x32_bf16 v[88:91], v[136:139], v[176:179], v[88:91]
	v_mfma_f32_16x16x32_bf16 v[76:79], v[128:131], v[184:187], v[76:79]
	v_mfma_f32_16x16x32_bf16 v[72:75], v[136:139], v[184:187], v[72:75]
	v_mfma_f32_16x16x32_bf16 v[124:127], v[132:135], v[164:167], v[124:127]
	v_mfma_f32_16x16x32_bf16 v[120:123], v[140:143], v[164:167], v[120:123]
	v_mfma_f32_16x16x32_bf16 v[108:111], v[132:135], v[172:175], v[108:111]
	v_mfma_f32_16x16x32_bf16 v[104:107], v[140:143], v[172:175], v[104:107]
	v_mfma_f32_16x16x32_bf16 v[92:95], v[132:135], v[180:183], v[92:95]
	v_mfma_f32_16x16x32_bf16 v[88:91], v[140:143], v[180:183], v[88:91]
	v_mfma_f32_16x16x32_bf16 v[76:79], v[132:135], v[188:191], v[76:79]
	v_mfma_f32_16x16x32_bf16 v[72:75], v[140:143], v[188:191], v[72:75]
	s_setprio 0
	s_setprio 1
	v_mfma_f32_16x16x32_bf16 v[116:119], v[144:147], v[160:163], v[116:119]
	v_mfma_f32_16x16x32_bf16 v[112:115], v[152:155], v[160:163], v[112:115]
	v_mfma_f32_16x16x32_bf16 v[100:103], v[144:147], v[168:171], v[100:103]
	v_mfma_f32_16x16x32_bf16 v[96:99], v[152:155], v[168:171], v[96:99]
	v_mfma_f32_16x16x32_bf16 v[84:87], v[144:147], v[176:179], v[84:87]
	v_mfma_f32_16x16x32_bf16 v[80:83], v[152:155], v[176:179], v[80:83]
	v_mfma_f32_16x16x32_bf16 v[68:71], v[144:147], v[184:187], v[68:71]
	v_mfma_f32_16x16x32_bf16 v[64:67], v[152:155], v[184:187], v[64:67]
	v_mfma_f32_16x16x32_bf16 v[116:119], v[148:151], v[164:167], v[116:119]
	v_mfma_f32_16x16x32_bf16 v[112:115], v[156:159], v[164:167], v[112:115]
	v_mfma_f32_16x16x32_bf16 v[100:103], v[148:151], v[172:175], v[100:103]
	v_mfma_f32_16x16x32_bf16 v[96:99], v[156:159], v[172:175], v[96:99]
	v_mfma_f32_16x16x32_bf16 v[84:87], v[148:151], v[180:183], v[84:87]
	v_mfma_f32_16x16x32_bf16 v[80:83], v[156:159], v[180:183], v[80:83]
	v_mfma_f32_16x16x32_bf16 v[68:71], v[148:151], v[188:191], v[68:71]
	v_mfma_f32_16x16x32_bf16 v[64:67], v[156:159], v[188:191], v[64:67]
	s_setprio 0
	s_barrier
	ds_read_b128 v[160:163], v201 offset:49152
	ds_read_b128 v[164:167], v201 offset:50176
	ds_read_b128 v[168:171], v201 offset:51200
	ds_read_b128 v[172:175], v201 offset:52224
	ds_read_b128 v[176:179], v201 offset:53248
	ds_read_b128 v[180:183], v201 offset:54272
	ds_read_b128 v[184:187], v201 offset:55296
	ds_read_b128 v[188:191], v201 offset:56320
	s_mov_b32 s30, m0
	s_mov_b32 m0, s2
	s_nop 2
	global_load_lds_dwordx4 v196, s[62:63]
	s_mov_b32 m0, s30
	s_nop 0
	s_mov_b32 s30, m0
	s_mov_b32 m0, s83
	s_nop 2
	global_load_lds_dwordx4 v197, s[62:63]
	s_mov_b32 m0, s30
	s_add_u32 s30, s36, 0x80
	s_addc_u32 s31, s37, 0
	s_mov_b32 s36, m0
	s_mov_b32 m0, s0
	s_nop 2
	global_load_lds_dwordx4 v196, s[30:31]
	s_mov_b32 m0, s36
	s_nop 0
	s_mov_b32 s36, m0
	s_mov_b32 m0, s1
	s_nop 2
	global_load_lds_dwordx4 v197, s[30:31]
	s_mov_b32 m0, s36
	s_mov_b32 s30, m0
	s_mov_b32 m0, s84
	s_nop 2
	global_load_lds_dwordx4 v198, s[56:57]
	s_mov_b32 m0, s30
	s_nop 0
	s_mov_b32 s30, m0
	s_mov_b32 m0, s85
	s_nop 2
	global_load_lds_dwordx4 v199, s[56:57]
	s_mov_b32 m0, s30
	s_waitcnt vmcnt(8)
	s_waitcnt lgkmcnt(0)
	s_setprio 1
	s_barrier
	v_mfma_f32_16x16x32_bf16 v[60:63], v[128:131], v[160:163], v[60:63]
	v_mfma_f32_16x16x32_bf16 v[56:59], v[136:139], v[160:163], v[56:59]
	v_mfma_f32_16x16x32_bf16 v[44:47], v[128:131], v[168:171], v[44:47]
	v_mfma_f32_16x16x32_bf16 v[40:43], v[136:139], v[168:171], v[40:43]
	v_mfma_f32_16x16x32_bf16 v[20:23], v[128:131], v[176:179], v[20:23]
	v_mfma_f32_16x16x32_bf16 v[16:19], v[136:139], v[176:179], v[16:19]
	v_mfma_f32_16x16x32_bf16 v[4:7], v[128:131], v[184:187], v[4:7]
	v_mfma_f32_16x16x32_bf16 v[0:3], v[136:139], v[184:187], v[0:3]
	v_mfma_f32_16x16x32_bf16 v[60:63], v[132:135], v[164:167], v[60:63]
	v_mfma_f32_16x16x32_bf16 v[56:59], v[140:143], v[164:167], v[56:59]
	v_mfma_f32_16x16x32_bf16 v[44:47], v[132:135], v[172:175], v[44:47]
	v_mfma_f32_16x16x32_bf16 v[40:43], v[140:143], v[172:175], v[40:43]
	v_mfma_f32_16x16x32_bf16 v[20:23], v[132:135], v[180:183], v[20:23]
	v_mfma_f32_16x16x32_bf16 v[16:19], v[140:143], v[180:183], v[16:19]
	v_mfma_f32_16x16x32_bf16 v[4:7], v[132:135], v[188:191], v[4:7]
	v_mfma_f32_16x16x32_bf16 v[0:3], v[140:143], v[188:191], v[0:3]
	s_setprio 0
	s_setprio 1
	v_mfma_f32_16x16x32_bf16 v[52:55], v[144:147], v[160:163], v[52:55]
	v_mfma_f32_16x16x32_bf16 v[48:51], v[152:155], v[160:163], v[48:51]
	v_mfma_f32_16x16x32_bf16 v[36:39], v[144:147], v[168:171], v[36:39]
	v_mfma_f32_16x16x32_bf16 v[32:35], v[152:155], v[168:171], v[32:35]
	v_mfma_f32_16x16x32_bf16 v[28:31], v[144:147], v[176:179], v[28:31]
	v_mfma_f32_16x16x32_bf16 v[24:27], v[152:155], v[176:179], v[24:27]
	v_mfma_f32_16x16x32_bf16 v[12:15], v[144:147], v[184:187], v[12:15]
	v_mfma_f32_16x16x32_bf16 v[8:11], v[152:155], v[184:187], v[8:11]
	v_mfma_f32_16x16x32_bf16 v[52:55], v[148:151], v[164:167], v[52:55]
	v_mfma_f32_16x16x32_bf16 v[48:51], v[156:159], v[164:167], v[48:51]
	v_mfma_f32_16x16x32_bf16 v[36:39], v[148:151], v[172:175], v[36:39]
	v_mfma_f32_16x16x32_bf16 v[32:35], v[156:159], v[172:175], v[32:35]
	v_mfma_f32_16x16x32_bf16 v[28:31], v[148:151], v[180:183], v[28:31]
	v_mfma_f32_16x16x32_bf16 v[24:27], v[156:159], v[180:183], v[24:27]
	v_mfma_f32_16x16x32_bf16 v[12:15], v[148:151], v[188:191], v[12:15]
	v_mfma_f32_16x16x32_bf16 v[8:11], v[156:159], v[188:191], v[8:11]
	s_setprio 0
	s_barrier
	s_add_i32 s48, s48, 2
	s_add_u32 s44, s44, 0x100
	s_addc_u32 s45, s45, 0
	s_add_u32 s46, s46, 0x100
	s_addc_u32 s47, s47, 0
	s_cmp_gt_u32 s48, 29
	s_mov_b64 s[30:31], s[34:35]
	s_cbranch_scc1 .LBB0_521

.LBB0_695:
	s_add_u32 s10, s6, s36
	s_addc_u32 s11, s7, s37
	s_add_u32 s76, s10, 0x100
	s_addc_u32 s77, s11, 0
	s_add_u32 s62, s14, s36
	s_addc_u32 s63, s15, s37
	s_add_u32 s62, s62, 0x100
	s_addc_u32 s63, s63, 0
	s_add_u32 s78, s16, s36
	v_add_u32_e32 v128, 0x10000, v134
	s_addc_u32 s79, s17, s37
	ds_read_b128 v[138:141], v128
	ds_read_b128 v[142:145], v128 offset:1024
	ds_read_b128 v[146:149], v128 offset:2048
	ds_read_b128 v[150:153], v128 offset:3072
	v_add_u32_e32 v128, 0x14000, v134
	s_add_u32 s78, s78, 0x100
	ds_read_b128 v[154:157], v128
	ds_read_b128 v[158:161], v128 offset:1024
	ds_read_b128 v[162:165], v128 offset:2048
	ds_read_b128 v[166:169], v128 offset:3072
	s_addc_u32 s79, s79, 0
	s_cmp_eq_u32 vcc_lo, 12
	s_cselect_b32 s82, s87, s62
	s_cselect_b32 s83, s86, s63
	s_cselect_b32 s63, s96, s79
	s_cselect_b32 s62, s97, s78
	s_cselect_b32 s80, s25, s76
	s_cselect_b32 s81, s23, s77
	s_add_u32 s78, s82, 0x80
	s_addc_u32 s79, s83, 0
	s_add_u32 s76, s80, 0x80
	s_addc_u32 s77, s81, 0
	ds_read_b128 v[170:173], v135
	ds_read_b128 v[174:177], v135 offset:1024
	ds_read_b128 v[178:181], v135 offset:2048
	ds_read_b128 v[182:185], v135 offset:3072
	ds_read_b128 v[186:189], v135 offset:4096
	ds_read_b128 v[190:193], v135 offset:5120
	ds_read_b128 v[194:197], v135 offset:6144
	ds_read_b128 v[198:201], v135 offset:7168
	s_add_u32 s10, s10, 0x40080
	s_addc_u32 s11, s11, 0
	s_mov_b32 vcc_hi, m0
	s_mov_b32 m0, s55
	s_nop 2
	global_load_lds_dwordx4 v132, s[10:11]
	s_mov_b32 m0, vcc_hi
	s_nop 0
	s_mov_b32 vcc_hi, m0
	s_mov_b32 m0, s84
	s_nop 2
	global_load_lds_dwordx4 v133, s[10:11]
	s_mov_b32 m0, vcc_hi
	s_waitcnt vmcnt(8)
	s_waitcnt lgkmcnt(0)
	s_setprio 1
	s_barrier
	v_mfma_scale_f32_16x16x128_f8f6f4 v[124:127], v[138:145], v[170:177], v[124:127], v136, v136 op_sel_hi:[0,0,0]
	v_mfma_scale_f32_16x16x128_f8f6f4 v[120:123], v[146:153], v[170:177], v[120:123], v136, v136 op_sel_hi:[0,0,0]
	v_mfma_scale_f32_16x16x128_f8f6f4 v[116:119], v[138:145], v[178:185], v[116:119], v136, v136 op_sel_hi:[0,0,0]
	v_mfma_scale_f32_16x16x128_f8f6f4 v[112:115], v[146:153], v[178:185], v[112:115], v136, v136 op_sel_hi:[0,0,0]
	v_mfma_scale_f32_16x16x128_f8f6f4 v[202:205], v[138:145], v[186:193], v[92:95], v136, v136 op_sel_hi:[0,0,0]
	v_mfma_scale_f32_16x16x128_f8f6f4 v[206:209], v[146:153], v[186:193], v[88:91], v136, v136 op_sel_hi:[0,0,0]
	v_mfma_scale_f32_16x16x128_f8f6f4 v[210:213], v[138:145], v[194:201], v[84:87], v136, v136 op_sel_hi:[0,0,0]
	v_mfma_scale_f32_16x16x128_f8f6f4 v[214:217], v[146:153], v[194:201], v[80:83], v136, v136 op_sel_hi:[0,0,0]
	s_setprio 0
	s_setprio 1
	v_mfma_scale_f32_16x16x128_f8f6f4 v[108:111], v[154:161], v[170:177], v[108:111], v136, v136 op_sel_hi:[0,0,0]
	v_mfma_scale_f32_16x16x128_f8f6f4 v[104:107], v[162:169], v[170:177], v[104:107], v136, v136 op_sel_hi:[0,0,0]
	v_mfma_scale_f32_16x16x128_f8f6f4 v[100:103], v[154:161], v[178:185], v[100:103], v136, v136 op_sel_hi:[0,0,0]
	v_mfma_scale_f32_16x16x128_f8f6f4 v[96:99], v[162:169], v[178:185], v[96:99], v136, v136 op_sel_hi:[0,0,0]
	v_mfma_scale_f32_16x16x128_f8f6f4 v[170:173], v[154:161], v[186:193], v[76:79], v136, v136 op_sel_hi:[0,0,0]
	v_mfma_scale_f32_16x16x128_f8f6f4 v[174:177], v[162:169], v[186:193], v[72:75], v136, v136 op_sel_hi:[0,0,0]
	v_mfma_scale_f32_16x16x128_f8f6f4 v[178:181], v[154:161], v[194:201], v[68:71], v136, v136 op_sel_hi:[0,0,0]
	v_mfma_scale_f32_16x16x128_f8f6f4 v[182:185], v[162:169], v[194:201], v[64:67], v136, v136 op_sel_hi:[0,0,0]
	s_setprio 0
	s_barrier
	s_nop 4
	ds_read_b128 v[64:67], v135 offset:16384
	ds_read_b128 v[68:71], v135 offset:17408
	ds_read_b128 v[72:75], v135 offset:18432
	ds_read_b128 v[76:79], v135 offset:19456
	ds_read_b128 v[80:83], v135 offset:20480
	ds_read_b128 v[84:87], v135 offset:21504
	ds_read_b128 v[88:91], v135 offset:22528
	ds_read_b128 v[92:95], v135 offset:23552
	s_mov_b32 s10, m0
	s_mov_b32 m0, s13
	s_nop 2
	global_load_lds_dwordx4 v137, s[82:83]
	s_mov_b32 m0, s10
	s_nop 0
	s_mov_b32 s10, m0
	s_mov_b32 m0, s43
	s_nop 2
	global_load_lds_dwordx4 v254, s[82:83]
	s_mov_b32 m0, s10
	s_nop 0
	s_mov_b32 s10, m0
	s_mov_b32 m0, s44
	s_nop 2
	global_load_lds_dwordx4 v137, s[62:63]
	s_mov_b32 m0, s10
	s_nop 0
	s_mov_b32 s10, m0
	s_mov_b32 m0, s45
	s_nop 2
	global_load_lds_dwordx4 v254, s[62:63]
	s_mov_b32 m0, s10
	s_nop 0
	s_mov_b32 s10, m0
	s_mov_b32 m0, s5
	s_nop 2
	global_load_lds_dwordx4 v132, s[80:81]
	s_mov_b32 m0, s10
	s_nop 0
	s_mov_b32 s10, m0
	s_mov_b32 m0, s46
	s_nop 2
	global_load_lds_dwordx4 v133, s[80:81]
	s_mov_b32 m0, s10
	s_waitcnt vmcnt(8)
	s_waitcnt lgkmcnt(0)
	s_setprio 1
	s_barrier
	v_mfma_scale_f32_16x16x128_f8f6f4 v[60:63], v[138:145], v[64:71], v[60:63], v136, v136 op_sel_hi:[0,0,0]
	v_mfma_scale_f32_16x16x128_f8f6f4 v[186:189], v[146:153], v[64:71], v[56:59], v136, v136 op_sel_hi:[0,0,0]
	v_mfma_scale_f32_16x16x128_f8f6f4 v[190:193], v[138:145], v[72:79], v[52:55], v136, v136 op_sel_hi:[0,0,0]
	v_mfma_scale_f32_16x16x128_f8f6f4 v[194:197], v[146:153], v[72:79], v[48:51], v136, v136 op_sel_hi:[0,0,0]
	v_mfma_scale_f32_16x16x128_f8f6f4 v[198:201], v[138:145], v[80:87], v[12:15], v136, v136 op_sel_hi:[0,0,0]
	v_mfma_scale_f32_16x16x128_f8f6f4 v[218:221], v[146:153], v[80:87], v[8:11], v136, v136 op_sel_hi:[0,0,0]
	v_mfma_scale_f32_16x16x128_f8f6f4 v[222:225], v[138:145], v[88:95], v[4:7], v136, v136 op_sel_hi:[0,0,0]
	v_mfma_scale_f32_16x16x128_f8f6f4 v[226:229], v[146:153], v[88:95], v[0:3], v136, v136 op_sel_hi:[0,0,0]
	s_setprio 0
	s_setprio 1
	v_mfma_scale_f32_16x16x128_f8f6f4 v[24:27], v[162:169], v[80:87], v[24:27], v136, v136 op_sel_hi:[0,0,0]
	v_mfma_scale_f32_16x16x128_f8f6f4 v[230:233], v[154:161], v[64:71], v[44:47], v136, v136 op_sel_hi:[0,0,0]
	v_mfma_scale_f32_16x16x128_f8f6f4 v[234:237], v[162:169], v[64:71], v[40:43], v136, v136 op_sel_hi:[0,0,0]
	v_mfma_scale_f32_16x16x128_f8f6f4 v[238:241], v[154:161], v[72:79], v[36:39], v136, v136 op_sel_hi:[0,0,0]
	v_mfma_scale_f32_16x16x128_f8f6f4 v[242:245], v[162:169], v[72:79], v[20:23], v136, v136 op_sel_hi:[0,0,0]
	v_mfma_scale_f32_16x16x128_f8f6f4 v[246:249], v[154:161], v[80:87], v[16:19], v136, v136 op_sel_hi:[0,0,0]
	v_mfma_scale_f32_16x16x128_f8f6f4 v[250:253], v[154:161], v[88:95], v[28:31], v136, v136 op_sel_hi:[0,0,0]
	v_mfma_scale_f32_16x16x128_f8f6f4 v[128:131], v[162:169], v[88:95], v[32:35], v136, v136 op_sel_hi:[0,0,0]
	s_setprio 0
	s_barrier
	v_add_u32_e32 v8, 0x18000, v134
	ds_read_b128 v[0:3], v8
	ds_read_b128 v[4:7], v8 offset:1024
	ds_read_b128 v[16:19], v8 offset:2048
	ds_read_b128 v[20:23], v8 offset:3072
	v_add_u32_e32 v8, 0x1c000, v134
	ds_read_b128 v[28:31], v8
	ds_read_b128 v[32:35], v8 offset:1024
	ds_read_b128 v[138:141], v8 offset:2048
	ds_read_b128 v[142:145], v8 offset:3072
	ds_read_b128 v[8:11], v135 offset:32768
	ds_read_b128 v[12:15], v135 offset:33792
	ds_read_b128 v[36:39], v135 offset:34816
	ds_read_b128 v[40:43], v135 offset:35840
	ds_read_b128 v[44:47], v135 offset:36864
	ds_read_b128 v[48:51], v135 offset:37888
	ds_read_b128 v[52:55], v135 offset:38912
	ds_read_b128 v[56:59], v135 offset:39936
	s_add_u32 s10, s80, 0x40000
	s_addc_u32 s11, s81, 0
	s_mov_b32 s80, m0
	s_mov_b32 m0, s47
	s_nop 2
	global_load_lds_dwordx4 v132, s[10:11]
	s_mov_b32 m0, s80
	s_nop 0
	s_mov_b32 s80, m0
	s_mov_b32 m0, s48
	s_nop 2
	global_load_lds_dwordx4 v133, s[10:11]
	s_mov_b32 m0, s80
	s_waitcnt vmcnt(8)
	s_waitcnt lgkmcnt(0)
	s_setprio 1
	s_barrier
	v_mfma_scale_f32_16x16x128_f8f6f4 v[124:127], v[0:7], v[8:15], v[124:127], v136, v136 op_sel_hi:[0,0,0]
	v_mfma_scale_f32_16x16x128_f8f6f4 v[120:123], v[16:23], v[8:15], v[120:123], v136, v136 op_sel_hi:[0,0,0]
	v_mfma_scale_f32_16x16x128_f8f6f4 v[116:119], v[0:7], v[36:43], v[116:119], v136, v136 op_sel_hi:[0,0,0]
	v_mfma_scale_f32_16x16x128_f8f6f4 v[112:115], v[16:23], v[36:43], v[112:115], v136, v136 op_sel_hi:[0,0,0]
	v_mfma_scale_f32_16x16x128_f8f6f4 v[92:95], v[0:7], v[44:51], v[202:205], v136, v136 op_sel_hi:[0,0,0]
	v_mfma_scale_f32_16x16x128_f8f6f4 v[88:91], v[16:23], v[44:51], v[206:209], v136, v136 op_sel_hi:[0,0,0]
	v_mfma_scale_f32_16x16x128_f8f6f4 v[84:87], v[0:7], v[52:59], v[210:213], v136, v136 op_sel_hi:[0,0,0]
	v_mfma_scale_f32_16x16x128_f8f6f4 v[80:83], v[16:23], v[52:59], v[214:217], v136, v136 op_sel_hi:[0,0,0]
	s_setprio 0
	s_setprio 1
	v_mfma_scale_f32_16x16x128_f8f6f4 v[108:111], v[28:35], v[8:15], v[108:111], v136, v136 op_sel_hi:[0,0,0]
	v_mfma_scale_f32_16x16x128_f8f6f4 v[104:107], v[138:145], v[8:15], v[104:107], v136, v136 op_sel_hi:[0,0,0]
	v_mfma_scale_f32_16x16x128_f8f6f4 v[100:103], v[28:35], v[36:43], v[100:103], v136, v136 op_sel_hi:[0,0,0]
	v_mfma_scale_f32_16x16x128_f8f6f4 v[96:99], v[138:145], v[36:43], v[96:99], v136, v136 op_sel_hi:[0,0,0]
	v_mfma_scale_f32_16x16x128_f8f6f4 v[76:79], v[28:35], v[44:51], v[170:173], v136, v136 op_sel_hi:[0,0,0]
	v_mfma_scale_f32_16x16x128_f8f6f4 v[72:75], v[138:145], v[44:51], v[174:177], v136, v136 op_sel_hi:[0,0,0]
	v_mfma_scale_f32_16x16x128_f8f6f4 v[68:71], v[28:35], v[52:59], v[178:181], v136, v136 op_sel_hi:[0,0,0]
	v_mfma_scale_f32_16x16x128_f8f6f4 v[64:67], v[138:145], v[52:59], v[182:185], v136, v136 op_sel_hi:[0,0,0]
	s_setprio 0
	s_barrier
	ds_read_b128 v[36:39], v135 offset:49152
	ds_read_b128 v[40:43], v135 offset:50176
	ds_read_b128 v[146:149], v135 offset:51200
	ds_read_b128 v[150:153], v135 offset:52224
	ds_read_b128 v[154:157], v135 offset:53248
	ds_read_b128 v[158:161], v135 offset:54272
	ds_read_b128 v[162:165], v135 offset:55296
	ds_read_b128 v[166:169], v135 offset:56320
	s_mov_b32 s10, m0
	s_mov_b32 m0, s49
	s_nop 2
	global_load_lds_dwordx4 v137, s[78:79]
	s_mov_b32 m0, s10
	s_nop 0
	s_mov_b32 s10, m0
	s_mov_b32 m0, s50
	s_nop 2
	global_load_lds_dwordx4 v254, s[78:79]
	s_mov_b32 m0, s10
	s_add_u32 s10, s62, 0x80
	s_addc_u32 s11, s63, 0
	s_mov_b32 s62, m0
	s_mov_b32 m0, s53
	s_nop 2
	global_load_lds_dwordx4 v137, s[10:11]
	s_mov_b32 m0, s62
	s_nop 0
	s_mov_b32 s62, m0
	s_mov_b32 m0, s54
	s_nop 2
	global_load_lds_dwordx4 v254, s[10:11]
	s_mov_b32 m0, s62
	s_mov_b32 s10, m0
	s_mov_b32 m0, s51
	s_nop 2
	global_load_lds_dwordx4 v132, s[76:77]
	s_mov_b32 m0, s10
	s_nop 0
	s_mov_b32 s10, m0
	s_mov_b32 m0, s52
	s_nop 2
	global_load_lds_dwordx4 v133, s[76:77]
	s_mov_b32 m0, s10
	s_waitcnt vmcnt(8)
	s_waitcnt lgkmcnt(0)
	s_setprio 1
	s_barrier
	v_mfma_scale_f32_16x16x128_f8f6f4 v[60:63], v[0:7], v[36:43], v[60:63], v136, v136 op_sel_hi:[0,0,0]
	v_mfma_scale_f32_16x16x128_f8f6f4 v[56:59], v[16:23], v[36:43], v[186:189], v136, v136 op_sel_hi:[0,0,0]
	v_mfma_scale_f32_16x16x128_f8f6f4 v[52:55], v[0:7], v[146:153], v[190:193], v136, v136 op_sel_hi:[0,0,0]
	v_mfma_scale_f32_16x16x128_f8f6f4 v[48:51], v[16:23], v[146:153], v[194:197], v136, v136 op_sel_hi:[0,0,0]
	v_mfma_scale_f32_16x16x128_f8f6f4 v[12:15], v[0:7], v[154:161], v[198:201], v136, v136 op_sel_hi:[0,0,0]
	v_mfma_scale_f32_16x16x128_f8f6f4 v[8:11], v[16:23], v[154:161], v[218:221], v136, v136 op_sel_hi:[0,0,0]
	v_mfma_scale_f32_16x16x128_f8f6f4 v[4:7], v[0:7], v[162:169], v[222:225], v136, v136 op_sel_hi:[0,0,0]
	v_mfma_scale_f32_16x16x128_f8f6f4 v[0:3], v[16:23], v[162:169], v[226:229], v136, v136 op_sel_hi:[0,0,0]
	s_setprio 0
	s_setprio 1
	v_mfma_scale_f32_16x16x128_f8f6f4 v[44:47], v[28:35], v[36:43], v[230:233], v136, v136 op_sel_hi:[0,0,0]
	v_mfma_scale_f32_16x16x128_f8f6f4 v[40:43], v[138:145], v[36:43], v[234:237], v136, v136 op_sel_hi:[0,0,0]
	v_mfma_scale_f32_16x16x128_f8f6f4 v[36:39], v[28:35], v[146:153], v[238:241], v136, v136 op_sel_hi:[0,0,0]
	v_mfma_scale_f32_16x16x128_f8f6f4 v[20:23], v[138:145], v[146:153], v[242:245], v136, v136 op_sel_hi:[0,0,0]
	v_mfma_scale_f32_16x16x128_f8f6f4 v[16:19], v[28:35], v[154:161], v[246:249], v136, v136 op_sel_hi:[0,0,0]
	v_mfma_scale_f32_16x16x128_f8f6f4 v[24:27], v[138:145], v[154:161], v[24:27], v136, v136 op_sel_hi:[0,0,0]
	v_mfma_scale_f32_16x16x128_f8f6f4 v[28:31], v[28:35], v[162:169], v[250:253], v136, v136 op_sel_hi:[0,0,0]
	v_mfma_scale_f32_16x16x128_f8f6f4 v[32:35], v[138:145], v[162:169], v[128:131], v136, v136 op_sel_hi:[0,0,0]
	s_setprio 0
	s_barrier
	s_add_i32 vcc_lo, vcc_lo, 2
	s_add_u32 s36, s36, 0x100
	s_addc_u32 s37, s37, 0
	s_cmp_gt_u32 vcc_lo, 13
	s_cbranch_scc0 .LBB0_695
	s_and_b64 vcc, exec, s[20:21]
	s_cbranch_vccz .LBB0_698
	s_barrier

.Lz7_a:
	s_waitcnt vmcnt(8)
	s_waitcnt lgkmcnt(0)
	s_setprio 1
	s_barrier
	v_mfma_scale_f32_16x16x128_f8f6f4 v[140:143], v[116:123], v[180:187], v[140:143], v153, v153 op_sel_hi:[0,0,0]
	v_mfma_scale_f32_16x16x128_f8f6f4 v[132:135], v[156:163], v[180:187], v[132:135], v153, v153 op_sel_hi:[0,0,0]
	v_mfma_scale_f32_16x16x128_f8f6f4 v[124:127], v[116:123], v[188:195], v[124:127], v153, v153 op_sel_hi:[0,0,0]
	v_mfma_scale_f32_16x16x128_f8f6f4 v[108:111], v[156:163], v[188:195], v[108:111], v153, v153 op_sel_hi:[0,0,0]
	v_mfma_scale_f32_16x16x128_f8f6f4 v[144:147], v[116:123], v[196:203], v[96:99], v153, v153 op_sel_hi:[0,0,0]
	v_mfma_scale_f32_16x16x128_f8f6f4 v[212:215], v[156:163], v[196:203], v[88:91], v153, v153 op_sel_hi:[0,0,0]
	v_mfma_scale_f32_16x16x128_f8f6f4 v[216:219], v[116:123], v[204:211], v[80:83], v153, v153 op_sel_hi:[0,0,0]
	v_mfma_scale_f32_16x16x128_f8f6f4 v[220:223], v[156:163], v[204:211], v[72:75], v153, v153 op_sel_hi:[0,0,0]
	s_setprio 0
	s_setprio 1
	v_mfma_scale_f32_16x16x128_f8f6f4 v[136:139], v[164:171], v[180:187], v[136:139], v153, v153 op_sel_hi:[0,0,0]
	v_mfma_scale_f32_16x16x128_f8f6f4 v[128:131], v[172:179], v[180:187], v[128:131], v153, v153 op_sel_hi:[0,0,0]
	v_mfma_scale_f32_16x16x128_f8f6f4 v[112:115], v[164:171], v[188:195], v[112:115], v153, v153 op_sel_hi:[0,0,0]
	v_mfma_scale_f32_16x16x128_f8f6f4 v[100:103], v[172:179], v[188:195], v[100:103], v153, v153 op_sel_hi:[0,0,0]
	v_mfma_scale_f32_16x16x128_f8f6f4 v[180:183], v[164:171], v[196:203], v[92:95], v153, v153 op_sel_hi:[0,0,0]
	v_mfma_scale_f32_16x16x128_f8f6f4 v[184:187], v[172:179], v[196:203], v[84:87], v153, v153 op_sel_hi:[0,0,0]
	v_mfma_scale_f32_16x16x128_f8f6f4 v[188:191], v[164:171], v[204:211], v[76:79], v153, v153 op_sel_hi:[0,0,0]
	v_mfma_scale_f32_16x16x128_f8f6f4 v[192:195], v[172:179], v[204:211], v[68:71], v153, v153 op_sel_hi:[0,0,0]
	s_setprio 0
	s_barrier
	s_nop 4
	ds_read_b128 v[68:71], v152 offset:16384
	ds_read_b128 v[72:75], v152 offset:17408
	ds_read_b128 v[76:79], v152 offset:18432
	ds_read_b128 v[80:83], v152 offset:19456
	ds_read_b128 v[84:87], v152 offset:20480
	ds_read_b128 v[88:91], v152 offset:21504
	ds_read_b128 v[92:95], v152 offset:22528
	ds_read_b128 v[96:99], v152 offset:23552
	s_mov_b32 s72, m0
	s_mov_b32 m0, s3
	s_nop 2
	global_load_lds_dwordx4 v252, s[64:65]
	s_mov_b32 m0, s72
	s_nop 0
	s_mov_b32 s72, m0
	s_mov_b32 m0, s27
	s_nop 2
	global_load_lds_dwordx4 v253, s[64:65]
	s_mov_b32 m0, s72
	s_mov_b32 s64, m0
	s_mov_b32 m0, s33
	s_nop 2
	global_load_lds_dwordx4 v252, s[62:63]
	s_mov_b32 m0, s64
	s_nop 0
	s_mov_b32 s64, m0
	s_mov_b32 m0, s40
	s_nop 2
	global_load_lds_dwordx4 v253, s[62:63]
	s_mov_b32 m0, s64
	s_mov_b32 s62, m0
	s_mov_b32 m0, s2
	s_nop 2
	global_load_lds_dwordx4 v104, s[60:61]
	s_mov_b32 m0, s62
	s_nop 0
	s_mov_b32 s62, m0
	s_mov_b32 m0, s41
	s_nop 2
	global_load_lds_dwordx4 v105, s[60:61]
	s_mov_b32 m0, s62
	s_cmp_lg_u32 s83, -2
	s_cbranch_scc1 .Lz7_b
	v_mov_b32_e32 v64, 0
	v_mov_b32_e32 v65, 0
	v_pk_mov_b32 v[66:67], v[64:65], v[64:65]
	v_pk_mov_b32 v[56:57], v[64:65], v[64:65]
	v_pk_mov_b32 v[58:59], v[64:65], v[64:65]
	v_pk_mov_b32 v[48:49], v[64:65], v[64:65]
	v_pk_mov_b32 v[50:51], v[64:65], v[64:65]
	v_pk_mov_b32 v[40:41], v[64:65], v[64:65]
	v_pk_mov_b32 v[42:43], v[64:65], v[64:65]
	v_pk_mov_b32 v[28:29], v[64:65], v[64:65]
	v_pk_mov_b32 v[30:31], v[64:65], v[64:65]
	v_pk_mov_b32 v[20:21], v[64:65], v[64:65]
	v_pk_mov_b32 v[22:23], v[64:65], v[64:65]
	v_pk_mov_b32 v[12:13], v[64:65], v[64:65]
	v_pk_mov_b32 v[14:15], v[64:65], v[64:65]
	v_pk_mov_b32 v[4:5], v[64:65], v[64:65]
	v_pk_mov_b32 v[6:7], v[64:65], v[64:65]
	v_pk_mov_b32 v[60:61], v[64:65], v[64:65]
	v_pk_mov_b32 v[62:63], v[64:65], v[64:65]
	v_pk_mov_b32 v[52:53], v[64:65], v[64:65]
	v_pk_mov_b32 v[54:55], v[64:65], v[64:65]
	v_pk_mov_b32 v[32:33], v[64:65], v[64:65]
	v_pk_mov_b32 v[34:35], v[64:65], v[64:65]
	v_pk_mov_b32 v[44:45], v[64:65], v[64:65]
	v_pk_mov_b32 v[46:47], v[64:65], v[64:65]
	v_pk_mov_b32 v[24:25], v[64:65], v[64:65]
	v_pk_mov_b32 v[26:27], v[64:65], v[64:65]
	v_pk_mov_b32 v[16:17], v[64:65], v[64:65]
	v_pk_mov_b32 v[18:19], v[64:65], v[64:65]
	v_pk_mov_b32 v[8:9], v[64:65], v[64:65]
	v_pk_mov_b32 v[10:11], v[64:65], v[64:65]
	v_pk_mov_b32 v[0:1], v[64:65], v[64:65]
	v_pk_mov_b32 v[2:3], v[64:65], v[64:65]
.Lz7_b:
	s_waitcnt vmcnt(8)
	s_waitcnt lgkmcnt(0)
	s_cmp_lg_u32 s32, 0
	s_cbranch_scc1 .Lp7_ragskip_1
	s_barrier
	s_setprio 1
	s_waitcnt lgkmcnt(6)
	v_mfma_scale_f32_16x16x128_f8f6f4 v[64:67], v[116:123], v[68:75], v[64:67], v153, v153 op_sel_hi:[0,0,0]
	v_mfma_scale_f32_16x16x128_f8f6f4 v[56:59], v[156:163], v[68:75], v[56:59], v153, v153 op_sel_hi:[0,0,0]
	s_waitcnt lgkmcnt(4)
	v_mfma_scale_f32_16x16x128_f8f6f4 v[48:51], v[116:123], v[76:83], v[48:51], v153, v153 op_sel_hi:[0,0,0]
	v_mfma_scale_f32_16x16x128_f8f6f4 v[204:207], v[156:163], v[76:83], v[40:43], v153, v153 op_sel_hi:[0,0,0]
	s_waitcnt lgkmcnt(2)
	v_mfma_scale_f32_16x16x128_f8f6f4 v[208:211], v[116:123], v[84:91], v[28:31], v153, v153 op_sel_hi:[0,0,0]
	v_mfma_scale_f32_16x16x128_f8f6f4 v[224:227], v[156:163], v[84:91], v[20:23], v153, v153 op_sel_hi:[0,0,0]
	s_waitcnt lgkmcnt(0)
	v_mfma_scale_f32_16x16x128_f8f6f4 v[228:231], v[116:123], v[92:99], v[12:15], v153, v153 op_sel_hi:[0,0,0]
	v_mfma_scale_f32_16x16x128_f8f6f4 v[232:235], v[156:163], v[92:99], v[4:7], v153, v153 op_sel_hi:[0,0,0]
	s_setprio 0
	s_setprio 1
	v_mfma_scale_f32_16x16x128_f8f6f4 v[60:63], v[164:171], v[68:75], v[60:63], v153, v153 op_sel_hi:[0,0,0]
	v_mfma_scale_f32_16x16x128_f8f6f4 v[52:55], v[172:179], v[68:75], v[52:55], v153, v153 op_sel_hi:[0,0,0]
	v_mfma_scale_f32_16x16x128_f8f6f4 v[32:35], v[172:179], v[76:83], v[32:35], v153, v153 op_sel_hi:[0,0,0]
	v_mfma_scale_f32_16x16x128_f8f6f4 v[236:239], v[164:171], v[76:83], v[44:47], v153, v153 op_sel_hi:[0,0,0]
	v_mfma_scale_f32_16x16x128_f8f6f4 v[240:243], v[164:171], v[84:91], v[24:27], v153, v153 op_sel_hi:[0,0,0]
	v_mfma_scale_f32_16x16x128_f8f6f4 v[244:247], v[172:179], v[84:91], v[16:19], v153, v153 op_sel_hi:[0,0,0]
	v_mfma_scale_f32_16x16x128_f8f6f4 v[248:251], v[164:171], v[92:99], v[8:11], v153, v153 op_sel_hi:[0,0,0]
	v_mfma_scale_f32_16x16x128_f8f6f4 v[148:151], v[172:179], v[92:99], v[0:3], v153, v153 op_sel_hi:[0,0,0]
	s_setprio 0
.Lp7_rag_1:
	s_barrier
	s_nop 3
	v_add_u32_e32 v8, 0x18000, v254
	ds_read_b128 v[0:3], v8
	ds_read_b128 v[4:7], v8 offset:1024
	ds_read_b128 v[116:119], v8 offset:2048
	ds_read_b128 v[120:123], v8 offset:3072
	v_add_u32_e32 v8, 0x1c000, v254
	ds_read_b128 v[156:159], v8
	ds_read_b128 v[160:163], v8 offset:1024
	ds_read_b128 v[164:167], v8 offset:2048
	ds_read_b128 v[168:171], v8 offset:3072
	ds_read_b128 v[8:11], v152 offset:32768
	ds_read_b128 v[12:15], v152 offset:33792
	ds_read_b128 v[16:19], v152 offset:34816
	ds_read_b128 v[20:23], v152 offset:35840
	ds_read_b128 v[24:27], v152 offset:36864
	ds_read_b128 v[28:31], v152 offset:37888
	ds_read_b128 v[40:43], v152 offset:38912
	ds_read_b128 v[44:47], v152 offset:39936
	s_mov_b32 s62, m0
	s_mov_b32 m0, s42
	s_nop 2
	global_load_lds_dwordx4 v106, s[60:61]
	s_mov_b32 m0, s62
	s_nop 0
	s_mov_b32 s62, m0
	s_mov_b32 m0, s43
	s_nop 2
	global_load_lds_dwordx4 v107, s[60:61]
	s_mov_b32 m0, s62
	s_waitcnt vmcnt(8)
	s_waitcnt lgkmcnt(0)
	s_setprio 1
	s_barrier
	v_mfma_scale_f32_16x16x128_f8f6f4 v[140:143], v[0:7], v[8:15], v[140:143], v153, v153 op_sel_hi:[0,0,0]
	v_mfma_scale_f32_16x16x128_f8f6f4 v[132:135], v[116:123], v[8:15], v[132:135], v153, v153 op_sel_hi:[0,0,0]
	v_mfma_scale_f32_16x16x128_f8f6f4 v[124:127], v[0:7], v[16:23], v[124:127], v153, v153 op_sel_hi:[0,0,0]
	v_mfma_scale_f32_16x16x128_f8f6f4 v[108:111], v[116:123], v[16:23], v[108:111], v153, v153 op_sel_hi:[0,0,0]
	v_mfma_scale_f32_16x16x128_f8f6f4 v[96:99], v[0:7], v[24:31], v[144:147], v153, v153 op_sel_hi:[0,0,0]
	v_mfma_scale_f32_16x16x128_f8f6f4 v[88:91], v[116:123], v[24:31], v[212:215], v153, v153 op_sel_hi:[0,0,0]
	v_mfma_scale_f32_16x16x128_f8f6f4 v[80:83], v[0:7], v[40:47], v[216:219], v153, v153 op_sel_hi:[0,0,0]
	v_mfma_scale_f32_16x16x128_f8f6f4 v[72:75], v[116:123], v[40:47], v[220:223], v153, v153 op_sel_hi:[0,0,0]
	s_setprio 0
	s_setprio 1
	v_mfma_scale_f32_16x16x128_f8f6f4 v[136:139], v[156:163], v[8:15], v[136:139], v153, v153 op_sel_hi:[0,0,0]
	v_mfma_scale_f32_16x16x128_f8f6f4 v[128:131], v[164:171], v[8:15], v[128:131], v153, v153 op_sel_hi:[0,0,0]
	v_mfma_scale_f32_16x16x128_f8f6f4 v[112:115], v[156:163], v[16:23], v[112:115], v153, v153 op_sel_hi:[0,0,0]
	v_mfma_scale_f32_16x16x128_f8f6f4 v[100:103], v[164:171], v[16:23], v[100:103], v153, v153 op_sel_hi:[0,0,0]
	v_mfma_scale_f32_16x16x128_f8f6f4 v[92:95], v[156:163], v[24:31], v[180:183], v153, v153 op_sel_hi:[0,0,0]
	v_mfma_scale_f32_16x16x128_f8f6f4 v[84:87], v[164:171], v[24:31], v[184:187], v153, v153 op_sel_hi:[0,0,0]
	v_mfma_scale_f32_16x16x128_f8f6f4 v[76:79], v[156:163], v[40:47], v[188:191], v153, v153 op_sel_hi:[0,0,0]
	v_mfma_scale_f32_16x16x128_f8f6f4 v[68:71], v[164:171], v[40:47], v[192:195], v153, v153 op_sel_hi:[0,0,0]
	s_setprio 0
	s_barrier
	ds_read_b128 v[172:175], v152 offset:49152
	ds_read_b128 v[176:179], v152 offset:50176
	ds_read_b128 v[180:183], v152 offset:51200
	ds_read_b128 v[184:187], v152 offset:52224
	ds_read_b128 v[188:191], v152 offset:53248
	ds_read_b128 v[192:195], v152 offset:54272
	ds_read_b128 v[196:199], v152 offset:55296
	ds_read_b128 v[200:203], v152 offset:56320
	s_mov_b32 s60, m0
	s_mov_b32 m0, s46
	s_nop 2
	global_load_lds_dwordx4 v252, s[56:57]
	s_mov_b32 m0, s60
	s_nop 0
	s_mov_b32 s60, m0
	s_mov_b32 m0, s48
	s_nop 2
	global_load_lds_dwordx4 v253, s[56:57]
	s_mov_b32 m0, s60
	s_mov_b32 s56, m0
	s_mov_b32 m0, s53
	s_nop 2
	global_load_lds_dwordx4 v252, s[58:59]
	s_mov_b32 m0, s56
	s_nop 0
	s_mov_b32 s56, m0
	s_mov_b32 m0, s54
	s_nop 2
	global_load_lds_dwordx4 v253, s[58:59]
	s_mov_b32 m0, s56
	s_nop 0
	s_mov_b32 s56, m0
	s_mov_b32 m0, s49
	s_nop 2
	global_load_lds_dwordx4 v104, s[36:37]
	s_mov_b32 m0, s56
	s_nop 0
	s_mov_b32 s56, m0
	s_mov_b32 m0, s52
	s_nop 2
	global_load_lds_dwordx4 v105, s[36:37]
	s_mov_b32 m0, s56
	s_waitcnt vmcnt(8)
	s_waitcnt lgkmcnt(0)
	s_cmp_lg_u32 s32, 0
	s_cbranch_scc1 .Lp7_ragskip_3
	s_barrier
	s_setprio 1
	s_waitcnt lgkmcnt(6)
	v_mfma_scale_f32_16x16x128_f8f6f4 v[64:67], v[0:7], v[172:179], v[64:67], v153, v153 op_sel_hi:[0,0,0]
	v_mfma_scale_f32_16x16x128_f8f6f4 v[56:59], v[116:123], v[172:179], v[56:59], v153, v153 op_sel_hi:[0,0,0]
	s_waitcnt lgkmcnt(4)
	v_mfma_scale_f32_16x16x128_f8f6f4 v[48:51], v[0:7], v[180:187], v[48:51], v153, v153 op_sel_hi:[0,0,0]
	v_mfma_scale_f32_16x16x128_f8f6f4 v[40:43], v[116:123], v[180:187], v[204:207], v153, v153 op_sel_hi:[0,0,0]
	s_waitcnt lgkmcnt(2)
	v_mfma_scale_f32_16x16x128_f8f6f4 v[28:31], v[0:7], v[188:195], v[208:211], v153, v153 op_sel_hi:[0,0,0]
	v_mfma_scale_f32_16x16x128_f8f6f4 v[20:23], v[116:123], v[188:195], v[224:227], v153, v153 op_sel_hi:[0,0,0]
	s_waitcnt lgkmcnt(0)
	v_mfma_scale_f32_16x16x128_f8f6f4 v[12:15], v[0:7], v[196:203], v[228:231], v153, v153 op_sel_hi:[0,0,0]
	v_mfma_scale_f32_16x16x128_f8f6f4 v[4:7], v[116:123], v[196:203], v[232:235], v153, v153 op_sel_hi:[0,0,0]
	s_setprio 0
	s_setprio 1
	v_mfma_scale_f32_16x16x128_f8f6f4 v[60:63], v[156:163], v[172:179], v[60:63], v153, v153 op_sel_hi:[0,0,0]
	v_mfma_scale_f32_16x16x128_f8f6f4 v[52:55], v[164:171], v[172:179], v[52:55], v153, v153 op_sel_hi:[0,0,0]
	v_mfma_scale_f32_16x16x128_f8f6f4 v[44:47], v[156:163], v[180:187], v[236:239], v153, v153 op_sel_hi:[0,0,0]
	v_mfma_scale_f32_16x16x128_f8f6f4 v[32:35], v[164:171], v[180:187], v[32:35], v153, v153 op_sel_hi:[0,0,0]
	v_mfma_scale_f32_16x16x128_f8f6f4 v[24:27], v[156:163], v[188:195], v[240:243], v153, v153 op_sel_hi:[0,0,0]
	v_mfma_scale_f32_16x16x128_f8f6f4 v[16:19], v[164:171], v[188:195], v[244:247], v153, v153 op_sel_hi:[0,0,0]
	v_mfma_scale_f32_16x16x128_f8f6f4 v[8:11], v[156:163], v[196:203], v[248:251], v153, v153 op_sel_hi:[0,0,0]
	v_mfma_scale_f32_16x16x128_f8f6f4 v[0:3], v[164:171], v[196:203], v[148:151], v153, v153 op_sel_hi:[0,0,0]
	s_setprio 0

.Lp7_ragskip_1:
	s_barrier
	s_branch .Lp7_rag_1

.Lz8_a:
	s_waitcnt vmcnt(8)
	s_waitcnt lgkmcnt(0)
	s_setprio 1
	s_barrier
	v_mfma_scale_f32_16x16x128_f8f6f4 v[124:127], v[128:135], v[172:179], v[124:127], v169, v169 op_sel_hi:[0,0,0]
	v_mfma_scale_f32_16x16x128_f8f6f4 v[120:123], v[136:143], v[172:179], v[120:123], v169, v169 op_sel_hi:[0,0,0]
	v_mfma_scale_f32_16x16x128_f8f6f4 v[108:111], v[128:135], v[180:187], v[108:111], v169, v169 op_sel_hi:[0,0,0]
	v_mfma_scale_f32_16x16x128_f8f6f4 v[104:107], v[136:143], v[180:187], v[104:107], v169, v169 op_sel_hi:[0,0,0]
	v_mfma_scale_f32_16x16x128_f8f6f4 v[204:207], v[128:135], v[188:195], v[92:95], v169, v169 op_sel_hi:[0,0,0]
	v_mfma_scale_f32_16x16x128_f8f6f4 v[208:211], v[136:143], v[188:195], v[88:91], v169, v169 op_sel_hi:[0,0,0]
	v_mfma_scale_f32_16x16x128_f8f6f4 v[212:215], v[128:135], v[196:203], v[76:79], v169, v169 op_sel_hi:[0,0,0]
	v_mfma_scale_f32_16x16x128_f8f6f4 v[216:219], v[136:143], v[196:203], v[72:75], v169, v169 op_sel_hi:[0,0,0]
	s_setprio 0
	s_setprio 1
	v_mfma_scale_f32_16x16x128_f8f6f4 v[116:119], v[144:151], v[172:179], v[116:119], v169, v169 op_sel_hi:[0,0,0]
	v_mfma_scale_f32_16x16x128_f8f6f4 v[112:115], v[152:159], v[172:179], v[112:115], v169, v169 op_sel_hi:[0,0,0]
	v_mfma_scale_f32_16x16x128_f8f6f4 v[100:103], v[144:151], v[180:187], v[100:103], v169, v169 op_sel_hi:[0,0,0]
	v_mfma_scale_f32_16x16x128_f8f6f4 v[96:99], v[152:159], v[180:187], v[96:99], v169, v169 op_sel_hi:[0,0,0]
	v_mfma_scale_f32_16x16x128_f8f6f4 v[172:175], v[144:151], v[188:195], v[84:87], v169, v169 op_sel_hi:[0,0,0]
	v_mfma_scale_f32_16x16x128_f8f6f4 v[176:179], v[152:159], v[188:195], v[80:83], v169, v169 op_sel_hi:[0,0,0]
	v_mfma_scale_f32_16x16x128_f8f6f4 v[180:183], v[144:151], v[196:203], v[68:71], v169, v169 op_sel_hi:[0,0,0]
	v_mfma_scale_f32_16x16x128_f8f6f4 v[184:187], v[152:159], v[196:203], v[64:67], v169, v169 op_sel_hi:[0,0,0]
	s_setprio 0
	s_barrier
	s_nop 4
	ds_read_b128 v[64:67], v168 offset:16384
	ds_read_b128 v[68:71], v168 offset:17408
	ds_read_b128 v[72:75], v168 offset:18432
	ds_read_b128 v[76:79], v168 offset:19456
	ds_read_b128 v[80:83], v168 offset:20480
	ds_read_b128 v[84:87], v168 offset:21504
	ds_read_b128 v[88:91], v168 offset:22528
	ds_read_b128 v[92:95], v168 offset:23552
	s_mov_b32 s34, m0
	s_mov_b32 m0, s31
	s_nop 2
	global_load_lds_dwordx4 v162, s[60:61]
	s_mov_b32 m0, s34
	s_nop 0
	s_mov_b32 s34, m0
	s_mov_b32 m0, s44
	s_nop 2
	global_load_lds_dwordx4 v163, s[60:61]
	s_mov_b32 m0, s34
	s_nop 0
	s_mov_b32 s34, m0
	s_mov_b32 m0, s45
	s_nop 2
	global_load_lds_dwordx4 v162, s[46:47]
	s_mov_b32 m0, s34
	s_nop 0
	s_mov_b32 s34, m0
	s_mov_b32 m0, s48
	s_nop 2
	global_load_lds_dwordx4 v163, s[46:47]
	s_mov_b32 m0, s34
	s_nop 0
	s_mov_b32 s34, m0
	s_mov_b32 m0, s2
	s_nop 2
	global_load_lds_dwordx4 v164, s[58:59]
	s_mov_b32 m0, s34
	s_nop 0
	s_mov_b32 s34, m0
	s_mov_b32 m0, s49
	s_nop 2
	global_load_lds_dwordx4 v165, s[58:59]
	s_mov_b32 m0, s34
	s_cmp_lg_u32 s80, -2
	s_cbranch_scc1 .Lz8_b
	v_mov_b32_e32 v60, 0
	v_mov_b32_e32 v61, 0
	v_pk_mov_b32 v[62:63], v[60:61], v[60:61]
	v_pk_mov_b32 v[56:57], v[60:61], v[60:61]
	v_pk_mov_b32 v[58:59], v[60:61], v[60:61]
	v_pk_mov_b32 v[44:45], v[60:61], v[60:61]
	v_pk_mov_b32 v[46:47], v[60:61], v[60:61]
	v_pk_mov_b32 v[40:41], v[60:61], v[60:61]
	v_pk_mov_b32 v[42:43], v[60:61], v[60:61]
	v_pk_mov_b32 v[24:25], v[60:61], v[60:61]
	v_pk_mov_b32 v[26:27], v[60:61], v[60:61]
	v_pk_mov_b32 v[12:13], v[60:61], v[60:61]
	v_pk_mov_b32 v[14:15], v[60:61], v[60:61]
	v_pk_mov_b32 v[4:5], v[60:61], v[60:61]
	v_pk_mov_b32 v[6:7], v[60:61], v[60:61]
	v_pk_mov_b32 v[0:1], v[60:61], v[60:61]
	v_pk_mov_b32 v[2:3], v[60:61], v[60:61]
	v_pk_mov_b32 v[52:53], v[60:61], v[60:61]
	v_pk_mov_b32 v[54:55], v[60:61], v[60:61]
	v_pk_mov_b32 v[48:49], v[60:61], v[60:61]
	v_pk_mov_b32 v[50:51], v[60:61], v[60:61]
	v_pk_mov_b32 v[28:29], v[60:61], v[60:61]
	v_pk_mov_b32 v[30:31], v[60:61], v[60:61]
	v_pk_mov_b32 v[20:21], v[60:61], v[60:61]
	v_pk_mov_b32 v[22:23], v[60:61], v[60:61]
	v_pk_mov_b32 v[36:37], v[60:61], v[60:61]
	v_pk_mov_b32 v[38:39], v[60:61], v[60:61]
	v_pk_mov_b32 v[32:33], v[60:61], v[60:61]
	v_pk_mov_b32 v[34:35], v[60:61], v[60:61]
	v_pk_mov_b32 v[16:17], v[60:61], v[60:61]
	v_pk_mov_b32 v[18:19], v[60:61], v[60:61]
	v_pk_mov_b32 v[8:9], v[60:61], v[60:61]
	v_pk_mov_b32 v[10:11], v[60:61], v[60:61]
.Lz8_b:
	s_waitcnt vmcnt(8)
	s_waitcnt lgkmcnt(0)
	s_cmp_le_i32 s42, s32
	s_cbranch_scc1 .Lp8_ragskip_1
	s_barrier
	s_setprio 1
	s_waitcnt lgkmcnt(6)
	v_mfma_scale_f32_16x16x128_f8f6f4 v[60:63], v[128:135], v[64:71], v[60:63], v169, v169 op_sel_hi:[0,0,0]
	v_mfma_scale_f32_16x16x128_f8f6f4 v[56:59], v[136:143], v[64:71], v[56:59], v169, v169 op_sel_hi:[0,0,0]
	s_waitcnt lgkmcnt(4)
	v_mfma_scale_f32_16x16x128_f8f6f4 v[188:191], v[128:135], v[72:79], v[44:47], v169, v169 op_sel_hi:[0,0,0]
	v_mfma_scale_f32_16x16x128_f8f6f4 v[192:195], v[136:143], v[72:79], v[40:43], v169, v169 op_sel_hi:[0,0,0]
	s_waitcnt lgkmcnt(2)
	v_mfma_scale_f32_16x16x128_f8f6f4 v[196:199], v[128:135], v[80:87], v[24:27], v169, v169 op_sel_hi:[0,0,0]
	v_mfma_scale_f32_16x16x128_f8f6f4 v[200:203], v[136:143], v[80:87], v[12:15], v169, v169 op_sel_hi:[0,0,0]
	s_waitcnt lgkmcnt(0)
	v_mfma_scale_f32_16x16x128_f8f6f4 v[220:223], v[128:135], v[88:95], v[4:7], v169, v169 op_sel_hi:[0,0,0]
	v_mfma_scale_f32_16x16x128_f8f6f4 v[224:227], v[136:143], v[88:95], v[0:3], v169, v169 op_sel_hi:[0,0,0]
	s_setprio 0
	s_setprio 1
	v_mfma_scale_f32_16x16x128_f8f6f4 v[52:55], v[144:151], v[64:71], v[52:55], v169, v169 op_sel_hi:[0,0,0]
	v_mfma_scale_f32_16x16x128_f8f6f4 v[48:51], v[152:159], v[64:71], v[48:51], v169, v169 op_sel_hi:[0,0,0]
	v_mfma_scale_f32_16x16x128_f8f6f4 v[228:231], v[144:151], v[72:79], v[28:31], v169, v169 op_sel_hi:[0,0,0]
	v_mfma_scale_f32_16x16x128_f8f6f4 v[232:235], v[152:159], v[72:79], v[20:23], v169, v169 op_sel_hi:[0,0,0]
	v_mfma_scale_f32_16x16x128_f8f6f4 v[236:239], v[144:151], v[80:87], v[36:39], v169, v169 op_sel_hi:[0,0,0]
	v_mfma_scale_f32_16x16x128_f8f6f4 v[240:243], v[152:159], v[80:87], v[32:35], v169, v169 op_sel_hi:[0,0,0]
	v_mfma_scale_f32_16x16x128_f8f6f4 v[244:247], v[144:151], v[88:95], v[16:19], v169, v169 op_sel_hi:[0,0,0]
	v_mfma_scale_f32_16x16x128_f8f6f4 v[248:251], v[152:159], v[88:95], v[8:11], v169, v169 op_sel_hi:[0,0,0]
	s_setprio 0
.Lp8_rag_1:
	s_barrier
	ds_read_b128 v[0:3], v170
	ds_read_b128 v[4:7], v170 offset:1024
	s_nop 1
	ds_read_b128 v[16:19], v170 offset:2048
	ds_read_b128 v[20:23], v170 offset:3072
	ds_read_b128 v[128:131], v171
	ds_read_b128 v[132:135], v171 offset:1024
	ds_read_b128 v[136:139], v171 offset:2048
	ds_read_b128 v[140:143], v171 offset:3072
	ds_read_b128 v[8:11], v168 offset:32768
	ds_read_b128 v[12:15], v168 offset:33792
	ds_read_b128 v[24:27], v168 offset:34816
	ds_read_b128 v[28:31], v168 offset:35840
	ds_read_b128 v[32:35], v168 offset:36864
	ds_read_b128 v[36:39], v168 offset:37888
	ds_read_b128 v[40:43], v168 offset:38912
	ds_read_b128 v[44:47], v168 offset:39936
	s_add_u32 s34, s58, 0x40000
	s_addc_u32 s35, s59, 0
	s_mov_b32 s58, m0
	s_mov_b32 m0, s52
	s_nop 2
	global_load_lds_dwordx4 v164, s[34:35]
	s_mov_b32 m0, s58
	s_nop 0
	s_mov_b32 s58, m0
	s_mov_b32 m0, s53
	s_nop 2
	global_load_lds_dwordx4 v165, s[34:35]
	s_mov_b32 m0, s58
	s_waitcnt vmcnt(8)
	s_waitcnt lgkmcnt(0)
	s_setprio 1
	s_barrier
	v_mfma_scale_f32_16x16x128_f8f6f4 v[124:127], v[0:7], v[8:15], v[124:127], v169, v169 op_sel_hi:[0,0,0]
	v_mfma_scale_f32_16x16x128_f8f6f4 v[120:123], v[16:23], v[8:15], v[120:123], v169, v169 op_sel_hi:[0,0,0]
	v_mfma_scale_f32_16x16x128_f8f6f4 v[108:111], v[0:7], v[24:31], v[108:111], v169, v169 op_sel_hi:[0,0,0]
	v_mfma_scale_f32_16x16x128_f8f6f4 v[104:107], v[16:23], v[24:31], v[104:107], v169, v169 op_sel_hi:[0,0,0]
	v_mfma_scale_f32_16x16x128_f8f6f4 v[92:95], v[0:7], v[32:39], v[204:207], v169, v169 op_sel_hi:[0,0,0]
	v_mfma_scale_f32_16x16x128_f8f6f4 v[88:91], v[16:23], v[32:39], v[208:211], v169, v169 op_sel_hi:[0,0,0]
	v_mfma_scale_f32_16x16x128_f8f6f4 v[76:79], v[0:7], v[40:47], v[212:215], v169, v169 op_sel_hi:[0,0,0]
	v_mfma_scale_f32_16x16x128_f8f6f4 v[72:75], v[16:23], v[40:47], v[216:219], v169, v169 op_sel_hi:[0,0,0]
	s_setprio 0
	s_setprio 1
	v_mfma_scale_f32_16x16x128_f8f6f4 v[116:119], v[128:135], v[8:15], v[116:119], v169, v169 op_sel_hi:[0,0,0]
	v_mfma_scale_f32_16x16x128_f8f6f4 v[112:115], v[136:143], v[8:15], v[112:115], v169, v169 op_sel_hi:[0,0,0]
	v_mfma_scale_f32_16x16x128_f8f6f4 v[100:103], v[128:135], v[24:31], v[100:103], v169, v169 op_sel_hi:[0,0,0]
	v_mfma_scale_f32_16x16x128_f8f6f4 v[96:99], v[136:143], v[24:31], v[96:99], v169, v169 op_sel_hi:[0,0,0]
	v_mfma_scale_f32_16x16x128_f8f6f4 v[84:87], v[128:135], v[32:39], v[172:175], v169, v169 op_sel_hi:[0,0,0]
	v_mfma_scale_f32_16x16x128_f8f6f4 v[80:83], v[136:143], v[32:39], v[176:179], v169, v169 op_sel_hi:[0,0,0]
	v_mfma_scale_f32_16x16x128_f8f6f4 v[68:71], v[128:135], v[40:47], v[180:183], v169, v169 op_sel_hi:[0,0,0]
	v_mfma_scale_f32_16x16x128_f8f6f4 v[64:67], v[136:143], v[40:47], v[184:187], v169, v169 op_sel_hi:[0,0,0]
	s_setprio 0
	s_barrier
	ds_read_b128 v[28:31], v168 offset:49152
	ds_read_b128 v[32:35], v168 offset:50176
	ds_read_b128 v[144:147], v168 offset:51200
	ds_read_b128 v[148:151], v168 offset:52224
	ds_read_b128 v[152:155], v168 offset:53248
	ds_read_b128 v[156:159], v168 offset:54272
	ds_read_b128 v[172:175], v168 offset:55296
	ds_read_b128 v[176:179], v168 offset:56320
	s_mov_b32 s34, m0
	s_mov_b32 m0, s54
	s_nop 2
	global_load_lds_dwordx4 v162, s[56:57]
	s_mov_b32 m0, s34
	s_nop 0
	s_mov_b32 s34, m0
	s_mov_b32 m0, s55
	s_nop 2
	global_load_lds_dwordx4 v163, s[56:57]
	s_mov_b32 m0, s34
	s_add_u32 s34, s46, 0x80
	s_addc_u32 s35, s47, 0
	s_mov_b32 s46, m0
	s_mov_b32 m0, s64
	s_nop 2
	global_load_lds_dwordx4 v162, s[34:35]
	s_mov_b32 m0, s46
	s_nop 0
	s_mov_b32 s46, m0
	s_mov_b32 m0, s65
	s_nop 2
	global_load_lds_dwordx4 v163, s[34:35]
	s_mov_b32 m0, s46
	s_mov_b32 s34, m0
	s_mov_b32 m0, s62
	s_nop 2
	global_load_lds_dwordx4 v164, s[50:51]
	s_mov_b32 m0, s34
	s_nop 0
	s_mov_b32 s34, m0
	s_mov_b32 m0, s63
	s_nop 2
	global_load_lds_dwordx4 v165, s[50:51]
	s_mov_b32 m0, s34
	s_waitcnt vmcnt(8)
	s_waitcnt lgkmcnt(0)
	s_cmp_le_i32 s42, s32
	s_cbranch_scc1 .Lp8_ragskip_3
	s_barrier
	s_setprio 1
	s_waitcnt lgkmcnt(6)
	v_mfma_scale_f32_16x16x128_f8f6f4 v[60:63], v[0:7], v[28:35], v[60:63], v169, v169 op_sel_hi:[0,0,0]
	v_mfma_scale_f32_16x16x128_f8f6f4 v[56:59], v[16:23], v[28:35], v[56:59], v169, v169 op_sel_hi:[0,0,0]
	s_waitcnt lgkmcnt(4)
	v_mfma_scale_f32_16x16x128_f8f6f4 v[44:47], v[0:7], v[144:151], v[188:191], v169, v169 op_sel_hi:[0,0,0]
	v_mfma_scale_f32_16x16x128_f8f6f4 v[40:43], v[16:23], v[144:151], v[192:195], v169, v169 op_sel_hi:[0,0,0]
	s_waitcnt lgkmcnt(2)
	v_mfma_scale_f32_16x16x128_f8f6f4 v[24:27], v[0:7], v[152:159], v[196:199], v169, v169 op_sel_hi:[0,0,0]
	v_mfma_scale_f32_16x16x128_f8f6f4 v[12:15], v[16:23], v[152:159], v[200:203], v169, v169 op_sel_hi:[0,0,0]
	s_waitcnt lgkmcnt(0)
	v_mfma_scale_f32_16x16x128_f8f6f4 v[4:7], v[0:7], v[172:179], v[220:223], v169, v169 op_sel_hi:[0,0,0]
	v_mfma_scale_f32_16x16x128_f8f6f4 v[0:3], v[16:23], v[172:179], v[224:227], v169, v169 op_sel_hi:[0,0,0]
	s_setprio 0
	s_setprio 1
	v_mfma_scale_f32_16x16x128_f8f6f4 v[52:55], v[128:135], v[28:35], v[52:55], v169, v169 op_sel_hi:[0,0,0]
	v_mfma_scale_f32_16x16x128_f8f6f4 v[48:51], v[136:143], v[28:35], v[48:51], v169, v169 op_sel_hi:[0,0,0]
	v_mfma_scale_f32_16x16x128_f8f6f4 v[28:31], v[128:135], v[144:151], v[228:231], v169, v169 op_sel_hi:[0,0,0]
	v_mfma_scale_f32_16x16x128_f8f6f4 v[20:23], v[136:143], v[144:151], v[232:235], v169, v169 op_sel_hi:[0,0,0]
	v_mfma_scale_f32_16x16x128_f8f6f4 v[36:39], v[128:135], v[152:159], v[236:239], v169, v169 op_sel_hi:[0,0,0]
	v_mfma_scale_f32_16x16x128_f8f6f4 v[32:35], v[136:143], v[152:159], v[240:243], v169, v169 op_sel_hi:[0,0,0]
	v_mfma_scale_f32_16x16x128_f8f6f4 v[16:19], v[128:135], v[172:179], v[244:247], v169, v169 op_sel_hi:[0,0,0]
	v_mfma_scale_f32_16x16x128_f8f6f4 v[8:11], v[136:143], v[172:179], v[248:251], v169, v169 op_sel_hi:[0,0,0]
	s_setprio 0

.LBB0_1186:
	ds_read_b128 v[0:3], v134
	ds_read_b128 v[4:7], v134 offset:1024
	ds_read_b128 v[8:11], v134 offset:2048
	ds_read_b128 v[12:15], v134 offset:3072
	ds_read_b128 v[16:19], v136
	ds_read_b128 v[20:23], v136 offset:1024
	ds_read_b128 v[24:27], v136 offset:2048
	ds_read_b128 v[28:31], v136 offset:3072
	s_and_b64 s[24:25], s[18:19], exec
	s_cselect_b32 s27, s13, s21
	s_cselect_b32 s26, s12, s20
	s_cselect_b32 s29, s15, s31
	s_cselect_b32 s28, s14, s30
	s_cselect_b32 s25, s17, s23
	s_cselect_b32 s24, s16, s22
	s_add_u32 s36, s20, 0x100
	s_addc_u32 s37, s21, 0
	s_add_u32 s46, s30, 0x100
	s_addc_u32 s47, s31, 0
	s_add_u32 s40, s22, 0x100
	s_addc_u32 s41, s23, 0
	s_add_u32 s34, s30, 0x180
	s_addc_u32 s35, s31, 0
	s_add_u32 s30, s20, 0x180
	s_addc_u32 s31, s21, 0
	ds_read_b128 v[32:35], v137
	ds_read_b128 v[36:39], v137 offset:1024
	ds_read_b128 v[40:43], v137 offset:2048
	ds_read_b128 v[44:47], v137 offset:3072
	ds_read_b128 v[48:51], v137 offset:4096
	ds_read_b128 v[52:55], v137 offset:5120
	ds_read_b128 v[56:59], v137 offset:6144
	ds_read_b128 v[60:63], v137 offset:7168
	s_add_u32 s74, s20, 0x10080
	s_addc_u32 s75, s21, 0
	s_mov_b32 s73, m0
	s_mov_b32 m0, s62
	s_nop 2
	global_load_lds_dwordx4 v132, s[74:75]
	s_mov_b32 m0, s73
	s_nop 0
	s_mov_b32 s73, m0
	s_mov_b32 m0, s63
	s_nop 2
	global_load_lds_dwordx4 v133, s[74:75]
	s_mov_b32 m0, s73
	s_waitcnt vmcnt(8)
	s_waitcnt lgkmcnt(0)
	s_setprio 1
	s_barrier
	v_mfma_f32_16x16x32_bf16 v[64:67], v[0:3], v[32:35], 0
	v_mfma_f32_16x16x32_bf16 v[68:71], v[8:11], v[32:35], 0
	v_mfma_f32_16x16x32_bf16 v[72:75], v[0:3], v[40:43], 0
	v_mfma_f32_16x16x32_bf16 v[76:79], v[8:11], v[40:43], 0
	v_mfma_f32_16x16x32_bf16 v[80:83], v[0:3], v[48:51], 0
	v_mfma_f32_16x16x32_bf16 v[84:87], v[8:11], v[48:51], 0
	v_mfma_f32_16x16x32_bf16 v[88:91], v[0:3], v[56:59], 0
	v_mfma_f32_16x16x32_bf16 v[92:95], v[8:11], v[56:59], 0
	v_mfma_f32_16x16x32_bf16 v[64:67], v[4:7], v[36:39], v[64:67]
	v_mfma_f32_16x16x32_bf16 v[68:71], v[12:15], v[36:39], v[68:71]
	v_mfma_f32_16x16x32_bf16 v[72:75], v[4:7], v[44:47], v[72:75]
	v_mfma_f32_16x16x32_bf16 v[76:79], v[12:15], v[44:47], v[76:79]
	v_mfma_f32_16x16x32_bf16 v[80:83], v[4:7], v[52:55], v[80:83]
	v_mfma_f32_16x16x32_bf16 v[84:87], v[12:15], v[52:55], v[84:87]
	v_mfma_f32_16x16x32_bf16 v[88:91], v[4:7], v[60:63], v[88:91]
	v_mfma_f32_16x16x32_bf16 v[92:95], v[12:15], v[60:63], v[92:95]
	s_setprio 0
	s_setprio 1
	v_mfma_f32_16x16x32_bf16 v[96:99], v[16:19], v[32:35], 0
	v_mfma_f32_16x16x32_bf16 v[32:35], v[24:27], v[32:35], 0
	v_mfma_f32_16x16x32_bf16 v[96:99], v[20:23], v[36:39], v[96:99]
	v_mfma_f32_16x16x32_bf16 v[32:35], v[28:31], v[36:39], v[32:35]
	v_mfma_f32_16x16x32_bf16 v[36:39], v[16:19], v[40:43], 0
	v_mfma_f32_16x16x32_bf16 v[40:43], v[24:27], v[40:43], 0
	v_mfma_f32_16x16x32_bf16 v[36:39], v[20:23], v[44:47], v[36:39]
	v_mfma_f32_16x16x32_bf16 v[40:43], v[28:31], v[44:47], v[40:43]
	v_mfma_f32_16x16x32_bf16 v[44:47], v[16:19], v[48:51], 0
	v_mfma_f32_16x16x32_bf16 v[48:51], v[24:27], v[48:51], 0
	v_mfma_f32_16x16x32_bf16 v[44:47], v[20:23], v[52:55], v[44:47]
	v_mfma_f32_16x16x32_bf16 v[48:51], v[28:31], v[52:55], v[48:51]
	v_mfma_f32_16x16x32_bf16 v[52:55], v[16:19], v[56:59], 0
	v_mfma_f32_16x16x32_bf16 v[56:59], v[24:27], v[56:59], 0
	v_mfma_f32_16x16x32_bf16 v[52:55], v[20:23], v[60:63], v[52:55]
	v_mfma_f32_16x16x32_bf16 v[56:59], v[28:31], v[60:63], v[56:59]
	s_setprio 0
	s_barrier
	ds_read_b128 v[60:63], v137 offset:16384
	ds_read_b128 v[100:103], v137 offset:17408
	ds_read_b128 v[104:107], v137 offset:18432
	ds_read_b128 v[108:111], v137 offset:19456
	ds_read_b128 v[112:115], v137 offset:20480
	ds_read_b128 v[116:119], v137 offset:21504
	ds_read_b128 v[120:123], v137 offset:22528
	ds_read_b128 v[124:127], v137 offset:23552
	s_mov_b32 s73, m0
	s_mov_b32 m0, s49
	s_nop 2
	global_load_lds_dwordx4 v130, s[46:47]
	s_mov_b32 m0, s73
	s_nop 0
	s_mov_b32 s73, m0
	s_mov_b32 m0, s50
	s_nop 2
	global_load_lds_dwordx4 v131, s[46:47]
	s_mov_b32 m0, s73
	s_mov_b32 s46, m0
	s_mov_b32 m0, s51
	s_nop 2
	global_load_lds_dwordx4 v130, s[40:41]
	s_mov_b32 m0, s46
	s_nop 0
	s_mov_b32 s46, m0
	s_mov_b32 m0, s52
	s_nop 2
	global_load_lds_dwordx4 v131, s[40:41]
	s_mov_b32 m0, s46
	s_mov_b32 s40, m0
	s_mov_b32 m0, s2
	s_nop 2
	global_load_lds_dwordx4 v132, s[36:37]
	s_mov_b32 m0, s40
	s_nop 0
	s_mov_b32 s40, m0
	s_mov_b32 m0, s53
	s_nop 2
	global_load_lds_dwordx4 v133, s[36:37]
	s_mov_b32 m0, s40
	s_waitcnt vmcnt(8)
	s_waitcnt lgkmcnt(0)
	s_setprio 1
	s_barrier
	v_mfma_f32_16x16x32_bf16 v[140:143], v[0:3], v[60:63], 0
	v_mfma_f32_16x16x32_bf16 v[148:151], v[0:3], v[104:107], 0
	v_mfma_f32_16x16x32_bf16 v[156:159], v[0:3], v[112:115], 0
	v_mfma_f32_16x16x32_bf16 v[0:3], v[0:3], v[120:123], 0
	v_mfma_f32_16x16x32_bf16 v[140:143], v[4:7], v[100:103], v[140:143]
	v_mfma_f32_16x16x32_bf16 v[148:151], v[4:7], v[108:111], v[148:151]
	v_mfma_f32_16x16x32_bf16 v[156:159], v[4:7], v[116:119], v[156:159]
	v_mfma_f32_16x16x32_bf16 v[0:3], v[4:7], v[124:127], v[0:3]
	v_mfma_f32_16x16x32_bf16 v[4:7], v[8:11], v[120:123], 0
	v_mfma_f32_16x16x32_bf16 v[144:147], v[8:11], v[60:63], 0
	v_mfma_f32_16x16x32_bf16 v[152:155], v[8:11], v[104:107], 0
	v_mfma_f32_16x16x32_bf16 v[160:163], v[8:11], v[112:115], 0
	v_mfma_f32_16x16x32_bf16 v[4:7], v[12:15], v[124:127], v[4:7]
	v_mfma_f32_16x16x32_bf16 v[144:147], v[12:15], v[100:103], v[144:147]
	v_mfma_f32_16x16x32_bf16 v[152:155], v[12:15], v[108:111], v[152:155]
	v_mfma_f32_16x16x32_bf16 v[160:163], v[12:15], v[116:119], v[160:163]
	s_setprio 0
	s_setprio 1
	v_mfma_f32_16x16x32_bf16 v[8:11], v[16:19], v[60:63], 0
	v_mfma_f32_16x16x32_bf16 v[12:15], v[24:27], v[60:63], 0
	v_mfma_f32_16x16x32_bf16 v[8:11], v[20:23], v[100:103], v[8:11]
	v_mfma_f32_16x16x32_bf16 v[12:15], v[28:31], v[100:103], v[12:15]
	v_mfma_f32_16x16x32_bf16 v[60:63], v[16:19], v[104:107], 0
	v_mfma_f32_16x16x32_bf16 v[100:103], v[24:27], v[104:107], 0
	v_mfma_f32_16x16x32_bf16 v[104:107], v[16:19], v[112:115], 0
	v_mfma_f32_16x16x32_bf16 v[16:19], v[16:19], v[120:123], 0
	v_mfma_f32_16x16x32_bf16 v[60:63], v[20:23], v[108:111], v[60:63]
	v_mfma_f32_16x16x32_bf16 v[100:103], v[28:31], v[108:111], v[100:103]
	v_mfma_f32_16x16x32_bf16 v[104:107], v[20:23], v[116:119], v[104:107]
	v_mfma_f32_16x16x32_bf16 v[108:111], v[24:27], v[112:115], 0
	v_mfma_f32_16x16x32_bf16 v[16:19], v[20:23], v[124:127], v[16:19]
	v_mfma_f32_16x16x32_bf16 v[20:23], v[24:27], v[120:123], 0
	v_mfma_f32_16x16x32_bf16 v[108:111], v[28:31], v[116:119], v[108:111]
	v_mfma_f32_16x16x32_bf16 v[20:23], v[28:31], v[124:127], v[20:23]
	s_setprio 0
	s_barrier
	ds_read_b128 v[24:27], v138
	ds_read_b128 v[28:31], v138 offset:1024
	ds_read_b128 v[112:115], v138 offset:2048
	ds_read_b128 v[116:119], v138 offset:3072
	ds_read_b128 v[120:123], v139
	ds_read_b128 v[124:127], v139 offset:1024
	ds_read_b128 v[164:167], v139 offset:2048
	ds_read_b128 v[168:171], v139 offset:3072
	ds_read_b128 v[172:175], v137 offset:32768
	ds_read_b128 v[176:179], v137 offset:33792
	ds_read_b128 v[180:183], v137 offset:34816
	ds_read_b128 v[184:187], v137 offset:35840
	ds_read_b128 v[188:191], v137 offset:36864
	ds_read_b128 v[192:195], v137 offset:37888
	ds_read_b128 v[196:199], v137 offset:38912
	ds_read_b128 v[200:203], v137 offset:39936
	s_add_u32 s36, s20, 0x10100
	s_addc_u32 s37, s21, 0
	s_mov_b32 s40, m0
	s_mov_b32 m0, s54
	s_nop 2
	global_load_lds_dwordx4 v132, s[36:37]
	s_mov_b32 m0, s40
	s_nop 0
	s_mov_b32 s40, m0
	s_mov_b32 m0, s55
	s_nop 2
	global_load_lds_dwordx4 v133, s[36:37]
	s_mov_b32 m0, s40
	s_waitcnt vmcnt(8)
	s_waitcnt lgkmcnt(0)
	s_setprio 1
	s_barrier
	v_mfma_f32_16x16x32_bf16 v[64:67], v[24:27], v[172:175], v[64:67]
	v_mfma_f32_16x16x32_bf16 v[68:71], v[112:115], v[172:175], v[68:71]
	v_mfma_f32_16x16x32_bf16 v[72:75], v[24:27], v[180:183], v[72:75]
	v_mfma_f32_16x16x32_bf16 v[76:79], v[112:115], v[180:183], v[76:79]
	v_mfma_f32_16x16x32_bf16 v[80:83], v[24:27], v[188:191], v[80:83]
	v_mfma_f32_16x16x32_bf16 v[84:87], v[112:115], v[188:191], v[84:87]
	v_mfma_f32_16x16x32_bf16 v[88:91], v[24:27], v[196:199], v[88:91]
	v_mfma_f32_16x16x32_bf16 v[92:95], v[112:115], v[196:199], v[92:95]
	v_mfma_f32_16x16x32_bf16 v[64:67], v[28:31], v[176:179], v[64:67]
	v_mfma_f32_16x16x32_bf16 v[68:71], v[116:119], v[176:179], v[68:71]
	v_mfma_f32_16x16x32_bf16 v[72:75], v[28:31], v[184:187], v[72:75]
	v_mfma_f32_16x16x32_bf16 v[76:79], v[116:119], v[184:187], v[76:79]
	v_mfma_f32_16x16x32_bf16 v[80:83], v[28:31], v[192:195], v[80:83]
	v_mfma_f32_16x16x32_bf16 v[84:87], v[116:119], v[192:195], v[84:87]
	v_mfma_f32_16x16x32_bf16 v[88:91], v[28:31], v[200:203], v[88:91]
	v_mfma_f32_16x16x32_bf16 v[92:95], v[116:119], v[200:203], v[92:95]
	s_setprio 0
	s_setprio 1
	v_mfma_f32_16x16x32_bf16 v[96:99], v[120:123], v[172:175], v[96:99]
	v_mfma_f32_16x16x32_bf16 v[32:35], v[164:167], v[172:175], v[32:35]
	v_mfma_f32_16x16x32_bf16 v[36:39], v[120:123], v[180:183], v[36:39]
	v_mfma_f32_16x16x32_bf16 v[40:43], v[164:167], v[180:183], v[40:43]
	v_mfma_f32_16x16x32_bf16 v[44:47], v[120:123], v[188:191], v[44:47]
	v_mfma_f32_16x16x32_bf16 v[48:51], v[164:167], v[188:191], v[48:51]
	v_mfma_f32_16x16x32_bf16 v[52:55], v[120:123], v[196:199], v[52:55]
	v_mfma_f32_16x16x32_bf16 v[56:59], v[164:167], v[196:199], v[56:59]
	v_mfma_f32_16x16x32_bf16 v[96:99], v[124:127], v[176:179], v[96:99]
	v_mfma_f32_16x16x32_bf16 v[32:35], v[168:171], v[176:179], v[32:35]
	v_mfma_f32_16x16x32_bf16 v[36:39], v[124:127], v[184:187], v[36:39]
	v_mfma_f32_16x16x32_bf16 v[40:43], v[168:171], v[184:187], v[40:43]
	v_mfma_f32_16x16x32_bf16 v[44:47], v[124:127], v[192:195], v[44:47]
	v_mfma_f32_16x16x32_bf16 v[48:51], v[168:171], v[192:195], v[48:51]
	v_mfma_f32_16x16x32_bf16 v[52:55], v[124:127], v[200:203], v[52:55]
	v_mfma_f32_16x16x32_bf16 v[56:59], v[168:171], v[200:203], v[56:59]
	s_setprio 0
	s_barrier
	ds_read_b128 v[172:175], v137 offset:49152
	ds_read_b128 v[176:179], v137 offset:50176
	ds_read_b128 v[180:183], v137 offset:51200
	ds_read_b128 v[184:187], v137 offset:52224
	ds_read_b128 v[188:191], v137 offset:53248
	ds_read_b128 v[192:195], v137 offset:54272
	ds_read_b128 v[196:199], v137 offset:55296
	ds_read_b128 v[200:203], v137 offset:56320
	s_mov_b32 s36, m0
	s_mov_b32 m0, s56
	s_nop 2
	global_load_lds_dwordx4 v130, s[34:35]
	s_mov_b32 m0, s36
	s_add_u32 s22, s22, 0x180
	s_mov_b32 s36, m0
	s_mov_b32 m0, s57
	s_nop 2
	global_load_lds_dwordx4 v131, s[34:35]
	s_mov_b32 m0, s36
	s_addc_u32 s23, s23, 0
	s_mov_b32 s34, m0
	s_mov_b32 m0, s60
	s_nop 2
	global_load_lds_dwordx4 v130, s[22:23]
	s_mov_b32 m0, s34
	s_nop 0
	s_mov_b32 s34, m0
	s_mov_b32 m0, s61
	s_nop 2
	global_load_lds_dwordx4 v131, s[22:23]
	s_mov_b32 m0, s34
	s_mov_b32 s22, m0
	s_mov_b32 m0, s58
	s_nop 2
	global_load_lds_dwordx4 v132, s[30:31]
	s_mov_b32 m0, s22
	s_nop 0
	s_mov_b32 s22, m0
	s_mov_b32 m0, s59
	s_nop 2
	global_load_lds_dwordx4 v133, s[30:31]
	s_mov_b32 m0, s22
	s_waitcnt vmcnt(8)
	s_waitcnt lgkmcnt(0)
	s_setprio 1
	s_barrier
	v_mfma_f32_16x16x32_bf16 v[0:3], v[24:27], v[196:199], v[0:3]
	v_mfma_f32_16x16x32_bf16 v[4:7], v[112:115], v[196:199], v[4:7]
	v_mfma_f32_16x16x32_bf16 v[140:143], v[24:27], v[172:175], v[140:143]
	v_mfma_f32_16x16x32_bf16 v[144:147], v[112:115], v[172:175], v[144:147]
	v_mfma_f32_16x16x32_bf16 v[148:151], v[24:27], v[180:183], v[148:151]
	v_mfma_f32_16x16x32_bf16 v[152:155], v[112:115], v[180:183], v[152:155]
	v_mfma_f32_16x16x32_bf16 v[156:159], v[24:27], v[188:191], v[156:159]
	v_mfma_f32_16x16x32_bf16 v[160:163], v[112:115], v[188:191], v[160:163]
	v_mfma_f32_16x16x32_bf16 v[0:3], v[28:31], v[200:203], v[0:3]
	v_mfma_f32_16x16x32_bf16 v[4:7], v[116:119], v[200:203], v[4:7]
	v_mfma_f32_16x16x32_bf16 v[140:143], v[28:31], v[176:179], v[140:143]
	v_mfma_f32_16x16x32_bf16 v[144:147], v[116:119], v[176:179], v[144:147]
	v_mfma_f32_16x16x32_bf16 v[148:151], v[28:31], v[184:187], v[148:151]
	v_mfma_f32_16x16x32_bf16 v[152:155], v[116:119], v[184:187], v[152:155]
	v_mfma_f32_16x16x32_bf16 v[156:159], v[28:31], v[192:195], v[156:159]
	v_mfma_f32_16x16x32_bf16 v[160:163], v[116:119], v[192:195], v[160:163]
	s_setprio 0
	s_setprio 1
	v_mfma_f32_16x16x32_bf16 v[8:11], v[120:123], v[172:175], v[8:11]
	v_mfma_f32_16x16x32_bf16 v[12:15], v[164:167], v[172:175], v[12:15]
	v_mfma_f32_16x16x32_bf16 v[24:27], v[120:123], v[180:183], v[60:63]
	v_mfma_f32_16x16x32_bf16 v[28:31], v[164:167], v[180:183], v[100:103]
	v_mfma_f32_16x16x32_bf16 v[60:63], v[120:123], v[188:191], v[104:107]
	v_mfma_f32_16x16x32_bf16 v[100:103], v[164:167], v[188:191], v[108:111]
	v_mfma_f32_16x16x32_bf16 v[16:19], v[120:123], v[196:199], v[16:19]
	v_mfma_f32_16x16x32_bf16 v[20:23], v[164:167], v[196:199], v[20:23]
	v_mfma_f32_16x16x32_bf16 v[8:11], v[124:127], v[176:179], v[8:11]
	v_mfma_f32_16x16x32_bf16 v[12:15], v[168:171], v[176:179], v[12:15]
	v_mfma_f32_16x16x32_bf16 v[24:27], v[124:127], v[184:187], v[24:27]
	v_mfma_f32_16x16x32_bf16 v[28:31], v[168:171], v[184:187], v[28:31]
	v_mfma_f32_16x16x32_bf16 v[60:63], v[124:127], v[192:195], v[60:63]
	v_mfma_f32_16x16x32_bf16 v[100:103], v[168:171], v[192:195], v[100:103]
	v_mfma_f32_16x16x32_bf16 v[16:19], v[124:127], v[200:203], v[16:19]
	v_mfma_f32_16x16x32_bf16 v[20:23], v[168:171], v[200:203], v[20:23]
	s_setprio 0
	s_barrier
	ds_read_b128 v[104:107], v134
	ds_read_b128 v[108:111], v134 offset:1024
	ds_read_b128 v[112:115], v134 offset:2048
	ds_read_b128 v[116:119], v134 offset:3072
	ds_read_b128 v[120:123], v136
	ds_read_b128 v[124:127], v136 offset:1024
	ds_read_b128 v[164:167], v136 offset:2048
	ds_read_b128 v[168:171], v136 offset:3072
	s_add_u32 s30, s28, 0x80
	s_addc_u32 s31, s29, 0
	s_add_u32 s22, s26, 0x80
	s_addc_u32 s23, s27, 0
	ds_read_b128 v[172:175], v137
	ds_read_b128 v[176:179], v137 offset:1024
	ds_read_b128 v[180:183], v137 offset:2048
	ds_read_b128 v[184:187], v137 offset:3072
	ds_read_b128 v[188:191], v137 offset:4096
	ds_read_b128 v[192:195], v137 offset:5120
	ds_read_b128 v[196:199], v137 offset:6144
	ds_read_b128 v[200:203], v137 offset:7168
	s_add_u32 s20, s20, 0x10180
	s_addc_u32 s21, s21, 0
	s_mov_b32 s34, m0
	s_mov_b32 m0, s62
	s_nop 2
	global_load_lds_dwordx4 v132, s[20:21]
	s_mov_b32 m0, s34
	s_nop 0
	s_mov_b32 s34, m0
	s_mov_b32 m0, s63
	s_nop 2
	global_load_lds_dwordx4 v133, s[20:21]
	s_mov_b32 m0, s34
	s_waitcnt vmcnt(8)
	s_waitcnt lgkmcnt(0)
	s_setprio 1
	s_barrier
	v_mfma_f32_16x16x32_bf16 v[88:91], v[104:107], v[196:199], v[88:91]
	v_mfma_f32_16x16x32_bf16 v[64:67], v[104:107], v[172:175], v[64:67]
	v_mfma_f32_16x16x32_bf16 v[68:71], v[112:115], v[172:175], v[68:71]
	v_mfma_f32_16x16x32_bf16 v[72:75], v[104:107], v[180:183], v[72:75]
	v_mfma_f32_16x16x32_bf16 v[76:79], v[112:115], v[180:183], v[76:79]
	v_mfma_f32_16x16x32_bf16 v[80:83], v[104:107], v[188:191], v[80:83]
	v_mfma_f32_16x16x32_bf16 v[84:87], v[112:115], v[188:191], v[84:87]
	v_mfma_f32_16x16x32_bf16 v[204:207], v[108:111], v[200:203], v[88:91]
	v_mfma_f32_16x16x32_bf16 v[88:91], v[112:115], v[196:199], v[92:95]
	v_mfma_f32_16x16x32_bf16 v[64:67], v[108:111], v[176:179], v[64:67]
	v_mfma_f32_16x16x32_bf16 v[68:71], v[116:119], v[176:179], v[68:71]
	v_mfma_f32_16x16x32_bf16 v[72:75], v[108:111], v[184:187], v[72:75]
	v_mfma_f32_16x16x32_bf16 v[76:79], v[116:119], v[184:187], v[76:79]
	v_mfma_f32_16x16x32_bf16 v[80:83], v[108:111], v[192:195], v[80:83]
	v_mfma_f32_16x16x32_bf16 v[84:87], v[116:119], v[192:195], v[84:87]
	v_mfma_f32_16x16x32_bf16 v[92:95], v[116:119], v[200:203], v[88:91]
	s_setprio 0
	s_setprio 1
	v_mfma_f32_16x16x32_bf16 v[48:51], v[164:167], v[188:191], v[48:51]
	v_mfma_f32_16x16x32_bf16 v[88:91], v[120:123], v[172:175], v[96:99]
	v_mfma_f32_16x16x32_bf16 v[32:35], v[164:167], v[172:175], v[32:35]
	v_mfma_f32_16x16x32_bf16 v[36:39], v[120:123], v[180:183], v[36:39]
	v_mfma_f32_16x16x32_bf16 v[40:43], v[164:167], v[180:183], v[40:43]
	v_mfma_f32_16x16x32_bf16 v[44:47], v[120:123], v[188:191], v[44:47]
	v_mfma_f32_16x16x32_bf16 v[172:175], v[168:171], v[192:195], v[48:51]
	v_mfma_f32_16x16x32_bf16 v[48:51], v[120:123], v[196:199], v[52:55]
	v_mfma_f32_16x16x32_bf16 v[32:35], v[168:171], v[176:179], v[32:35]
	v_mfma_f32_16x16x32_bf16 v[36:39], v[124:127], v[184:187], v[36:39]
	v_mfma_f32_16x16x32_bf16 v[40:43], v[168:171], v[184:187], v[40:43]
	v_mfma_f32_16x16x32_bf16 v[44:47], v[124:127], v[192:195], v[44:47]
	v_mfma_f32_16x16x32_bf16 v[52:55], v[124:127], v[200:203], v[48:51]
	v_mfma_f32_16x16x32_bf16 v[48:51], v[164:167], v[196:199], v[56:59]
	v_mfma_f32_16x16x32_bf16 v[208:211], v[124:127], v[176:179], v[88:91]
	v_mfma_f32_16x16x32_bf16 v[176:179], v[168:171], v[200:203], v[48:51]
	s_setprio 0
	s_barrier
	s_nop 3
	ds_read_b128 v[48:51], v137 offset:16384
	ds_read_b128 v[56:59], v137 offset:17408
	ds_read_b128 v[88:91], v137 offset:18432
	ds_read_b128 v[96:99], v137 offset:19456
	ds_read_b128 v[180:183], v137 offset:20480
	ds_read_b128 v[184:187], v137 offset:21504
	ds_read_b128 v[188:191], v137 offset:22528
	ds_read_b128 v[192:195], v137 offset:23552
	s_mov_b32 s20, m0
	s_mov_b32 m0, s49
	s_nop 2
	global_load_lds_dwordx4 v130, s[28:29]
	s_mov_b32 m0, s20
	s_nop 0
	s_mov_b32 s20, m0
	s_mov_b32 m0, s50
	s_nop 2
	global_load_lds_dwordx4 v131, s[28:29]
	s_mov_b32 m0, s20
	s_nop 0
	s_mov_b32 s20, m0
	s_mov_b32 m0, s51
	s_nop 2
	global_load_lds_dwordx4 v130, s[24:25]
	s_mov_b32 m0, s20
	s_nop 0
	s_mov_b32 s20, m0
	s_mov_b32 m0, s52
	s_nop 2
	global_load_lds_dwordx4 v131, s[24:25]
	s_mov_b32 m0, s20
	s_nop 0
	s_mov_b32 s20, m0
	s_mov_b32 m0, s2
	s_nop 2
	global_load_lds_dwordx4 v132, s[26:27]
	s_mov_b32 m0, s20
	s_nop 0
	s_mov_b32 s20, m0
	s_mov_b32 m0, s53
	s_nop 2
	global_load_lds_dwordx4 v133, s[26:27]
	s_mov_b32 m0, s20
	s_waitcnt vmcnt(8)
	s_waitcnt lgkmcnt(0)
	s_setprio 1
	s_barrier
	v_mfma_f32_16x16x32_bf16 v[0:3], v[104:107], v[188:191], v[0:3]
	v_mfma_f32_16x16x32_bf16 v[4:7], v[112:115], v[188:191], v[4:7]
	v_mfma_f32_16x16x32_bf16 v[140:143], v[104:107], v[48:51], v[140:143]
	v_mfma_f32_16x16x32_bf16 v[144:147], v[112:115], v[48:51], v[144:147]
	v_mfma_f32_16x16x32_bf16 v[148:151], v[104:107], v[88:91], v[148:151]
	v_mfma_f32_16x16x32_bf16 v[152:155], v[112:115], v[88:91], v[152:155]
	v_mfma_f32_16x16x32_bf16 v[156:159], v[104:107], v[180:183], v[156:159]
	v_mfma_f32_16x16x32_bf16 v[160:163], v[112:115], v[180:183], v[160:163]
	v_mfma_f32_16x16x32_bf16 v[0:3], v[108:111], v[192:195], v[0:3]
	v_mfma_f32_16x16x32_bf16 v[4:7], v[116:119], v[192:195], v[4:7]
	v_mfma_f32_16x16x32_bf16 v[140:143], v[108:111], v[56:59], v[140:143]
	v_mfma_f32_16x16x32_bf16 v[144:147], v[116:119], v[56:59], v[144:147]
	v_mfma_f32_16x16x32_bf16 v[148:151], v[108:111], v[96:99], v[148:151]
	v_mfma_f32_16x16x32_bf16 v[152:155], v[116:119], v[96:99], v[152:155]
	v_mfma_f32_16x16x32_bf16 v[156:159], v[108:111], v[184:187], v[156:159]
	v_mfma_f32_16x16x32_bf16 v[160:163], v[116:119], v[184:187], v[160:163]
	s_setprio 0
	s_setprio 1
	v_mfma_f32_16x16x32_bf16 v[12:15], v[164:167], v[48:51], v[12:15]
	v_mfma_f32_16x16x32_bf16 v[196:199], v[168:171], v[56:59], v[12:15]
	v_mfma_f32_16x16x32_bf16 v[12:15], v[120:123], v[88:91], v[24:27]
	v_mfma_f32_16x16x32_bf16 v[24:27], v[124:127], v[96:99], v[12:15]
	v_mfma_f32_16x16x32_bf16 v[12:15], v[164:167], v[88:91], v[28:31]
	v_mfma_f32_16x16x32_bf16 v[200:203], v[168:171], v[96:99], v[12:15]
	v_mfma_f32_16x16x32_bf16 v[12:15], v[120:123], v[180:183], v[60:63]
	v_mfma_f32_16x16x32_bf16 v[212:215], v[124:127], v[184:187], v[12:15]
	v_mfma_f32_16x16x32_bf16 v[12:15], v[164:167], v[180:183], v[100:103]
	v_mfma_f32_16x16x32_bf16 v[8:11], v[120:123], v[48:51], v[8:11]
	v_mfma_f32_16x16x32_bf16 v[180:183], v[168:171], v[184:187], v[12:15]
	v_mfma_f32_16x16x32_bf16 v[12:15], v[120:123], v[188:191], v[16:19]
	v_mfma_f32_16x16x32_bf16 v[8:11], v[124:127], v[56:59], v[8:11]
	v_mfma_f32_16x16x32_bf16 v[184:187], v[124:127], v[192:195], v[12:15]
	v_mfma_f32_16x16x32_bf16 v[12:15], v[164:167], v[188:191], v[20:23]
	v_mfma_f32_16x16x32_bf16 v[164:167], v[168:171], v[192:195], v[12:15]
	s_setprio 0
	s_barrier
	s_nop 4
	ds_read_b128 v[12:15], v138
	ds_read_b128 v[16:19], v138 offset:1024
	ds_read_b128 v[168:171], v138 offset:2048
	ds_read_b128 v[188:191], v138 offset:3072
	ds_read_b128 v[192:195], v139
	ds_read_b128 v[216:219], v139 offset:1024
	ds_read_b128 v[220:223], v139 offset:2048
	ds_read_b128 v[224:227], v139 offset:3072
	ds_read_b128 v[20:23], v137 offset:32768
	ds_read_b128 v[28:31], v137 offset:33792
	ds_read_b128 v[60:63], v137 offset:34816
	ds_read_b128 v[100:103], v137 offset:35840
	ds_read_b128 v[228:231], v137 offset:36864
	ds_read_b128 v[232:235], v137 offset:37888
	ds_read_b128 v[236:239], v137 offset:38912
	ds_read_b128 v[240:243], v137 offset:39936
	s_add_u32 s20, s26, 0x10000
	s_addc_u32 s21, s27, 0
	s_mov_b32 s26, m0
	s_mov_b32 m0, s54
	s_nop 2
	global_load_lds_dwordx4 v132, s[20:21]
	s_mov_b32 m0, s26
	s_nop 0
	s_mov_b32 s26, m0
	s_mov_b32 m0, s55
	s_nop 2
	global_load_lds_dwordx4 v133, s[20:21]
	s_mov_b32 m0, s26
	s_waitcnt vmcnt(8)
	s_waitcnt lgkmcnt(0)
	s_setprio 1
	s_barrier
	v_mfma_f32_16x16x32_bf16 v[48:51], v[12:15], v[20:23], v[64:67]
	v_mfma_f32_16x16x32_bf16 v[120:123], v[16:19], v[28:31], v[48:51]
	v_mfma_f32_16x16x32_bf16 v[48:51], v[168:171], v[20:23], v[68:71]
	v_mfma_f32_16x16x32_bf16 v[112:115], v[188:191], v[28:31], v[48:51]
	v_mfma_f32_16x16x32_bf16 v[48:51], v[12:15], v[60:63], v[72:75]
	v_mfma_f32_16x16x32_bf16 v[104:107], v[16:19], v[100:103], v[48:51]
	v_mfma_f32_16x16x32_bf16 v[48:51], v[168:171], v[60:63], v[76:79]
	v_mfma_f32_16x16x32_bf16 v[96:99], v[188:191], v[100:103], v[48:51]
	v_mfma_f32_16x16x32_bf16 v[48:51], v[12:15], v[228:231], v[80:83]
	v_mfma_f32_16x16x32_bf16 v[88:91], v[16:19], v[232:235], v[48:51]
	v_mfma_f32_16x16x32_bf16 v[48:51], v[168:171], v[228:231], v[84:87]
	v_mfma_f32_16x16x32_bf16 v[80:83], v[188:191], v[232:235], v[48:51]
	v_mfma_f32_16x16x32_bf16 v[48:51], v[12:15], v[236:239], v[204:207]
	v_mfma_f32_16x16x32_bf16 v[56:59], v[16:19], v[240:243], v[48:51]
	v_mfma_f32_16x16x32_bf16 v[48:51], v[168:171], v[236:239], v[92:95]
	v_mfma_f32_16x16x32_bf16 v[48:51], v[188:191], v[240:243], v[48:51]
	s_setprio 0
	s_setprio 1
	v_mfma_f32_16x16x32_bf16 v[64:67], v[192:195], v[20:23], v[208:211]
	v_mfma_f32_16x16x32_bf16 v[20:23], v[220:223], v[20:23], v[32:35]
	v_mfma_f32_16x16x32_bf16 v[116:119], v[224:227], v[28:31], v[20:23]
	v_mfma_f32_16x16x32_bf16 v[20:23], v[192:195], v[60:63], v[36:39]
	v_mfma_f32_16x16x32_bf16 v[108:111], v[216:219], v[100:103], v[20:23]
	v_mfma_f32_16x16x32_bf16 v[20:23], v[220:223], v[60:63], v[40:43]
	v_mfma_f32_16x16x32_bf16 v[100:103], v[224:227], v[100:103], v[20:23]
	v_mfma_f32_16x16x32_bf16 v[20:23], v[192:195], v[228:231], v[44:47]
	v_mfma_f32_16x16x32_bf16 v[92:95], v[216:219], v[232:235], v[20:23]
	v_mfma_f32_16x16x32_bf16 v[20:23], v[220:223], v[228:231], v[172:175]
	v_mfma_f32_16x16x32_bf16 v[84:87], v[224:227], v[232:235], v[20:23]
	v_mfma_f32_16x16x32_bf16 v[20:23], v[192:195], v[236:239], v[52:55]
	v_mfma_f32_16x16x32_bf16 v[60:63], v[216:219], v[240:243], v[20:23]
	v_mfma_f32_16x16x32_bf16 v[20:23], v[220:223], v[236:239], v[176:179]
	v_mfma_f32_16x16x32_bf16 v[124:127], v[216:219], v[28:31], v[64:67]
	v_mfma_f32_16x16x32_bf16 v[52:55], v[224:227], v[240:243], v[20:23]
	s_setprio 0
	s_barrier
	ds_read_b128 v[32:35], v137 offset:49152
	ds_read_b128 v[40:43], v137 offset:50176
	ds_read_b128 v[172:175], v137 offset:51200
	ds_read_b128 v[176:179], v137 offset:52224
	ds_read_b128 v[204:207], v137 offset:53248
	ds_read_b128 v[208:211], v137 offset:54272
	ds_read_b128 v[228:231], v137 offset:55296
	ds_read_b128 v[232:235], v137 offset:56320
	s_mov_b32 s20, m0
	s_mov_b32 m0, s56
	s_nop 2
	global_load_lds_dwordx4 v130, s[30:31]
	s_mov_b32 m0, s20
	s_nop 0
	s_mov_b32 s20, m0
	s_mov_b32 m0, s57
	s_nop 2
	global_load_lds_dwordx4 v131, s[30:31]
	s_mov_b32 m0, s20
	s_add_u32 s20, s24, 0x80
	s_addc_u32 s21, s25, 0
	s_mov_b32 s24, m0
	s_mov_b32 m0, s60
	s_nop 2
	global_load_lds_dwordx4 v130, s[20:21]
	s_mov_b32 m0, s24
	s_nop 0
	s_mov_b32 s24, m0
	s_mov_b32 m0, s61
	s_nop 2
	global_load_lds_dwordx4 v131, s[20:21]
	s_mov_b32 m0, s24
	s_mov_b32 s20, m0
	s_mov_b32 m0, s58
	s_nop 2
	global_load_lds_dwordx4 v132, s[22:23]
	s_mov_b32 m0, s20
	s_nop 0
	s_mov_b32 s20, m0
	s_mov_b32 m0, s59
	s_nop 2
	global_load_lds_dwordx4 v133, s[22:23]
	s_mov_b32 m0, s20
	s_waitcnt vmcnt(8)
	s_waitcnt lgkmcnt(0)
	s_setprio 1
	s_barrier
	v_mfma_f32_16x16x32_bf16 v[20:23], v[12:15], v[32:35], v[140:143]
	v_mfma_f32_16x16x32_bf16 v[76:79], v[16:19], v[40:43], v[20:23]
	v_mfma_f32_16x16x32_bf16 v[20:23], v[168:171], v[32:35], v[144:147]
	v_mfma_f32_16x16x32_bf16 v[68:71], v[188:191], v[40:43], v[20:23]
	v_mfma_f32_16x16x32_bf16 v[20:23], v[12:15], v[172:175], v[148:151]
	v_mfma_f32_16x16x32_bf16 v[44:47], v[16:19], v[176:179], v[20:23]
	v_mfma_f32_16x16x32_bf16 v[20:23], v[168:171], v[172:175], v[152:155]
	v_mfma_f32_16x16x32_bf16 v[36:39], v[188:191], v[176:179], v[20:23]
	v_mfma_f32_16x16x32_bf16 v[20:23], v[12:15], v[204:207], v[156:159]
	v_mfma_f32_16x16x32_bf16 v[0:3], v[12:15], v[228:231], v[0:3]
	v_mfma_f32_16x16x32_bf16 v[28:31], v[16:19], v[208:211], v[20:23]
	v_mfma_f32_16x16x32_bf16 v[20:23], v[168:171], v[204:207], v[160:163]
	v_mfma_f32_16x16x32_bf16 v[12:15], v[16:19], v[232:235], v[0:3]
	v_mfma_f32_16x16x32_bf16 v[0:3], v[168:171], v[228:231], v[4:7]
	v_mfma_f32_16x16x32_bf16 v[20:23], v[188:191], v[208:211], v[20:23]
	v_mfma_f32_16x16x32_bf16 v[4:7], v[188:191], v[232:235], v[0:3]
	s_setprio 0
	s_setprio 1
	v_mfma_f32_16x16x32_bf16 v[0:3], v[192:195], v[32:35], v[8:11]
	v_mfma_f32_16x16x32_bf16 v[72:75], v[216:219], v[40:43], v[0:3]
	v_mfma_f32_16x16x32_bf16 v[0:3], v[220:223], v[32:35], v[196:199]
	v_mfma_f32_16x16x32_bf16 v[64:67], v[224:227], v[40:43], v[0:3]
	v_mfma_f32_16x16x32_bf16 v[0:3], v[192:195], v[172:175], v[24:27]
	v_mfma_f32_16x16x32_bf16 v[40:43], v[216:219], v[176:179], v[0:3]
	v_mfma_f32_16x16x32_bf16 v[0:3], v[220:223], v[172:175], v[200:203]
	v_mfma_f32_16x16x32_bf16 v[32:35], v[224:227], v[176:179], v[0:3]
	v_mfma_f32_16x16x32_bf16 v[0:3], v[192:195], v[204:207], v[212:215]
	v_mfma_f32_16x16x32_bf16 v[24:27], v[216:219], v[208:211], v[0:3]
	v_mfma_f32_16x16x32_bf16 v[0:3], v[220:223], v[204:207], v[180:183]
	v_mfma_f32_16x16x32_bf16 v[16:19], v[224:227], v[208:211], v[0:3]
	v_mfma_f32_16x16x32_bf16 v[0:3], v[192:195], v[228:231], v[184:187]
	v_mfma_f32_16x16x32_bf16 v[8:11], v[216:219], v[232:235], v[0:3]
	v_mfma_f32_16x16x32_bf16 v[0:3], v[220:223], v[228:231], v[164:167]
	v_mfma_f32_16x16x32_bf16 v[0:3], v[224:227], v[232:235], v[0:3]
	s_setprio 0
	s_barrier
	s_andn2_b64 vcc, exec, s[10:11]
	s_cbranch_vccnz .LBB0_1188
	s_barrier

.LBB0_1200:
	v_and_b32_e32 v5, 15, v4
	v_or_b32_e32 v6, s0, v5
	s_add_u32 s14, s20, 0x80
	v_lshlrev_b32_e32 v8, 6, v6
	v_and_b32_e32 v9, 48, v4
	s_movk_i32 s9, 0x3c0
	s_addc_u32 s15, s21, 0
	s_add_i32 s26, 0, 0x18000
	v_and_or_b32 v8, v8, s9, v9
	s_waitcnt vmcnt(2)
	s_barrier
	s_add_i32 s9, s3, s26
	s_mov_b32 s11, m0
	s_mov_b32 m0, s9
	s_nop 2
	global_load_lds_dwordx4 v0, s[14:15]
	s_mov_b32 m0, s11
	s_add_i32 s11, s2, 0x1a000
	s_mov_b32 s16, m0
	s_mov_b32 m0, s11
	s_nop 2
	global_load_lds_dwordx4 v1, s[14:15]
	s_mov_b32 m0, s16
	v_ashrrev_i32_e32 v7, 6, v4
	s_add_u32 s16, s12, 0x80
	v_lshl_add_u32 v10, v7, 10, s33
	s_addc_u32 s17, s13, 0
	s_add_i32 s33, s2, 0x8000
	s_mov_b32 s24, m0
	s_mov_b32 m0, s33
	s_nop 2
	global_load_lds_dwordx4 v2, s[16:17]
	s_mov_b32 m0, s24
	v_add_lshl_u32 v7, v7, s38, 10
	s_add_i32 s38, s2, 0xa000
	s_mov_b32 s24, m0
	s_mov_b32 m0, s38
	s_nop 2
	global_load_lds_dwordx4 v3, s[16:17]
	s_mov_b32 m0, s24
	s_add_u32 s24, s20, 0x10080
	s_addc_u32 s25, s21, 0
	s_add_i32 s27, 0, 0x1c000
	s_add_i32 s3, s3, s27
	s_add_i32 s39, s2, 0x1e000
	s_add_i32 s53, s2, 0xc000
	s_add_i32 s54, s2, 0xe000
	s_add_u32 s40, s12, 0x100
	s_addc_u32 s41, s13, 0
	v_lshlrev_b32_e32 v4, 2, v4
	s_add_u32 s50, s20, 0x100
	v_lshl_or_b32 v5, v5, 6, v9
	v_and_b32_e32 v4, 32, v4
	s_addc_u32 s51, s21, 0
	v_lshlrev_b32_e32 v6, 2, v6
	v_bitop3_b32 v5, v5, v7, v4 bitop3:0xde
	s_add_u32 s46, s20, 0x10100
	v_and_b32_e32 v6, 32, v6
	s_mov_b32 s28, m0
	s_mov_b32 m0, s3
	s_nop 2
	global_load_lds_dwordx4 v0, s[24:25]
	s_mov_b32 m0, s28
	v_add_u32_e32 v4, 0, v5
	s_addc_u32 s47, s21, 0
	v_bitop3_b32 v6, v8, v10, v6 bitop3:0xde
	s_mov_b32 s28, m0
	s_mov_b32 m0, s39
	s_nop 2
	global_load_lds_dwordx4 v1, s[24:25]
	s_mov_b32 m0, s28
	v_add_u32_e32 v198, 0x10000, v4
	s_add_u32 s30, s20, 0x180
	s_waitcnt vmcnt(6)
	s_barrier
	v_add_u32_e32 v199, 0x14000, v4
	v_add_u32_e32 v4, 0, v6
	s_addc_u32 s31, s21, 0
	ds_read_b128 v[6:9], v198
	ds_read_b128 v[10:13], v198 offset:1024
	ds_read_b128 v[14:17], v198 offset:2048
	ds_read_b128 v[18:21], v198 offset:3072
	ds_read_b128 v[22:25], v199
	ds_read_b128 v[26:29], v199 offset:1024
	ds_read_b128 v[30:33], v199 offset:2048
	ds_read_b128 v[34:37], v199 offset:3072
	s_add_u32 s28, s12, 0x180
	s_addc_u32 s29, s13, 0
	s_add_u32 s56, s12, 0x10080
	s_addc_u32 s57, s13, 0
	s_add_u32 s36, s12, 0x10100
	s_addc_u32 s37, s13, 0
	s_add_u32 s34, s20, 0x10180
	s_addc_u32 s35, s21, 0
	v_add_u32_e32 v222, s26, v5
	s_add_u32 s26, s12, 0x10180
	v_add_u32_e32 v5, s27, v5
	s_addc_u32 s27, s13, 0
	v_readlane_b32 s55, v255, 0
	s_cmpk_gt_u32 s55, 0xff
	ds_read_b128 v[38:41], v4
	s_waitcnt vmcnt(4)
	ds_read_b128 v[42:45], v4 offset:1024
	ds_read_b128 v[46:49], v4 offset:2048
	ds_read_b128 v[50:53], v4 offset:3072
	ds_read_b128 v[54:57], v4 offset:4096
	ds_read_b128 v[58:61], v4 offset:5120
	ds_read_b128 v[62:65], v4 offset:6144
	ds_read_b128 v[66:69], v4 offset:7168
	s_mov_b32 s55, m0
	s_mov_b32 m0, s53
	s_nop 2
	global_load_lds_dwordx4 v2, s[56:57]
	s_mov_b32 m0, s55
	s_nop 0
	s_mov_b32 s55, m0
	s_mov_b32 m0, s54
	s_nop 2
	global_load_lds_dwordx4 v3, s[56:57]
	s_mov_b32 m0, s55
	s_waitcnt vmcnt(8)
	s_waitcnt lgkmcnt(0)
	s_setprio 1
	s_barrier
	v_mfma_f32_16x16x32_bf16 v[70:73], v[6:9], v[38:41], 0
	v_mfma_f32_16x16x32_bf16 v[74:77], v[14:17], v[38:41], 0
	v_mfma_f32_16x16x32_bf16 v[78:81], v[6:9], v[46:49], 0
	v_mfma_f32_16x16x32_bf16 v[82:85], v[14:17], v[46:49], 0
	v_mfma_f32_16x16x32_bf16 v[86:89], v[6:9], v[54:57], 0
	v_mfma_f32_16x16x32_bf16 v[90:93], v[14:17], v[54:57], 0
	v_mfma_f32_16x16x32_bf16 v[94:97], v[6:9], v[62:65], 0
	v_mfma_f32_16x16x32_bf16 v[98:101], v[14:17], v[62:65], 0
	v_mfma_f32_16x16x32_bf16 v[70:73], v[10:13], v[42:45], v[70:73]
	v_mfma_f32_16x16x32_bf16 v[74:77], v[18:21], v[42:45], v[74:77]
	v_mfma_f32_16x16x32_bf16 v[78:81], v[10:13], v[50:53], v[78:81]
	v_mfma_f32_16x16x32_bf16 v[82:85], v[18:21], v[50:53], v[82:85]
	v_mfma_f32_16x16x32_bf16 v[86:89], v[10:13], v[58:61], v[86:89]
	v_mfma_f32_16x16x32_bf16 v[90:93], v[18:21], v[58:61], v[90:93]
	v_mfma_f32_16x16x32_bf16 v[94:97], v[10:13], v[66:69], v[94:97]
	v_mfma_f32_16x16x32_bf16 v[98:101], v[18:21], v[66:69], v[98:101]
	s_setprio 0
	s_setprio 1
	v_mfma_f32_16x16x32_bf16 v[102:105], v[22:25], v[38:41], 0
	v_mfma_f32_16x16x32_bf16 v[38:41], v[30:33], v[38:41], 0
	v_mfma_f32_16x16x32_bf16 v[102:105], v[26:29], v[42:45], v[102:105]
	v_mfma_f32_16x16x32_bf16 v[38:41], v[34:37], v[42:45], v[38:41]
	v_mfma_f32_16x16x32_bf16 v[42:45], v[22:25], v[46:49], 0
	v_mfma_f32_16x16x32_bf16 v[46:49], v[30:33], v[46:49], 0
	v_mfma_f32_16x16x32_bf16 v[42:45], v[26:29], v[50:53], v[42:45]
	v_mfma_f32_16x16x32_bf16 v[46:49], v[34:37], v[50:53], v[46:49]
	v_mfma_f32_16x16x32_bf16 v[50:53], v[22:25], v[54:57], 0
	v_mfma_f32_16x16x32_bf16 v[54:57], v[30:33], v[54:57], 0
	v_mfma_f32_16x16x32_bf16 v[50:53], v[26:29], v[58:61], v[50:53]
	v_mfma_f32_16x16x32_bf16 v[54:57], v[34:37], v[58:61], v[54:57]
	v_mfma_f32_16x16x32_bf16 v[58:61], v[22:25], v[62:65], 0
	v_mfma_f32_16x16x32_bf16 v[62:65], v[30:33], v[62:65], 0
	v_mfma_f32_16x16x32_bf16 v[58:61], v[26:29], v[66:69], v[58:61]
	v_mfma_f32_16x16x32_bf16 v[62:65], v[34:37], v[66:69], v[62:65]
	s_setprio 0
	s_barrier
	ds_read_b128 v[66:69], v4 offset:16384
	ds_read_b128 v[106:109], v4 offset:17408
	ds_read_b128 v[110:113], v4 offset:18432
	ds_read_b128 v[114:117], v4 offset:19456
	ds_read_b128 v[118:121], v4 offset:20480
	ds_read_b128 v[122:125], v4 offset:21504
	ds_read_b128 v[126:129], v4 offset:22528
	ds_read_b128 v[130:133], v4 offset:23552
	s_mov_b32 s55, m0
	s_mov_b32 m0, s44
	s_nop 2
	global_load_lds_dwordx4 v0, s[50:51]
	s_mov_b32 m0, s55
	s_nop 0
	s_mov_b32 s55, m0
	s_mov_b32 m0, s45
	s_nop 2
	global_load_lds_dwordx4 v1, s[50:51]
	s_mov_b32 m0, s55
	s_mov_b32 s50, m0
	s_mov_b32 m0, s48
	s_nop 2
	global_load_lds_dwordx4 v0, s[46:47]
	s_mov_b32 m0, s50
	s_nop 0
	s_mov_b32 s50, m0
	s_mov_b32 m0, s49
	s_nop 2
	global_load_lds_dwordx4 v1, s[46:47]
	s_mov_b32 m0, s50
	s_mov_b32 s46, m0
	s_mov_b32 m0, s2
	s_nop 2
	global_load_lds_dwordx4 v2, s[40:41]
	s_mov_b32 m0, s46
	s_nop 0
	s_mov_b32 s46, m0
	s_mov_b32 m0, s52
	s_nop 2
	global_load_lds_dwordx4 v3, s[40:41]
	s_mov_b32 m0, s46
	s_waitcnt vmcnt(8)
	s_waitcnt lgkmcnt(0)
	s_barrier
	s_setprio 1
	s_waitcnt lgkmcnt(7)
	v_mfma_f32_16x16x32_bf16 v[134:137], v[6:9], v[66:69], 0
	s_waitcnt lgkmcnt(5)
	v_mfma_f32_16x16x32_bf16 v[142:145], v[6:9], v[110:113], 0
	s_waitcnt vmcnt(2) lgkmcnt(3)
	v_mfma_f32_16x16x32_bf16 v[150:153], v[6:9], v[118:121], 0
	s_waitcnt lgkmcnt(1)
	v_mfma_f32_16x16x32_bf16 v[6:9], v[6:9], v[126:129], 0
	v_mfma_f32_16x16x32_bf16 v[134:137], v[10:13], v[106:109], v[134:137]
	v_mfma_f32_16x16x32_bf16 v[142:145], v[10:13], v[114:117], v[142:145]
	v_mfma_f32_16x16x32_bf16 v[150:153], v[10:13], v[122:125], v[150:153]
	s_waitcnt lgkmcnt(0)
	v_mfma_f32_16x16x32_bf16 v[6:9], v[10:13], v[130:133], v[6:9]
	v_mfma_f32_16x16x32_bf16 v[10:13], v[14:17], v[126:129], 0
	v_mfma_f32_16x16x32_bf16 v[138:141], v[14:17], v[66:69], 0
	s_waitcnt vmcnt(0)
	v_mfma_f32_16x16x32_bf16 v[146:149], v[14:17], v[110:113], 0
	v_mfma_f32_16x16x32_bf16 v[154:157], v[14:17], v[118:121], 0
	v_mfma_f32_16x16x32_bf16 v[10:13], v[18:21], v[130:133], v[10:13]
	v_mfma_f32_16x16x32_bf16 v[138:141], v[18:21], v[106:109], v[138:141]
	v_mfma_f32_16x16x32_bf16 v[146:149], v[18:21], v[114:117], v[146:149]
	v_mfma_f32_16x16x32_bf16 v[154:157], v[18:21], v[122:125], v[154:157]
	s_setprio 0
	s_setprio 1
	v_mfma_f32_16x16x32_bf16 v[14:17], v[22:25], v[66:69], 0
	v_mfma_f32_16x16x32_bf16 v[18:21], v[30:33], v[66:69], 0
	v_mfma_f32_16x16x32_bf16 v[14:17], v[26:29], v[106:109], v[14:17]
	v_mfma_f32_16x16x32_bf16 v[18:21], v[34:37], v[106:109], v[18:21]
	v_mfma_f32_16x16x32_bf16 v[66:69], v[22:25], v[110:113], 0
	v_mfma_f32_16x16x32_bf16 v[106:109], v[30:33], v[110:113], 0
	v_mfma_f32_16x16x32_bf16 v[110:113], v[22:25], v[118:121], 0
	v_mfma_f32_16x16x32_bf16 v[22:25], v[22:25], v[126:129], 0
	v_mfma_f32_16x16x32_bf16 v[66:69], v[26:29], v[114:117], v[66:69]
	v_mfma_f32_16x16x32_bf16 v[106:109], v[34:37], v[114:117], v[106:109]
	v_mfma_f32_16x16x32_bf16 v[110:113], v[26:29], v[122:125], v[110:113]
	v_mfma_f32_16x16x32_bf16 v[114:117], v[30:33], v[118:121], 0
	v_mfma_f32_16x16x32_bf16 v[22:25], v[26:29], v[130:133], v[22:25]
	v_mfma_f32_16x16x32_bf16 v[26:29], v[30:33], v[126:129], 0
	v_mfma_f32_16x16x32_bf16 v[114:117], v[34:37], v[122:125], v[114:117]
	v_mfma_f32_16x16x32_bf16 v[26:29], v[34:37], v[130:133], v[26:29]
	s_setprio 0
	s_barrier
	ds_read_b128 v[30:33], v222
	ds_read_b128 v[34:37], v222 offset:1024
	ds_read_b128 v[118:121], v222 offset:2048
	ds_read_b128 v[122:125], v222 offset:3072
	ds_read_b128 v[126:129], v5
	ds_read_b128 v[130:133], v5 offset:1024
	ds_read_b128 v[158:161], v5 offset:2048
	ds_read_b128 v[162:165], v5 offset:3072
	ds_read_b128 v[166:169], v4 offset:32768
	ds_read_b128 v[170:173], v4 offset:33792
	ds_read_b128 v[174:177], v4 offset:34816
	ds_read_b128 v[178:181], v4 offset:35840
	ds_read_b128 v[182:185], v4 offset:36864
	ds_read_b128 v[186:189], v4 offset:37888
	ds_read_b128 v[190:193], v4 offset:38912
	ds_read_b128 v[194:197], v4 offset:39936
	s_mov_b32 s40, m0
	s_mov_b32 m0, s42
	s_nop 2
	global_load_lds_dwordx4 v2, s[36:37]
	s_mov_b32 m0, s40
	s_nop 0
	s_mov_b32 s40, m0
	s_mov_b32 m0, s43
	s_nop 2
	global_load_lds_dwordx4 v3, s[36:37]
	s_mov_b32 m0, s40
	s_waitcnt vmcnt(8)
	s_waitcnt lgkmcnt(0)
	s_setprio 1
	s_barrier
	v_mfma_f32_16x16x32_bf16 v[70:73], v[30:33], v[166:169], v[70:73]
	v_mfma_f32_16x16x32_bf16 v[74:77], v[118:121], v[166:169], v[74:77]
	v_mfma_f32_16x16x32_bf16 v[78:81], v[30:33], v[174:177], v[78:81]
	v_mfma_f32_16x16x32_bf16 v[82:85], v[118:121], v[174:177], v[82:85]
	v_mfma_f32_16x16x32_bf16 v[86:89], v[30:33], v[182:185], v[86:89]
	v_mfma_f32_16x16x32_bf16 v[90:93], v[118:121], v[182:185], v[90:93]
	v_mfma_f32_16x16x32_bf16 v[94:97], v[30:33], v[190:193], v[94:97]
	v_mfma_f32_16x16x32_bf16 v[98:101], v[118:121], v[190:193], v[98:101]
	v_mfma_f32_16x16x32_bf16 v[70:73], v[34:37], v[170:173], v[70:73]
	v_mfma_f32_16x16x32_bf16 v[74:77], v[122:125], v[170:173], v[74:77]
	v_mfma_f32_16x16x32_bf16 v[78:81], v[34:37], v[178:181], v[78:81]
	v_mfma_f32_16x16x32_bf16 v[82:85], v[122:125], v[178:181], v[82:85]
	v_mfma_f32_16x16x32_bf16 v[86:89], v[34:37], v[186:189], v[86:89]
	v_mfma_f32_16x16x32_bf16 v[90:93], v[122:125], v[186:189], v[90:93]
	v_mfma_f32_16x16x32_bf16 v[94:97], v[34:37], v[194:197], v[94:97]
	v_mfma_f32_16x16x32_bf16 v[98:101], v[122:125], v[194:197], v[98:101]
	s_setprio 0
	s_setprio 1
	v_mfma_f32_16x16x32_bf16 v[102:105], v[126:129], v[166:169], v[102:105]
	v_mfma_f32_16x16x32_bf16 v[38:41], v[158:161], v[166:169], v[38:41]
	v_mfma_f32_16x16x32_bf16 v[42:45], v[126:129], v[174:177], v[42:45]
	v_mfma_f32_16x16x32_bf16 v[46:49], v[158:161], v[174:177], v[46:49]
	v_mfma_f32_16x16x32_bf16 v[50:53], v[126:129], v[182:185], v[50:53]
	v_mfma_f32_16x16x32_bf16 v[54:57], v[158:161], v[182:185], v[54:57]
	v_mfma_f32_16x16x32_bf16 v[58:61], v[126:129], v[190:193], v[58:61]
	v_mfma_f32_16x16x32_bf16 v[62:65], v[158:161], v[190:193], v[62:65]
	v_mfma_f32_16x16x32_bf16 v[102:105], v[130:133], v[170:173], v[102:105]
	v_mfma_f32_16x16x32_bf16 v[38:41], v[162:165], v[170:173], v[38:41]
	v_mfma_f32_16x16x32_bf16 v[42:45], v[130:133], v[178:181], v[42:45]
	v_mfma_f32_16x16x32_bf16 v[46:49], v[162:165], v[178:181], v[46:49]
	v_mfma_f32_16x16x32_bf16 v[50:53], v[130:133], v[186:189], v[50:53]
	v_mfma_f32_16x16x32_bf16 v[54:57], v[162:165], v[186:189], v[54:57]
	v_mfma_f32_16x16x32_bf16 v[58:61], v[130:133], v[194:197], v[58:61]
	v_mfma_f32_16x16x32_bf16 v[62:65], v[162:165], v[194:197], v[62:65]
	s_setprio 0
	s_barrier
	ds_read_b128 v[166:169], v4 offset:49152
	ds_read_b128 v[170:173], v4 offset:50176
	ds_read_b128 v[174:177], v4 offset:51200
	ds_read_b128 v[178:181], v4 offset:52224
	ds_read_b128 v[182:185], v4 offset:53248
	ds_read_b128 v[186:189], v4 offset:54272
	ds_read_b128 v[190:193], v4 offset:55296
	ds_read_b128 v[194:197], v4 offset:56320
	s_mov_b32 s36, m0
	s_mov_b32 m0, s9
	s_nop 2
	global_load_lds_dwordx4 v0, s[30:31]
	s_mov_b32 m0, s36
	s_nop 0
	s_mov_b32 s36, m0
	s_mov_b32 m0, s11
	s_nop 2
	global_load_lds_dwordx4 v1, s[30:31]
	s_mov_b32 m0, s36
	s_mov_b32 s30, m0
	s_mov_b32 m0, s3
	s_nop 2
	global_load_lds_dwordx4 v0, s[34:35]
	s_mov_b32 m0, s30
	s_nop 0
	s_mov_b32 s30, m0
	s_mov_b32 m0, s39
	s_nop 2
	global_load_lds_dwordx4 v1, s[34:35]
	s_mov_b32 m0, s30
	s_nop 0
	s_mov_b32 s30, m0
	s_mov_b32 m0, s33
	s_nop 2
	global_load_lds_dwordx4 v2, s[28:29]
	s_mov_b32 m0, s30
	s_nop 0
	s_mov_b32 s30, m0
	s_mov_b32 m0, s38
	s_nop 2
	global_load_lds_dwordx4 v3, s[28:29]
	s_mov_b32 m0, s30
	s_waitcnt vmcnt(8)
	s_waitcnt lgkmcnt(0)
	s_setprio 1
	s_barrier
	v_mfma_f32_16x16x32_bf16 v[6:9], v[30:33], v[190:193], v[6:9]
	v_mfma_f32_16x16x32_bf16 v[10:13], v[118:121], v[190:193], v[10:13]
	v_mfma_f32_16x16x32_bf16 v[134:137], v[30:33], v[166:169], v[134:137]
	v_mfma_f32_16x16x32_bf16 v[138:141], v[118:121], v[166:169], v[138:141]
	v_mfma_f32_16x16x32_bf16 v[142:145], v[30:33], v[174:177], v[142:145]
	v_mfma_f32_16x16x32_bf16 v[146:149], v[118:121], v[174:177], v[146:149]
	v_mfma_f32_16x16x32_bf16 v[150:153], v[30:33], v[182:185], v[150:153]
	v_mfma_f32_16x16x32_bf16 v[154:157], v[118:121], v[182:185], v[154:157]
	v_mfma_f32_16x16x32_bf16 v[6:9], v[34:37], v[194:197], v[6:9]
	v_mfma_f32_16x16x32_bf16 v[10:13], v[122:125], v[194:197], v[10:13]
	v_mfma_f32_16x16x32_bf16 v[134:137], v[34:37], v[170:173], v[134:137]
	v_mfma_f32_16x16x32_bf16 v[138:141], v[122:125], v[170:173], v[138:141]
	v_mfma_f32_16x16x32_bf16 v[142:145], v[34:37], v[178:181], v[142:145]
	v_mfma_f32_16x16x32_bf16 v[146:149], v[122:125], v[178:181], v[146:149]
	v_mfma_f32_16x16x32_bf16 v[150:153], v[34:37], v[186:189], v[150:153]
	v_mfma_f32_16x16x32_bf16 v[154:157], v[122:125], v[186:189], v[154:157]
	s_setprio 0
	s_setprio 1
	v_mfma_f32_16x16x32_bf16 v[14:17], v[126:129], v[166:169], v[14:17]
	v_mfma_f32_16x16x32_bf16 v[18:21], v[158:161], v[166:169], v[18:21]
	v_mfma_f32_16x16x32_bf16 v[30:33], v[126:129], v[174:177], v[66:69]
	v_mfma_f32_16x16x32_bf16 v[34:37], v[158:161], v[174:177], v[106:109]
	v_mfma_f32_16x16x32_bf16 v[66:69], v[126:129], v[182:185], v[110:113]
	v_mfma_f32_16x16x32_bf16 v[106:109], v[158:161], v[182:185], v[114:117]
	v_mfma_f32_16x16x32_bf16 v[22:25], v[126:129], v[190:193], v[22:25]
	v_mfma_f32_16x16x32_bf16 v[26:29], v[158:161], v[190:193], v[26:29]
	v_mfma_f32_16x16x32_bf16 v[14:17], v[130:133], v[170:173], v[14:17]
	v_mfma_f32_16x16x32_bf16 v[18:21], v[162:165], v[170:173], v[18:21]
	v_mfma_f32_16x16x32_bf16 v[30:33], v[130:133], v[178:181], v[30:33]
	v_mfma_f32_16x16x32_bf16 v[34:37], v[162:165], v[178:181], v[34:37]
	v_mfma_f32_16x16x32_bf16 v[66:69], v[130:133], v[186:189], v[66:69]
	v_mfma_f32_16x16x32_bf16 v[106:109], v[162:165], v[186:189], v[106:109]
	v_mfma_f32_16x16x32_bf16 v[22:25], v[130:133], v[194:197], v[22:25]
	v_mfma_f32_16x16x32_bf16 v[26:29], v[162:165], v[194:197], v[26:29]
	s_setprio 0
	s_barrier
	ds_read_b128 v[110:113], v198
	ds_read_b128 v[114:117], v198 offset:1024
	ds_read_b128 v[118:121], v198 offset:2048
	ds_read_b128 v[122:125], v198 offset:3072
	ds_read_b128 v[126:129], v199
	ds_read_b128 v[130:133], v199 offset:1024
	ds_read_b128 v[158:161], v199 offset:2048
	ds_read_b128 v[162:165], v199 offset:3072
	ds_read_b128 v[166:169], v4
	ds_read_b128 v[170:173], v4 offset:1024
	ds_read_b128 v[174:177], v4 offset:2048
	ds_read_b128 v[178:181], v4 offset:3072
	ds_read_b128 v[182:185], v4 offset:4096
	ds_read_b128 v[186:189], v4 offset:5120
	ds_read_b128 v[190:193], v4 offset:6144
	ds_read_b128 v[194:197], v4 offset:7168
	s_mov_b32 s28, m0
	s_mov_b32 m0, s53
	s_nop 2
	global_load_lds_dwordx4 v2, s[26:27]
	s_mov_b32 m0, s28
	s_nop 0
	s_mov_b32 s28, m0
	s_mov_b32 m0, s54
	s_nop 2
	global_load_lds_dwordx4 v3, s[26:27]
	s_mov_b32 m0, s28
	s_waitcnt vmcnt(8)
	s_waitcnt lgkmcnt(0)
	s_setprio 1
	s_barrier
	v_mfma_f32_16x16x32_bf16 v[90:93], v[118:121], v[182:185], v[90:93]
	v_mfma_f32_16x16x32_bf16 v[70:73], v[110:113], v[166:169], v[70:73]
	v_mfma_f32_16x16x32_bf16 v[74:77], v[118:121], v[166:169], v[74:77]
	v_mfma_f32_16x16x32_bf16 v[78:81], v[110:113], v[174:177], v[78:81]
	v_mfma_f32_16x16x32_bf16 v[82:85], v[118:121], v[174:177], v[82:85]
	v_mfma_f32_16x16x32_bf16 v[86:89], v[110:113], v[182:185], v[86:89]
	v_mfma_f32_16x16x32_bf16 v[198:201], v[122:125], v[186:189], v[90:93]
	v_mfma_f32_16x16x32_bf16 v[90:93], v[110:113], v[190:193], v[94:97]
	v_mfma_f32_16x16x32_bf16 v[70:73], v[114:117], v[170:173], v[70:73]
	v_mfma_f32_16x16x32_bf16 v[74:77], v[122:125], v[170:173], v[74:77]
	v_mfma_f32_16x16x32_bf16 v[78:81], v[114:117], v[178:181], v[78:81]
	v_mfma_f32_16x16x32_bf16 v[82:85], v[122:125], v[178:181], v[82:85]
	v_mfma_f32_16x16x32_bf16 v[86:89], v[114:117], v[186:189], v[86:89]
	v_mfma_f32_16x16x32_bf16 v[92:95], v[114:117], v[194:197], v[90:93]
	v_mfma_f32_16x16x32_bf16 v[96:99], v[118:121], v[190:193], v[98:101]
	v_mfma_f32_16x16x32_bf16 v[202:205], v[122:125], v[194:197], v[96:99]
	s_setprio 0
	s_setprio 1
	v_mfma_f32_16x16x32_bf16 v[46:49], v[158:161], v[174:177], v[46:49]
	v_mfma_f32_16x16x32_bf16 v[96:99], v[126:129], v[166:169], v[102:105]
	v_mfma_f32_16x16x32_bf16 v[38:41], v[158:161], v[166:169], v[38:41]
	v_mfma_f32_16x16x32_bf16 v[166:169], v[162:165], v[178:181], v[46:49]
	v_mfma_f32_16x16x32_bf16 v[46:49], v[126:129], v[182:185], v[50:53]
	v_mfma_f32_16x16x32_bf16 v[100:103], v[130:133], v[170:173], v[96:99]
	v_mfma_f32_16x16x32_bf16 v[38:41], v[162:165], v[170:173], v[38:41]
	v_mfma_f32_16x16x32_bf16 v[170:173], v[130:133], v[186:189], v[46:49]
	v_mfma_f32_16x16x32_bf16 v[46:49], v[158:161], v[182:185], v[54:57]
	v_mfma_f32_16x16x32_bf16 v[42:45], v[126:129], v[174:177], v[42:45]
	v_mfma_f32_16x16x32_bf16 v[52:55], v[162:165], v[186:189], v[46:49]
	v_mfma_f32_16x16x32_bf16 v[46:49], v[126:129], v[190:193], v[58:61]
	v_mfma_f32_16x16x32_bf16 v[42:45], v[130:133], v[178:181], v[42:45]
	v_mfma_f32_16x16x32_bf16 v[174:177], v[130:133], v[194:197], v[46:49]
	v_mfma_f32_16x16x32_bf16 v[46:49], v[158:161], v[190:193], v[62:65]
	v_mfma_f32_16x16x32_bf16 v[178:181], v[162:165], v[194:197], v[46:49]
	s_setprio 0
	s_barrier
	s_nop 4
	ds_read_b128 v[46:49], v4 offset:16384
	ds_read_b128 v[56:59], v4 offset:17408
	ds_read_b128 v[60:63], v4 offset:18432
	ds_read_b128 v[96:99], v4 offset:19456
	ds_read_b128 v[182:185], v4 offset:20480
	ds_read_b128 v[186:189], v4 offset:21504
	ds_read_b128 v[190:193], v4 offset:22528
	ds_read_b128 v[194:197], v4 offset:23552
	s_mov_b32 s26, m0
	s_mov_b32 m0, s44
	s_nop 2
	global_load_lds_dwordx4 v0, s[20:21]
	s_mov_b32 m0, s26
	s_nop 0
	s_mov_b32 s26, m0
	s_mov_b32 m0, s45
	s_nop 2
	global_load_lds_dwordx4 v1, s[20:21]
	s_mov_b32 m0, s26
	s_mov_b32 s20, m0
	s_mov_b32 m0, s48
	s_nop 2
	global_load_lds_dwordx4 v0, s[18:19]
	s_mov_b32 m0, s20
	s_nop 0
	s_mov_b32 s20, m0
	s_mov_b32 m0, s49
	s_nop 2
	global_load_lds_dwordx4 v1, s[18:19]
	s_mov_b32 m0, s20
	s_mov_b32 s18, m0
	s_mov_b32 m0, s2
	s_nop 2
	global_load_lds_dwordx4 v2, s[12:13]
	s_mov_b32 m0, s18
	s_mov_b32 s2, m0
	s_mov_b32 m0, s52
	s_nop 2
	global_load_lds_dwordx4 v3, s[12:13]
	s_mov_b32 m0, s2
	s_waitcnt vmcnt(8)
	s_waitcnt lgkmcnt(0)
	s_setprio 1
	s_barrier
	v_mfma_f32_16x16x32_bf16 v[6:9], v[110:113], v[190:193], v[6:9]
	v_mfma_f32_16x16x32_bf16 v[134:137], v[110:113], v[46:49], v[134:137]
	v_mfma_f32_16x16x32_bf16 v[138:141], v[118:121], v[46:49], v[138:141]
	v_mfma_f32_16x16x32_bf16 v[142:145], v[110:113], v[60:63], v[142:145]
	v_mfma_f32_16x16x32_bf16 v[146:149], v[118:121], v[60:63], v[146:149]
	v_mfma_f32_16x16x32_bf16 v[150:153], v[110:113], v[182:185], v[150:153]
	v_mfma_f32_16x16x32_bf16 v[154:157], v[118:121], v[182:185], v[154:157]
	v_mfma_f32_16x16x32_bf16 v[6:9], v[114:117], v[194:197], v[6:9]
	v_mfma_f32_16x16x32_bf16 v[10:13], v[118:121], v[190:193], v[10:13]
	v_mfma_f32_16x16x32_bf16 v[134:137], v[114:117], v[56:59], v[134:137]
	v_mfma_f32_16x16x32_bf16 v[138:141], v[122:125], v[56:59], v[138:141]
	v_mfma_f32_16x16x32_bf16 v[142:145], v[114:117], v[96:99], v[142:145]
	v_mfma_f32_16x16x32_bf16 v[146:149], v[122:125], v[96:99], v[146:149]
	v_mfma_f32_16x16x32_bf16 v[150:153], v[114:117], v[186:189], v[150:153]
	v_mfma_f32_16x16x32_bf16 v[154:157], v[122:125], v[186:189], v[154:157]
	v_mfma_f32_16x16x32_bf16 v[206:209], v[122:125], v[194:197], v[10:13]
	s_setprio 0
	s_setprio 1
	v_mfma_f32_16x16x32_bf16 v[10:13], v[126:129], v[46:49], v[14:17]
	v_mfma_f32_16x16x32_bf16 v[210:213], v[130:133], v[56:59], v[10:13]
	v_mfma_f32_16x16x32_bf16 v[10:13], v[158:161], v[46:49], v[18:21]
	v_mfma_f32_16x16x32_bf16 v[16:19], v[162:165], v[56:59], v[10:13]
	v_mfma_f32_16x16x32_bf16 v[10:13], v[126:129], v[60:63], v[30:33]
	v_mfma_f32_16x16x32_bf16 v[214:217], v[130:133], v[96:99], v[10:13]
	v_mfma_f32_16x16x32_bf16 v[10:13], v[158:161], v[60:63], v[34:37]
	v_mfma_f32_16x16x32_bf16 v[32:35], v[162:165], v[96:99], v[10:13]
	v_mfma_f32_16x16x32_bf16 v[10:13], v[126:129], v[182:185], v[66:69]
	v_mfma_f32_16x16x32_bf16 v[218:221], v[130:133], v[186:189], v[10:13]
	v_mfma_f32_16x16x32_bf16 v[10:13], v[158:161], v[182:185], v[106:109]
	v_mfma_f32_16x16x32_bf16 v[182:185], v[162:165], v[186:189], v[10:13]
	v_mfma_f32_16x16x32_bf16 v[10:13], v[126:129], v[190:193], v[22:25]
	v_mfma_f32_16x16x32_bf16 v[128:131], v[130:133], v[194:197], v[10:13]
	v_mfma_f32_16x16x32_bf16 v[10:13], v[158:161], v[190:193], v[26:29]
	v_mfma_f32_16x16x32_bf16 v[158:161], v[162:165], v[194:197], v[10:13]
	s_setprio 0
	s_barrier
	s_nop 4
	ds_read_b128 v[10:13], v222
	ds_read_b128 v[24:27], v222 offset:1024
	ds_read_b128 v[64:67], v222 offset:2048
	ds_read_b128 v[162:165], v222 offset:3072
	ds_read_b128 v[186:189], v5
	ds_read_b128 v[190:193], v5 offset:1024
	ds_read_b128 v[194:197], v5 offset:2048
	ds_read_b128 v[222:225], v5 offset:3072
	ds_read_b128 v[20:23], v4 offset:32768
	ds_read_b128 v[28:31], v4 offset:33792
	ds_read_b128 v[60:63], v4 offset:34816
	ds_read_b128 v[226:229], v4 offset:35840
	ds_read_b128 v[230:233], v4 offset:36864
	ds_read_b128 v[234:237], v4 offset:37888
	ds_read_b128 v[238:241], v4 offset:38912
	ds_read_b128 v[242:245], v4 offset:39936
	s_mov_b32 s2, m0
	s_mov_b32 m0, s42
	s_nop 2
	global_load_lds_dwordx4 v2, s[22:23]
	s_mov_b32 m0, s2
	s_nop 0
	s_mov_b32 s2, m0
	s_mov_b32 m0, s43
	s_nop 2
	global_load_lds_dwordx4 v3, s[22:23]
	s_mov_b32 m0, s2
	s_waitcnt vmcnt(8)
	s_waitcnt lgkmcnt(0)
	s_setprio 1
	s_barrier
	v_mfma_f32_16x16x32_bf16 v[46:49], v[10:13], v[20:23], v[70:73]
	v_mfma_f32_16x16x32_bf16 v[120:123], v[24:27], v[28:31], v[46:49]
	v_mfma_f32_16x16x32_bf16 v[46:49], v[64:67], v[20:23], v[74:77]
	v_mfma_f32_16x16x32_bf16 v[112:115], v[162:165], v[28:31], v[46:49]
	v_mfma_f32_16x16x32_bf16 v[46:49], v[10:13], v[60:63], v[78:81]
	v_mfma_f32_16x16x32_bf16 v[104:107], v[24:27], v[226:229], v[46:49]
	v_mfma_f32_16x16x32_bf16 v[46:49], v[64:67], v[60:63], v[82:85]
	v_mfma_f32_16x16x32_bf16 v[96:99], v[162:165], v[226:229], v[46:49]
	v_mfma_f32_16x16x32_bf16 v[46:49], v[10:13], v[230:233], v[86:89]
	v_mfma_f32_16x16x32_bf16 v[88:91], v[24:27], v[234:237], v[46:49]
	v_mfma_f32_16x16x32_bf16 v[46:49], v[64:67], v[230:233], v[198:201]
	v_mfma_f32_16x16x32_bf16 v[80:83], v[162:165], v[234:237], v[46:49]
	v_mfma_f32_16x16x32_bf16 v[46:49], v[10:13], v[238:241], v[92:95]
	v_mfma_f32_16x16x32_bf16 v[56:59], v[24:27], v[242:245], v[46:49]
	v_mfma_f32_16x16x32_bf16 v[46:49], v[64:67], v[238:241], v[202:205]
	v_mfma_f32_16x16x32_bf16 v[48:51], v[162:165], v[242:245], v[46:49]
	s_setprio 0
	s_setprio 1
	v_mfma_f32_16x16x32_bf16 v[68:71], v[186:189], v[20:23], v[100:103]
	v_mfma_f32_16x16x32_bf16 v[20:23], v[194:197], v[20:23], v[38:41]
	v_mfma_f32_16x16x32_bf16 v[116:119], v[222:225], v[28:31], v[20:23]
	v_mfma_f32_16x16x32_bf16 v[20:23], v[186:189], v[60:63], v[42:45]
	v_mfma_f32_16x16x32_bf16 v[108:111], v[190:193], v[226:229], v[20:23]
	v_mfma_f32_16x16x32_bf16 v[20:23], v[194:197], v[60:63], v[166:169]
	v_mfma_f32_16x16x32_bf16 v[100:103], v[222:225], v[226:229], v[20:23]
	v_mfma_f32_16x16x32_bf16 v[20:23], v[186:189], v[230:233], v[170:173]
	v_mfma_f32_16x16x32_bf16 v[92:95], v[190:193], v[234:237], v[20:23]
	v_mfma_f32_16x16x32_bf16 v[20:23], v[194:197], v[230:233], v[52:55]
	v_mfma_f32_16x16x32_bf16 v[84:87], v[222:225], v[234:237], v[20:23]
	v_mfma_f32_16x16x32_bf16 v[20:23], v[186:189], v[238:241], v[174:177]
	v_mfma_f32_16x16x32_bf16 v[60:63], v[190:193], v[242:245], v[20:23]
	v_mfma_f32_16x16x32_bf16 v[20:23], v[194:197], v[238:241], v[178:181]
	v_mfma_f32_16x16x32_bf16 v[124:127], v[190:193], v[28:31], v[68:71]
	v_mfma_f32_16x16x32_bf16 v[52:55], v[222:225], v[242:245], v[20:23]
	s_setprio 0
	s_barrier
	ds_read_b128 v[40:43], v4 offset:49152
	ds_read_b128 v[166:169], v4 offset:50176
	ds_read_b128 v[170:173], v4 offset:51200
	ds_read_b128 v[174:177], v4 offset:52224
	ds_read_b128 v[178:181], v4 offset:53248
	ds_read_b128 v[198:201], v4 offset:54272
	ds_read_b128 v[202:205], v4 offset:55296
	ds_read_b128 v[226:229], v4 offset:56320
	s_mov_b32 s2, m0
	s_mov_b32 m0, s9
	s_nop 2
	global_load_lds_dwordx4 v0, s[14:15]
	s_mov_b32 m0, s2
	s_nop 0
	s_mov_b32 s2, m0
	s_mov_b32 m0, s11
	s_nop 2
	global_load_lds_dwordx4 v1, s[14:15]
	s_mov_b32 m0, s2
	s_nop 0
	s_mov_b32 s2, m0
	s_mov_b32 m0, s3
	s_nop 2
	global_load_lds_dwordx4 v0, s[24:25]
	s_mov_b32 m0, s2
	s_nop 0
	s_mov_b32 s2, m0
	s_mov_b32 m0, s39
	s_nop 2
	global_load_lds_dwordx4 v1, s[24:25]
	s_mov_b32 m0, s2
	s_nop 0
	s_mov_b32 s2, m0
	s_mov_b32 m0, s33
	s_nop 2
	global_load_lds_dwordx4 v2, s[16:17]
	s_mov_b32 m0, s2
	s_nop 0
	s_mov_b32 s2, m0
	s_mov_b32 m0, s38
	s_nop 2
	global_load_lds_dwordx4 v3, s[16:17]
	s_mov_b32 m0, s2
	s_waitcnt vmcnt(8)
	s_waitcnt lgkmcnt(0)
	s_setprio 1
	s_barrier
	v_mfma_f32_16x16x32_bf16 v[0:3], v[10:13], v[40:43], v[134:137]
	v_mfma_f32_16x16x32_bf16 v[76:79], v[24:27], v[166:169], v[0:3]
	v_mfma_f32_16x16x32_bf16 v[0:3], v[64:67], v[40:43], v[138:141]
	v_mfma_f32_16x16x32_bf16 v[68:71], v[162:165], v[166:169], v[0:3]
	v_mfma_f32_16x16x32_bf16 v[0:3], v[10:13], v[170:173], v[142:145]
	v_mfma_f32_16x16x32_bf16 v[44:47], v[24:27], v[174:177], v[0:3]
	v_mfma_f32_16x16x32_bf16 v[0:3], v[64:67], v[170:173], v[146:149]
	v_mfma_f32_16x16x32_bf16 v[36:39], v[162:165], v[174:177], v[0:3]
	v_mfma_f32_16x16x32_bf16 v[0:3], v[10:13], v[178:181], v[150:153]
	v_mfma_f32_16x16x32_bf16 v[28:31], v[24:27], v[198:201], v[0:3]
	v_mfma_f32_16x16x32_bf16 v[0:3], v[64:67], v[178:181], v[154:157]
	v_mfma_f32_16x16x32_bf16 v[20:23], v[162:165], v[198:201], v[0:3]
	v_mfma_f32_16x16x32_bf16 v[0:3], v[10:13], v[202:205], v[6:9]
	v_mfma_f32_16x16x32_bf16 v[12:15], v[24:27], v[226:229], v[0:3]
	v_mfma_f32_16x16x32_bf16 v[0:3], v[64:67], v[202:205], v[206:209]
	v_mfma_f32_16x16x32_bf16 v[4:7], v[162:165], v[226:229], v[0:3]
	s_setprio 0
	s_setprio 1
	v_mfma_f32_16x16x32_bf16 v[0:3], v[186:189], v[40:43], v[210:213]
	v_mfma_f32_16x16x32_bf16 v[72:75], v[190:193], v[166:169], v[0:3]
	v_mfma_f32_16x16x32_bf16 v[0:3], v[194:197], v[40:43], v[16:19]
	v_mfma_f32_16x16x32_bf16 v[64:67], v[222:225], v[166:169], v[0:3]
	v_mfma_f32_16x16x32_bf16 v[0:3], v[186:189], v[170:173], v[214:217]
	v_mfma_f32_16x16x32_bf16 v[40:43], v[190:193], v[174:177], v[0:3]
	v_mfma_f32_16x16x32_bf16 v[0:3], v[194:197], v[170:173], v[32:35]
	v_mfma_f32_16x16x32_bf16 v[32:35], v[222:225], v[174:177], v[0:3]
	v_mfma_f32_16x16x32_bf16 v[0:3], v[186:189], v[178:181], v[218:221]
	v_mfma_f32_16x16x32_bf16 v[24:27], v[190:193], v[198:201], v[0:3]
	v_mfma_f32_16x16x32_bf16 v[0:3], v[194:197], v[178:181], v[182:185]
	v_mfma_f32_16x16x32_bf16 v[16:19], v[222:225], v[198:201], v[0:3]
	v_mfma_f32_16x16x32_bf16 v[0:3], v[186:189], v[202:205], v[128:131]
	v_mfma_f32_16x16x32_bf16 v[8:11], v[190:193], v[226:229], v[0:3]
	v_mfma_f32_16x16x32_bf16 v[0:3], v[194:197], v[202:205], v[158:161]
	v_mfma_f32_16x16x32_bf16 v[0:3], v[222:225], v[226:229], v[0:3]
	s_setprio 0
	s_barrier
	s_cbranch_scc1 .LBB0_1202
	s_barrier

.LBB0_1341:
	s_add_u32 s70, s0, s28
	s_addc_u32 s71, s1, s29
	s_add_u32 s36, s70, 0x100
	s_addc_u32 s37, s71, 0
	s_add_u32 s34, s8, s28
	s_addc_u32 s35, s9, s29
	s_add_u32 s34, s34, 0x100
	s_addc_u32 s35, s35, 0
	s_add_u32 s40, s10, s28
	v_add_u32_e32 v137, 0x10000, v134
	s_addc_u32 s41, s11, s29
	ds_read_b128 v[138:141], v137
	ds_read_b128 v[142:145], v137 offset:1024
	s_waitcnt vmcnt(0)
	ds_read_b128 v[146:149], v137 offset:2048
	ds_read_b128 v[150:153], v137 offset:3072
	v_add_u32_e32 v137, 0x14000, v134
	s_add_u32 s40, s40, 0x100
	ds_read_b128 v[154:157], v137
	ds_read_b128 v[158:161], v137 offset:1024
	ds_read_b128 v[162:165], v137 offset:2048
	ds_read_b128 v[166:169], v137 offset:3072
	s_addc_u32 s41, s41, 0
	s_cmp_eq_u32 s69, 12
	s_cselect_b32 s44, s66, s34
	s_cselect_b32 s45, s65, s35
	s_cselect_b32 s35, s67, s41
	s_cselect_b32 s34, s68, s40
	s_cselect_b32 s42, s19, s36
	s_cselect_b32 s43, s17, s37
	s_add_u32 s40, s44, 0x80
	s_addc_u32 s41, s45, 0
	s_add_u32 s36, s42, 0x80
	s_addc_u32 s37, s43, 0
	ds_read_b128 v[170:173], v135
	ds_read_b128 v[174:177], v135 offset:1024
	ds_read_b128 v[178:181], v135 offset:2048
	ds_read_b128 v[182:185], v135 offset:3072
	ds_read_b128 v[186:189], v135 offset:4096
	ds_read_b128 v[190:193], v135 offset:5120
	ds_read_b128 v[194:197], v135 offset:6144
	ds_read_b128 v[198:201], v135 offset:7168
	s_add_u32 s70, s70, 0x40080
	s_addc_u32 s71, s71, 0
	s_mov_b32 s72, m0
	s_mov_b32 m0, s62
	s_nop 2
	global_load_lds_dwordx4 v132, s[70:71]
	s_mov_b32 m0, s72
	s_nop 0
	s_mov_b32 s72, m0
	s_mov_b32 m0, s63
	s_nop 2
	global_load_lds_dwordx4 v133, s[70:71]
	s_mov_b32 m0, s72
	s_waitcnt vmcnt(8)
	s_waitcnt lgkmcnt(0)
	s_setprio 1
	s_barrier
	v_mfma_scale_f32_16x16x128_f8f6f4 v[96:99], v[146:153], v[178:185], v[96:99], v136, v136 op_sel_hi:[0,0,0]
	v_mfma_scale_f32_16x16x128_f8f6f4 v[120:123], v[138:145], v[186:193], v[120:123], v136, v136 op_sel_hi:[0,0,0]
	v_mfma_scale_f32_16x16x128_f8f6f4 v[124:127], v[146:153], v[186:193], v[124:127], v136, v136 op_sel_hi:[0,0,0]
	v_mfma_scale_f32_16x16x128_f8f6f4 v[100:103], v[138:145], v[194:201], v[100:103], v136, v136 op_sel_hi:[0,0,0]
	v_mfma_scale_f32_16x16x128_f8f6f4 v[202:205], v[138:145], v[170:177], v[64:67], v136, v136 op_sel_hi:[0,0,0]
	v_mfma_scale_f32_16x16x128_f8f6f4 v[206:209], v[146:153], v[170:177], v[72:75], v136, v136 op_sel_hi:[0,0,0]
	v_mfma_scale_f32_16x16x128_f8f6f4 v[210:213], v[138:145], v[178:185], v[88:91], v136, v136 op_sel_hi:[0,0,0]
	v_mfma_scale_f32_16x16x128_f8f6f4 v[214:217], v[146:153], v[194:201], v[92:95], v136, v136 op_sel_hi:[0,0,0]
	s_setprio 0
	s_setprio 1
	v_mfma_scale_f32_16x16x128_f8f6f4 v[108:111], v[154:161], v[178:185], v[108:111], v136, v136 op_sel_hi:[0,0,0]
	v_mfma_scale_f32_16x16x128_f8f6f4 v[112:115], v[162:169], v[178:185], v[112:115], v136, v136 op_sel_hi:[0,0,0]
	v_mfma_scale_f32_16x16x128_f8f6f4 v[116:119], v[154:161], v[186:193], v[116:119], v136, v136 op_sel_hi:[0,0,0]
	v_mfma_scale_f32_16x16x128_f8f6f4 v[104:107], v[162:169], v[186:193], v[104:107], v136, v136 op_sel_hi:[0,0,0]
	v_mfma_scale_f32_16x16x128_f8f6f4 v[218:221], v[154:161], v[170:177], v[80:83], v136, v136 op_sel_hi:[0,0,0]
	v_mfma_scale_f32_16x16x128_f8f6f4 v[170:173], v[162:169], v[170:177], v[84:87], v136, v136 op_sel_hi:[0,0,0]
	v_mfma_scale_f32_16x16x128_f8f6f4 v[174:177], v[154:161], v[194:201], v[76:79], v136, v136 op_sel_hi:[0,0,0]
	v_mfma_scale_f32_16x16x128_f8f6f4 v[178:181], v[162:169], v[194:201], v[68:71], v136, v136 op_sel_hi:[0,0,0]
	s_setprio 0
	s_barrier
	ds_read_b128 v[64:67], v135 offset:16384
	s_nop 3
	ds_read_b128 v[68:71], v135 offset:17408
	ds_read_b128 v[72:75], v135 offset:18432
	ds_read_b128 v[76:79], v135 offset:19456
	ds_read_b128 v[80:83], v135 offset:20480
	ds_read_b128 v[84:87], v135 offset:21504
	ds_read_b128 v[88:91], v135 offset:22528
	ds_read_b128 v[92:95], v135 offset:23552
	s_mov_b32 s70, m0
	s_mov_b32 m0, s49
	s_nop 2
	global_load_lds_dwordx4 v130, s[44:45]
	s_mov_b32 m0, s70
	s_nop 0
	s_mov_b32 s70, m0
	s_mov_b32 m0, s50
	s_nop 2
	global_load_lds_dwordx4 v131, s[44:45]
	s_mov_b32 m0, s70
	s_mov_b32 s44, m0
	s_mov_b32 m0, s51
	s_nop 2
	global_load_lds_dwordx4 v130, s[34:35]
	s_mov_b32 m0, s44
	s_nop 0
	s_mov_b32 s44, m0
	s_mov_b32 m0, s52
	s_nop 2
	global_load_lds_dwordx4 v131, s[34:35]
	s_mov_b32 m0, s44
	s_nop 0
	s_mov_b32 s44, m0
	s_mov_b32 m0, s47
	s_nop 2
	global_load_lds_dwordx4 v132, s[42:43]
	s_mov_b32 m0, s44
	s_nop 0
	s_mov_b32 s44, m0
	s_mov_b32 m0, s53
	s_nop 2
	global_load_lds_dwordx4 v133, s[42:43]
	s_mov_b32 m0, s44
	s_waitcnt vmcnt(8)
	s_waitcnt lgkmcnt(0)
	s_setprio 1
	s_barrier
	v_mfma_scale_f32_16x16x128_f8f6f4 v[60:63], v[138:145], v[64:71], v[60:63], v136, v136 op_sel_hi:[0,0,0]
	v_mfma_scale_f32_16x16x128_f8f6f4 v[56:59], v[146:153], v[64:71], v[56:59], v136, v136 op_sel_hi:[0,0,0]
	v_mfma_scale_f32_16x16x128_f8f6f4 v[182:185], v[138:145], v[72:79], v[44:47], v136, v136 op_sel_hi:[0,0,0]
	v_mfma_scale_f32_16x16x128_f8f6f4 v[186:189], v[146:153], v[72:79], v[40:43], v136, v136 op_sel_hi:[0,0,0]
	v_mfma_scale_f32_16x16x128_f8f6f4 v[190:193], v[138:145], v[80:87], v[24:27], v136, v136 op_sel_hi:[0,0,0]
	v_mfma_scale_f32_16x16x128_f8f6f4 v[194:197], v[146:153], v[80:87], v[16:19], v136, v136 op_sel_hi:[0,0,0]
	v_mfma_scale_f32_16x16x128_f8f6f4 v[198:201], v[138:145], v[88:95], v[4:7], v136, v136 op_sel_hi:[0,0,0]
	v_mfma_scale_f32_16x16x128_f8f6f4 v[222:225], v[146:153], v[88:95], v[0:3], v136, v136 op_sel_hi:[0,0,0]
	s_setprio 0
	s_setprio 1
	v_mfma_scale_f32_16x16x128_f8f6f4 v[52:55], v[154:161], v[64:71], v[52:55], v136, v136 op_sel_hi:[0,0,0]
	v_mfma_scale_f32_16x16x128_f8f6f4 v[48:51], v[162:169], v[64:71], v[48:51], v136, v136 op_sel_hi:[0,0,0]
	v_mfma_scale_f32_16x16x128_f8f6f4 v[226:229], v[154:161], v[72:79], v[36:39], v136, v136 op_sel_hi:[0,0,0]
	v_mfma_scale_f32_16x16x128_f8f6f4 v[230:233], v[162:169], v[72:79], v[20:23], v136, v136 op_sel_hi:[0,0,0]
	v_mfma_scale_f32_16x16x128_f8f6f4 v[234:237], v[154:161], v[80:87], v[32:35], v136, v136 op_sel_hi:[0,0,0]
	v_mfma_scale_f32_16x16x128_f8f6f4 v[238:241], v[162:169], v[80:87], v[28:31], v136, v136 op_sel_hi:[0,0,0]
	v_mfma_scale_f32_16x16x128_f8f6f4 v[242:245], v[154:161], v[88:95], v[12:15], v136, v136 op_sel_hi:[0,0,0]
	v_mfma_scale_f32_16x16x128_f8f6f4 v[246:249], v[162:169], v[88:95], v[8:11], v136, v136 op_sel_hi:[0,0,0]
	s_setprio 0
	s_barrier
	s_nop 3
	v_add_u32_e32 v12, 0x18000, v134
	v_add_u32_e32 v16, 0x1c000, v134
	ds_read_b128 v[0:3], v12
	ds_read_b128 v[4:7], v12 offset:1024
	ds_read_b128 v[8:11], v12 offset:2048
	ds_read_b128 v[12:15], v12 offset:3072
	ds_read_b128 v[138:141], v16
	ds_read_b128 v[142:145], v16 offset:1024
	ds_read_b128 v[146:149], v16 offset:2048
	ds_read_b128 v[150:153], v16 offset:3072
	ds_read_b128 v[16:19], v135 offset:32768
	ds_read_b128 v[20:23], v135 offset:33792
	ds_read_b128 v[24:27], v135 offset:34816
	ds_read_b128 v[28:31], v135 offset:35840
	ds_read_b128 v[32:35], v135 offset:36864
	ds_read_b128 v[36:39], v135 offset:37888
	ds_read_b128 v[40:43], v135 offset:38912
	ds_read_b128 v[44:47], v135 offset:39936
	s_add_u32 s42, s42, 0x40000
	s_addc_u32 s43, s43, 0
	s_mov_b32 s44, m0
	s_mov_b32 m0, s54
	s_nop 2
	global_load_lds_dwordx4 v132, s[42:43]
	s_mov_b32 m0, s44
	s_nop 0
	s_mov_b32 s44, m0
	s_mov_b32 m0, s55
	s_nop 2
	global_load_lds_dwordx4 v133, s[42:43]
	s_mov_b32 m0, s44
	s_waitcnt vmcnt(8)
	s_waitcnt lgkmcnt(0)
	s_setprio 1
	s_barrier
	v_mfma_scale_f32_16x16x128_f8f6f4 v[64:67], v[0:7], v[16:23], v[202:205], v136, v136 op_sel_hi:[0,0,0]
	v_mfma_scale_f32_16x16x128_f8f6f4 v[72:75], v[8:15], v[16:23], v[206:209], v136, v136 op_sel_hi:[0,0,0]
	v_mfma_scale_f32_16x16x128_f8f6f4 v[88:91], v[0:7], v[24:31], v[210:213], v136, v136 op_sel_hi:[0,0,0]
	v_mfma_scale_f32_16x16x128_f8f6f4 v[96:99], v[8:15], v[24:31], v[96:99], v136, v136 op_sel_hi:[0,0,0]
	v_mfma_scale_f32_16x16x128_f8f6f4 v[120:123], v[0:7], v[32:39], v[120:123], v136, v136 op_sel_hi:[0,0,0]
	v_mfma_scale_f32_16x16x128_f8f6f4 v[124:127], v[8:15], v[32:39], v[124:127], v136, v136 op_sel_hi:[0,0,0]
	v_mfma_scale_f32_16x16x128_f8f6f4 v[100:103], v[0:7], v[40:47], v[100:103], v136, v136 op_sel_hi:[0,0,0]
	v_mfma_scale_f32_16x16x128_f8f6f4 v[92:95], v[8:15], v[40:47], v[214:217], v136, v136 op_sel_hi:[0,0,0]
	s_setprio 0
	s_setprio 1
	v_mfma_scale_f32_16x16x128_f8f6f4 v[80:83], v[138:145], v[16:23], v[218:221], v136, v136 op_sel_hi:[0,0,0]
	v_mfma_scale_f32_16x16x128_f8f6f4 v[84:87], v[146:153], v[16:23], v[170:173], v136, v136 op_sel_hi:[0,0,0]
	v_mfma_scale_f32_16x16x128_f8f6f4 v[108:111], v[138:145], v[24:31], v[108:111], v136, v136 op_sel_hi:[0,0,0]
	v_mfma_scale_f32_16x16x128_f8f6f4 v[112:115], v[146:153], v[24:31], v[112:115], v136, v136 op_sel_hi:[0,0,0]
	v_mfma_scale_f32_16x16x128_f8f6f4 v[116:119], v[138:145], v[32:39], v[116:119], v136, v136 op_sel_hi:[0,0,0]
	v_mfma_scale_f32_16x16x128_f8f6f4 v[104:107], v[146:153], v[32:39], v[104:107], v136, v136 op_sel_hi:[0,0,0]
	v_mfma_scale_f32_16x16x128_f8f6f4 v[76:79], v[138:145], v[40:47], v[174:177], v136, v136 op_sel_hi:[0,0,0]
	v_mfma_scale_f32_16x16x128_f8f6f4 v[68:71], v[146:153], v[40:47], v[178:181], v136, v136 op_sel_hi:[0,0,0]
	s_setprio 0
	s_barrier
	ds_read_b128 v[28:31], v135 offset:49152
	ds_read_b128 v[32:35], v135 offset:50176
	ds_read_b128 v[154:157], v135 offset:51200
	ds_read_b128 v[158:161], v135 offset:52224
	ds_read_b128 v[162:165], v135 offset:53248
	ds_read_b128 v[166:169], v135 offset:54272
	ds_read_b128 v[170:173], v135 offset:55296
	ds_read_b128 v[174:177], v135 offset:56320
	s_mov_b32 s42, m0
	s_mov_b32 m0, s56
	s_nop 2
	global_load_lds_dwordx4 v130, s[40:41]
	s_mov_b32 m0, s42
	s_add_u32 s34, s34, 0x80
	s_mov_b32 s42, m0
	s_mov_b32 m0, s57
	s_nop 2
	global_load_lds_dwordx4 v131, s[40:41]
	s_mov_b32 m0, s42
	s_addc_u32 s35, s35, 0
	s_mov_b32 s40, m0
	s_mov_b32 m0, s60
	s_nop 2
	global_load_lds_dwordx4 v130, s[34:35]
	s_mov_b32 m0, s40
	s_nop 0
	s_mov_b32 s40, m0
	s_mov_b32 m0, s61
	s_nop 2
	global_load_lds_dwordx4 v131, s[34:35]
	s_mov_b32 m0, s40
	s_mov_b32 s34, m0
	s_mov_b32 m0, s58
	s_nop 2
	global_load_lds_dwordx4 v132, s[36:37]
	s_mov_b32 m0, s34
	s_nop 0
	s_mov_b32 s34, m0
	s_mov_b32 m0, s59
	s_nop 2
	global_load_lds_dwordx4 v133, s[36:37]
	s_mov_b32 m0, s34
	s_waitcnt vmcnt(8)
	s_waitcnt lgkmcnt(0)
	s_setprio 1
	s_barrier
	v_mfma_scale_f32_16x16x128_f8f6f4 v[60:63], v[0:7], v[28:35], v[60:63], v136, v136 op_sel_hi:[0,0,0]
	v_mfma_scale_f32_16x16x128_f8f6f4 v[56:59], v[8:15], v[28:35], v[56:59], v136, v136 op_sel_hi:[0,0,0]
	v_mfma_scale_f32_16x16x128_f8f6f4 v[44:47], v[0:7], v[154:161], v[182:185], v136, v136 op_sel_hi:[0,0,0]
	v_mfma_scale_f32_16x16x128_f8f6f4 v[40:43], v[8:15], v[154:161], v[186:189], v136, v136 op_sel_hi:[0,0,0]
	v_mfma_scale_f32_16x16x128_f8f6f4 v[24:27], v[0:7], v[162:169], v[190:193], v136, v136 op_sel_hi:[0,0,0]
	v_mfma_scale_f32_16x16x128_f8f6f4 v[16:19], v[8:15], v[162:169], v[194:197], v136, v136 op_sel_hi:[0,0,0]
	v_mfma_scale_f32_16x16x128_f8f6f4 v[4:7], v[0:7], v[170:177], v[198:201], v136, v136 op_sel_hi:[0,0,0]
	v_mfma_scale_f32_16x16x128_f8f6f4 v[0:3], v[8:15], v[170:177], v[222:225], v136, v136 op_sel_hi:[0,0,0]
	s_setprio 0
	s_setprio 1
	v_mfma_scale_f32_16x16x128_f8f6f4 v[52:55], v[138:145], v[28:35], v[52:55], v136, v136 op_sel_hi:[0,0,0]
	v_mfma_scale_f32_16x16x128_f8f6f4 v[48:51], v[146:153], v[28:35], v[48:51], v136, v136 op_sel_hi:[0,0,0]
	v_mfma_scale_f32_16x16x128_f8f6f4 v[36:39], v[138:145], v[154:161], v[226:229], v136, v136 op_sel_hi:[0,0,0]
	v_mfma_scale_f32_16x16x128_f8f6f4 v[20:23], v[146:153], v[154:161], v[230:233], v136, v136 op_sel_hi:[0,0,0]
	v_mfma_scale_f32_16x16x128_f8f6f4 v[32:35], v[138:145], v[162:169], v[234:237], v136, v136 op_sel_hi:[0,0,0]
	v_mfma_scale_f32_16x16x128_f8f6f4 v[28:31], v[146:153], v[162:169], v[238:241], v136, v136 op_sel_hi:[0,0,0]
	v_mfma_scale_f32_16x16x128_f8f6f4 v[12:15], v[138:145], v[170:177], v[242:245], v136, v136 op_sel_hi:[0,0,0]
	v_mfma_scale_f32_16x16x128_f8f6f4 v[8:11], v[146:153], v[170:177], v[246:249], v136, v136 op_sel_hi:[0,0,0]
	s_setprio 0
	s_barrier
	s_add_i32 s69, s69, 2
	s_add_u32 s28, s28, 0x100
	s_addc_u32 s29, s29, 0
	s_cmp_gt_u32 s69, 13
	s_cbranch_scc0 .LBB0_1341
	s_and_b64 vcc, exec, s[14:15]
	s_cbranch_vccnz .LBB0_1344
	s_andn2_b64 vcc, exec, s[30:31]
	s_cbranch_vccnz .LBB0_1331
	s_branch .LBB0_1345
